# GEMM K-loops: redundant post-barrier lgkmcnt(0) and back-to-back s_setprio 0/1 pairs removed from the MMA segments (3 issue slots per 32-MFMA block); on top of DSA table mask + trims
# baseline (speedup 1.0000x reference)
.LBB0_98:
	s_add_u32 s54, s50, s52
	s_addc_u32 s55, s51, s53
	v_or_b32_e32 v146, 0x10000, v145
	v_add_u32_e32 v150, 0x10400, v145
	v_add_u32_e32 v154, 0x10800, v145
	v_add_u32_e32 v158, 0x10c00, v145
	v_or_b32_e32 v162, 0x14000, v145
	v_add_u32_e32 v166, 0x14400, v145
	v_add_u32_e32 v170, 0x14800, v145
	v_add_u32_e32 v174, 0x14c00, v145
	s_add_u32 s54, s54, 0x100
	ds_read_b128 v[146:149], v146
	ds_read_b128 v[150:153], v150
	ds_read_b128 v[154:157], v154
	ds_read_b128 v[158:161], v158
	ds_read_b128 v[162:165], v162
	ds_read_b128 v[166:169], v166
	ds_read_b128 v[170:173], v170
	ds_read_b128 v[174:177], v174
	s_addc_u32 s55, s55, 0
	s_add_u32 vcc_lo, s95, s52
	s_addc_u32 vcc_hi, s46, s53
	s_cmpk_eq_i32 s52, 0x1500
	s_cselect_b32 s57, s43, s55
	s_cselect_b32 s56, s42, s54
	s_cselect_b32 s55, s49, vcc_hi
	s_cselect_b32 s54, s48, vcc_lo
	s_mov_b32 m0, s89
	v_lshl_add_u64 v[194:195], v[140:141], 0, s[52:53]
	ds_read_b128 v[178:181], v144
	ds_read_b128 v[182:185], v144 offset:1024
	ds_read_b128 v[186:189], v144 offset:2048
	ds_read_b128 v[190:193], v144 offset:3072
	ds_read_b128 v[200:203], v144 offset:4096
	ds_read_b128 v[204:207], v144 offset:5120
	ds_read_b128 v[208:211], v144 offset:6144
	ds_read_b128 v[212:215], v144 offset:7168
	global_load_lds_dwordx4 v[194:195], off
	v_lshl_add_u64 v[194:195], v[142:143], 0, s[52:53]
	s_mov_b32 m0, s90
	s_nop 0
	global_load_lds_dwordx4 v[194:195], off
	s_waitcnt vmcnt(8)
	s_waitcnt lgkmcnt(0)
	s_barrier
	s_setprio 1
	v_mfma_f32_16x16x32_bf16 v[126:129], v[146:149], v[178:181], v[126:129]
	v_mfma_f32_16x16x32_bf16 v[122:125], v[154:157], v[178:181], v[122:125]
	v_mfma_f32_16x16x32_bf16 v[110:113], v[146:149], v[186:189], v[110:113]
	v_mfma_f32_16x16x32_bf16 v[106:109], v[154:157], v[186:189], v[106:109]
	v_mfma_f32_16x16x32_bf16 v[94:97], v[146:149], v[200:203], v[94:97]
	v_mfma_f32_16x16x32_bf16 v[90:93], v[154:157], v[200:203], v[90:93]
	v_mfma_f32_16x16x32_bf16 v[78:81], v[146:149], v[208:211], v[78:81]
	v_mfma_f32_16x16x32_bf16 v[74:77], v[154:157], v[208:211], v[74:77]
	v_mfma_f32_16x16x32_bf16 v[126:129], v[150:153], v[182:185], v[126:129]
	v_mfma_f32_16x16x32_bf16 v[122:125], v[158:161], v[182:185], v[122:125]
	v_mfma_f32_16x16x32_bf16 v[110:113], v[150:153], v[190:193], v[110:113]
	v_mfma_f32_16x16x32_bf16 v[106:109], v[158:161], v[190:193], v[106:109]
	v_mfma_f32_16x16x32_bf16 v[94:97], v[150:153], v[204:207], v[94:97]
	v_mfma_f32_16x16x32_bf16 v[90:93], v[158:161], v[204:207], v[90:93]
	v_mfma_f32_16x16x32_bf16 v[78:81], v[150:153], v[212:215], v[78:81]
	v_mfma_f32_16x16x32_bf16 v[74:77], v[158:161], v[212:215], v[74:77]
	v_mfma_f32_16x16x32_bf16 v[118:121], v[162:165], v[178:181], v[118:121]
	v_mfma_f32_16x16x32_bf16 v[114:117], v[170:173], v[178:181], v[114:117]
	v_mfma_f32_16x16x32_bf16 v[102:105], v[162:165], v[186:189], v[102:105]
	v_mfma_f32_16x16x32_bf16 v[98:101], v[170:173], v[186:189], v[98:101]
	v_mfma_f32_16x16x32_bf16 v[86:89], v[162:165], v[200:203], v[86:89]
	v_mfma_f32_16x16x32_bf16 v[82:85], v[170:173], v[200:203], v[82:85]
	v_mfma_f32_16x16x32_bf16 v[70:73], v[162:165], v[208:211], v[70:73]
	v_mfma_f32_16x16x32_bf16 v[66:69], v[170:173], v[208:211], v[66:69]
	v_mfma_f32_16x16x32_bf16 v[118:121], v[166:169], v[182:185], v[118:121]
	v_mfma_f32_16x16x32_bf16 v[114:117], v[174:177], v[182:185], v[114:117]
	v_mfma_f32_16x16x32_bf16 v[102:105], v[166:169], v[190:193], v[102:105]
	v_mfma_f32_16x16x32_bf16 v[98:101], v[174:177], v[190:193], v[98:101]
	v_mfma_f32_16x16x32_bf16 v[86:89], v[166:169], v[204:207], v[86:89]
	v_mfma_f32_16x16x32_bf16 v[82:85], v[174:177], v[204:207], v[82:85]
	v_mfma_f32_16x16x32_bf16 v[70:73], v[166:169], v[212:215], v[70:73]
	v_mfma_f32_16x16x32_bf16 v[66:69], v[174:177], v[212:215], v[66:69]
	s_setprio 0
	s_barrier
	s_mov_b32 m0, s58
	v_lshl_add_u64 v[194:195], s[54:55], 0, v[0:1]
	s_add_u32 vcc_lo, s54, 0xb0000
	ds_read_b128 v[178:181], v144 offset:16384
	ds_read_b128 v[182:185], v144 offset:17408
	ds_read_b128 v[186:189], v144 offset:18432
	ds_read_b128 v[190:193], v144 offset:19456
	ds_read_b128 v[200:203], v144 offset:20480
	ds_read_b128 v[204:207], v144 offset:21504
	ds_read_b128 v[208:211], v144 offset:22528
	ds_read_b128 v[212:215], v144 offset:23552
	global_load_lds_dwordx4 v[194:195], off
	v_lshl_add_u64 v[216:217], s[54:55], 0, v[130:131]
	s_mov_b32 m0, s59
	s_addc_u32 vcc_hi, s55, 0
	global_load_lds_dwordx4 v[216:217], off
	v_lshl_add_u64 v[218:219], vcc, 0, v[0:1]
	s_mov_b32 m0, s60
	v_lshl_add_u64 v[220:221], s[56:57], 0, v[132:133]
	global_load_lds_dwordx4 v[218:219], off
	v_lshl_add_u64 v[218:219], vcc, 0, v[130:131]
	s_mov_b32 m0, s61
	s_nop 0
	global_load_lds_dwordx4 v[218:219], off
	v_lshl_add_u64 v[218:219], s[56:57], 0, v[134:135]
	s_mov_b32 m0, s39
	s_nop 0
	global_load_lds_dwordx4 v[218:219], off
	s_mov_b32 m0, s64
	s_nop 0
	global_load_lds_dwordx4 v[220:221], off
	s_waitcnt vmcnt(8)
	s_waitcnt lgkmcnt(0)
	s_barrier
	s_setprio 1
	v_mfma_f32_16x16x32_bf16 v[62:65], v[146:149], v[178:181], v[62:65]
	v_mfma_f32_16x16x32_bf16 v[58:61], v[154:157], v[178:181], v[58:61]
	v_mfma_f32_16x16x32_bf16 v[46:49], v[146:149], v[186:189], v[46:49]
	v_mfma_f32_16x16x32_bf16 v[42:45], v[154:157], v[186:189], v[42:45]
	v_mfma_f32_16x16x32_bf16 v[30:33], v[146:149], v[200:203], v[30:33]
	v_mfma_f32_16x16x32_bf16 v[26:29], v[154:157], v[200:203], v[26:29]
	v_mfma_f32_16x16x32_bf16 v[14:17], v[146:149], v[208:211], v[14:17]
	v_mfma_f32_16x16x32_bf16 v[10:13], v[154:157], v[208:211], v[10:13]
	v_mfma_f32_16x16x32_bf16 v[62:65], v[150:153], v[182:185], v[62:65]
	v_mfma_f32_16x16x32_bf16 v[58:61], v[158:161], v[182:185], v[58:61]
	v_mfma_f32_16x16x32_bf16 v[46:49], v[150:153], v[190:193], v[46:49]
	v_mfma_f32_16x16x32_bf16 v[42:45], v[158:161], v[190:193], v[42:45]
	v_mfma_f32_16x16x32_bf16 v[30:33], v[150:153], v[204:207], v[30:33]
	v_mfma_f32_16x16x32_bf16 v[26:29], v[158:161], v[204:207], v[26:29]
	v_mfma_f32_16x16x32_bf16 v[14:17], v[150:153], v[212:215], v[14:17]
	v_mfma_f32_16x16x32_bf16 v[10:13], v[158:161], v[212:215], v[10:13]
	v_mfma_f32_16x16x32_bf16 v[54:57], v[162:165], v[178:181], v[54:57]
	v_mfma_f32_16x16x32_bf16 v[50:53], v[170:173], v[178:181], v[50:53]
	v_mfma_f32_16x16x32_bf16 v[38:41], v[162:165], v[186:189], v[38:41]
	v_mfma_f32_16x16x32_bf16 v[34:37], v[170:173], v[186:189], v[34:37]
	v_mfma_f32_16x16x32_bf16 v[22:25], v[162:165], v[200:203], v[22:25]
	v_mfma_f32_16x16x32_bf16 v[18:21], v[170:173], v[200:203], v[18:21]
	v_mfma_f32_16x16x32_bf16 v[6:9], v[162:165], v[208:211], v[6:9]
	v_mfma_f32_16x16x32_bf16 v[2:5], v[170:173], v[208:211], v[2:5]
	v_mfma_f32_16x16x32_bf16 v[54:57], v[166:169], v[182:185], v[54:57]
	v_mfma_f32_16x16x32_bf16 v[50:53], v[174:177], v[182:185], v[50:53]
	v_mfma_f32_16x16x32_bf16 v[38:41], v[166:169], v[190:193], v[38:41]
	v_mfma_f32_16x16x32_bf16 v[34:37], v[174:177], v[190:193], v[34:37]
	v_mfma_f32_16x16x32_bf16 v[22:25], v[166:169], v[204:207], v[22:25]
	v_mfma_f32_16x16x32_bf16 v[18:21], v[174:177], v[204:207], v[18:21]
	v_mfma_f32_16x16x32_bf16 v[6:9], v[166:169], v[212:215], v[6:9]
	v_mfma_f32_16x16x32_bf16 v[2:5], v[174:177], v[212:215], v[2:5]
	s_setprio 0
	s_barrier
	v_or_b32_e32 v146, 0x18000, v145
	v_add_u32_e32 v150, 0x18400, v145
	v_add_u32_e32 v154, 0x18800, v145
	v_add_u32_e32 v158, 0x18c00, v145
	v_or_b32_e32 v162, 0x1c000, v145
	v_add_u32_e32 v166, 0x1c400, v145
	v_add_u32_e32 v170, 0x1c800, v145
	v_add_u32_e32 v174, 0x1cc00, v145
	ds_read_b128 v[146:149], v146
	ds_read_b128 v[150:153], v150
	ds_read_b128 v[154:157], v154
	ds_read_b128 v[158:161], v158
	ds_read_b128 v[162:165], v162
	ds_read_b128 v[166:169], v166
	ds_read_b128 v[170:173], v170
	ds_read_b128 v[174:177], v174
	s_add_u32 s56, s56, 0xb0000
	s_addc_u32 s57, s57, 0
	s_mov_b32 m0, s65
	v_lshl_add_u64 v[222:223], s[56:57], 0, v[134:135]
	ds_read_b128 v[178:181], v144 offset:32768
	ds_read_b128 v[182:185], v144 offset:33792
	ds_read_b128 v[186:189], v144 offset:34816
	ds_read_b128 v[190:193], v144 offset:35840
	ds_read_b128 v[200:203], v144 offset:36864
	ds_read_b128 v[204:207], v144 offset:37888
	ds_read_b128 v[208:211], v144 offset:38912
	ds_read_b128 v[212:215], v144 offset:39936
	global_load_lds_dwordx4 v[222:223], off
	v_lshl_add_u64 v[222:223], s[56:57], 0, v[132:133]
	s_mov_b32 m0, s66
	s_nop 0
	global_load_lds_dwordx4 v[222:223], off
	s_waitcnt vmcnt(8)
	s_waitcnt lgkmcnt(0)
	s_barrier
	s_setprio 1
	v_mfma_f32_16x16x32_bf16 v[126:129], v[146:149], v[178:181], v[126:129]
	v_mfma_f32_16x16x32_bf16 v[122:125], v[154:157], v[178:181], v[122:125]
	v_mfma_f32_16x16x32_bf16 v[110:113], v[146:149], v[186:189], v[110:113]
	v_mfma_f32_16x16x32_bf16 v[106:109], v[154:157], v[186:189], v[106:109]
	v_mfma_f32_16x16x32_bf16 v[94:97], v[146:149], v[200:203], v[94:97]
	v_mfma_f32_16x16x32_bf16 v[90:93], v[154:157], v[200:203], v[90:93]
	v_mfma_f32_16x16x32_bf16 v[78:81], v[146:149], v[208:211], v[78:81]
	v_mfma_f32_16x16x32_bf16 v[74:77], v[154:157], v[208:211], v[74:77]
	v_mfma_f32_16x16x32_bf16 v[126:129], v[150:153], v[182:185], v[126:129]
	v_mfma_f32_16x16x32_bf16 v[122:125], v[158:161], v[182:185], v[122:125]
	v_mfma_f32_16x16x32_bf16 v[110:113], v[150:153], v[190:193], v[110:113]
	v_mfma_f32_16x16x32_bf16 v[106:109], v[158:161], v[190:193], v[106:109]
	v_mfma_f32_16x16x32_bf16 v[94:97], v[150:153], v[204:207], v[94:97]
	v_mfma_f32_16x16x32_bf16 v[90:93], v[158:161], v[204:207], v[90:93]
	v_mfma_f32_16x16x32_bf16 v[78:81], v[150:153], v[212:215], v[78:81]
	v_mfma_f32_16x16x32_bf16 v[74:77], v[158:161], v[212:215], v[74:77]
	v_mfma_f32_16x16x32_bf16 v[118:121], v[162:165], v[178:181], v[118:121]
	v_mfma_f32_16x16x32_bf16 v[114:117], v[170:173], v[178:181], v[114:117]
	v_mfma_f32_16x16x32_bf16 v[102:105], v[162:165], v[186:189], v[102:105]
	v_mfma_f32_16x16x32_bf16 v[98:101], v[170:173], v[186:189], v[98:101]
	v_mfma_f32_16x16x32_bf16 v[86:89], v[162:165], v[200:203], v[86:89]
	v_mfma_f32_16x16x32_bf16 v[82:85], v[170:173], v[200:203], v[82:85]
	v_mfma_f32_16x16x32_bf16 v[70:73], v[162:165], v[208:211], v[70:73]
	v_mfma_f32_16x16x32_bf16 v[66:69], v[170:173], v[208:211], v[66:69]
	v_mfma_f32_16x16x32_bf16 v[118:121], v[166:169], v[182:185], v[118:121]
	v_mfma_f32_16x16x32_bf16 v[114:117], v[174:177], v[182:185], v[114:117]
	v_mfma_f32_16x16x32_bf16 v[102:105], v[166:169], v[190:193], v[102:105]
	v_mfma_f32_16x16x32_bf16 v[98:101], v[174:177], v[190:193], v[98:101]
	v_mfma_f32_16x16x32_bf16 v[86:89], v[166:169], v[204:207], v[86:89]
	v_mfma_f32_16x16x32_bf16 v[82:85], v[174:177], v[204:207], v[82:85]
	v_mfma_f32_16x16x32_bf16 v[70:73], v[166:169], v[212:215], v[70:73]
	v_mfma_f32_16x16x32_bf16 v[66:69], v[174:177], v[212:215], v[66:69]
	s_setprio 0
	s_barrier
	s_mov_b32 m0, s67
	v_lshl_add_u64 v[194:195], v[194:195], 0, s[18:19]
	s_add_u32 s54, s54, 0xb0080
	ds_read_b128 v[178:181], v144 offset:49152
	ds_read_b128 v[182:185], v144 offset:50176
	ds_read_b128 v[186:189], v144 offset:51200
	ds_read_b128 v[190:193], v144 offset:52224
	ds_read_b128 v[200:203], v144 offset:53248
	ds_read_b128 v[204:207], v144 offset:54272
	ds_read_b128 v[208:211], v144 offset:55296
	ds_read_b128 v[212:215], v144 offset:56320
	global_load_lds_dwordx4 v[194:195], off
	v_lshl_add_u64 v[194:195], v[216:217], 0, s[18:19]
	s_mov_b32 m0, s80
	s_addc_u32 s55, s55, 0
	global_load_lds_dwordx4 v[194:195], off
	v_lshl_add_u64 v[194:195], s[54:55], 0, v[0:1]
	s_mov_b32 m0, s84
	s_nop 0
	global_load_lds_dwordx4 v[194:195], off
	v_lshl_add_u64 v[194:195], s[54:55], 0, v[130:131]
	s_mov_b32 m0, s85
	s_nop 0
	global_load_lds_dwordx4 v[194:195], off
	v_lshl_add_u64 v[194:195], v[218:219], 0, s[18:19]
	s_mov_b32 m0, s82
	s_nop 0
	global_load_lds_dwordx4 v[194:195], off
	v_lshl_add_u64 v[194:195], v[220:221], 0, s[18:19]
	s_mov_b32 m0, s83
	s_nop 0
	global_load_lds_dwordx4 v[194:195], off
	s_waitcnt vmcnt(8)
	s_waitcnt lgkmcnt(0)
	s_barrier
	s_setprio 1
	v_mfma_f32_16x16x32_bf16 v[62:65], v[146:149], v[178:181], v[62:65]
	v_mfma_f32_16x16x32_bf16 v[58:61], v[154:157], v[178:181], v[58:61]
	v_mfma_f32_16x16x32_bf16 v[46:49], v[146:149], v[186:189], v[46:49]
	v_mfma_f32_16x16x32_bf16 v[42:45], v[154:157], v[186:189], v[42:45]
	v_mfma_f32_16x16x32_bf16 v[30:33], v[146:149], v[200:203], v[30:33]
	v_mfma_f32_16x16x32_bf16 v[26:29], v[154:157], v[200:203], v[26:29]
	v_mfma_f32_16x16x32_bf16 v[14:17], v[146:149], v[208:211], v[14:17]
	v_mfma_f32_16x16x32_bf16 v[10:13], v[154:157], v[208:211], v[10:13]
	v_mfma_f32_16x16x32_bf16 v[62:65], v[150:153], v[182:185], v[62:65]
	v_mfma_f32_16x16x32_bf16 v[58:61], v[158:161], v[182:185], v[58:61]
	v_mfma_f32_16x16x32_bf16 v[46:49], v[150:153], v[190:193], v[46:49]
	v_mfma_f32_16x16x32_bf16 v[42:45], v[158:161], v[190:193], v[42:45]
	v_mfma_f32_16x16x32_bf16 v[30:33], v[150:153], v[204:207], v[30:33]
	v_mfma_f32_16x16x32_bf16 v[26:29], v[158:161], v[204:207], v[26:29]
	v_mfma_f32_16x16x32_bf16 v[14:17], v[150:153], v[212:215], v[14:17]
	v_mfma_f32_16x16x32_bf16 v[10:13], v[158:161], v[212:215], v[10:13]
	v_mfma_f32_16x16x32_bf16 v[54:57], v[162:165], v[178:181], v[54:57]
	v_mfma_f32_16x16x32_bf16 v[50:53], v[170:173], v[178:181], v[50:53]
	v_mfma_f32_16x16x32_bf16 v[38:41], v[162:165], v[186:189], v[38:41]
	v_mfma_f32_16x16x32_bf16 v[34:37], v[170:173], v[186:189], v[34:37]
	v_mfma_f32_16x16x32_bf16 v[22:25], v[162:165], v[200:203], v[22:25]
	v_mfma_f32_16x16x32_bf16 v[18:21], v[170:173], v[200:203], v[18:21]
	v_mfma_f32_16x16x32_bf16 v[6:9], v[162:165], v[208:211], v[6:9]
	v_mfma_f32_16x16x32_bf16 v[2:5], v[170:173], v[208:211], v[2:5]
	v_mfma_f32_16x16x32_bf16 v[54:57], v[166:169], v[182:185], v[54:57]
	v_mfma_f32_16x16x32_bf16 v[50:53], v[174:177], v[182:185], v[50:53]
	v_mfma_f32_16x16x32_bf16 v[38:41], v[166:169], v[190:193], v[38:41]
	v_mfma_f32_16x16x32_bf16 v[34:37], v[174:177], v[190:193], v[34:37]
	v_mfma_f32_16x16x32_bf16 v[22:25], v[166:169], v[204:207], v[22:25]
	v_mfma_f32_16x16x32_bf16 v[18:21], v[174:177], v[204:207], v[18:21]
	v_mfma_f32_16x16x32_bf16 v[6:9], v[166:169], v[212:215], v[6:9]
	v_mfma_f32_16x16x32_bf16 v[2:5], v[174:177], v[212:215], v[2:5]
	s_setprio 0
	s_barrier
	s_add_i32 s47, s47, 2
	s_add_u32 s52, s52, 0x100
	s_addc_u32 s53, s53, 0
	s_cmp_gt_u32 s47, 41
	s_cbranch_scc0 .LBB0_98
	s_and_b64 vcc, exec, s[16:17]
	s_cbranch_vccz .LBB0_101
	s_barrier

.LBB0_357:
	v_or_b32_e32 v0, 0x10000, v220
	v_add_u32_e32 v50, 0x10400, v220
	ds_read_b128 v[46:49], v0
	ds_read_b128 v[50:53], v50
	v_add_u32_e32 v0, 0x10800, v220
	v_add_u32_e32 v62, 0x10c00, v220
	ds_read_b128 v[58:61], v0
	ds_read_b128 v[62:65], v62
	v_or_b32_e32 v0, 0x14000, v220
	v_add_u32_e32 v78, 0x14400, v220
	ds_read_b128 v[74:77], v0
	ds_read_b128 v[78:81], v78
	v_add_u32_e32 v0, 0x14800, v220
	v_add_u32_e32 v86, 0x14c00, v220
	ds_read_b128 v[82:85], v0
	ds_read_b128 v[86:89], v86
	s_add_u32 s50, s40, 0xfffc0080
	s_addc_u32 s51, s41, -1
	s_cmp_eq_u32 vcc_hi, 12
	s_cselect_b32 s83, s29, s51
	s_cselect_b32 s82, s37, s50
	s_cselect_b32 s67, s39, vcc_lo
	s_cselect_b32 s66, s57, s59
	v_lshl_add_u64 v[182:183], s[40:41], 0, v[170:171]
	s_add_i32 m0, s88, 0xc000
	ds_read_b128 v[192:195], v219
	ds_read_b128 v[200:203], v219 offset:1024
	ds_read_b128 v[204:207], v219 offset:2048
	ds_read_b128 v[208:211], v219 offset:3072
	ds_read_b128 v[212:215], v219 offset:4096
	ds_read_b128 v[236:239], v219 offset:5120
	ds_read_b128 v[240:243], v219 offset:6144
	ds_read_b128 v[244:247], v219 offset:7168
	global_load_lds_dwordx4 v[182:183], off
	v_lshl_add_u64 v[182:183], s[40:41], 0, v[172:173]
	s_add_i32 m0, s88, 0xe000
	s_nop 0
	global_load_lds_dwordx4 v[182:183], off
	s_waitcnt vmcnt(8)
	s_waitcnt lgkmcnt(0)
	s_barrier
	s_setprio 1
	v_mfma_f32_16x16x32_bf16 v[158:161], v[46:49], v[192:195], v[158:161]
	v_mfma_f32_16x16x32_bf16 v[154:157], v[58:61], v[192:195], v[154:157]
	v_mfma_f32_16x16x32_bf16 v[142:145], v[46:49], v[204:207], v[142:145]
	v_mfma_f32_16x16x32_bf16 v[138:141], v[58:61], v[204:207], v[138:141]
	v_mfma_f32_16x16x32_bf16 v[126:129], v[46:49], v[212:215], v[126:129]
	v_mfma_f32_16x16x32_bf16 v[122:125], v[58:61], v[212:215], v[122:125]
	v_mfma_f32_16x16x32_bf16 v[110:113], v[46:49], v[240:243], v[110:113]
	v_mfma_f32_16x16x32_bf16 v[106:109], v[58:61], v[240:243], v[106:109]
	v_mfma_f32_16x16x32_bf16 v[158:161], v[50:53], v[200:203], v[158:161]
	v_mfma_f32_16x16x32_bf16 v[154:157], v[62:65], v[200:203], v[154:157]
	v_mfma_f32_16x16x32_bf16 v[142:145], v[50:53], v[208:211], v[142:145]
	v_mfma_f32_16x16x32_bf16 v[138:141], v[62:65], v[208:211], v[138:141]
	v_mfma_f32_16x16x32_bf16 v[126:129], v[50:53], v[236:239], v[126:129]
	v_mfma_f32_16x16x32_bf16 v[122:125], v[62:65], v[236:239], v[122:125]
	v_mfma_f32_16x16x32_bf16 v[110:113], v[50:53], v[244:247], v[110:113]
	v_mfma_f32_16x16x32_bf16 v[106:109], v[62:65], v[244:247], v[106:109]
	v_mfma_f32_16x16x32_bf16 v[150:153], v[74:77], v[192:195], v[150:153]
	v_mfma_f32_16x16x32_bf16 v[146:149], v[82:85], v[192:195], v[146:149]
	v_mfma_f32_16x16x32_bf16 v[134:137], v[74:77], v[204:207], v[134:137]
	v_mfma_f32_16x16x32_bf16 v[130:133], v[82:85], v[204:207], v[130:133]
	v_mfma_f32_16x16x32_bf16 v[118:121], v[74:77], v[212:215], v[118:121]
	v_mfma_f32_16x16x32_bf16 v[114:117], v[82:85], v[212:215], v[114:117]
	v_mfma_f32_16x16x32_bf16 v[102:105], v[74:77], v[240:243], v[102:105]
	v_mfma_f32_16x16x32_bf16 v[98:101], v[82:85], v[240:243], v[98:101]
	v_mfma_f32_16x16x32_bf16 v[150:153], v[78:81], v[200:203], v[150:153]
	v_mfma_f32_16x16x32_bf16 v[146:149], v[86:89], v[200:203], v[146:149]
	v_mfma_f32_16x16x32_bf16 v[134:137], v[78:81], v[208:211], v[134:137]
	v_mfma_f32_16x16x32_bf16 v[130:133], v[86:89], v[208:211], v[130:133]
	v_mfma_f32_16x16x32_bf16 v[118:121], v[78:81], v[236:239], v[118:121]
	v_mfma_f32_16x16x32_bf16 v[114:117], v[86:89], v[236:239], v[114:117]
	v_mfma_f32_16x16x32_bf16 v[102:105], v[78:81], v[244:247], v[102:105]
	v_mfma_f32_16x16x32_bf16 v[98:101], v[86:89], v[244:247], v[98:101]
	s_setprio 0
	s_barrier
	s_mov_b32 m0, s90
	v_lshl_add_u64 v[182:183], s[66:67], 0, v[166:167]
	s_add_u32 s50, s66, 0x40000
	ds_read_b128 v[192:195], v219 offset:16384
	ds_read_b128 v[200:203], v219 offset:17408
	ds_read_b128 v[204:207], v219 offset:18432
	ds_read_b128 v[208:211], v219 offset:19456
	ds_read_b128 v[212:215], v219 offset:20480
	ds_read_b128 v[236:239], v219 offset:21504
	ds_read_b128 v[240:243], v219 offset:22528
	ds_read_b128 v[244:247], v219 offset:23552
	global_load_lds_dwordx4 v[182:183], off
	v_lshl_add_u64 v[216:217], s[66:67], 0, v[162:163]
	s_mov_b32 m0, s91
	s_addc_u32 s51, s67, 0
	global_load_lds_dwordx4 v[216:217], off
	v_lshl_add_u64 v[222:223], s[50:51], 0, v[166:167]
	s_mov_b32 m0, s92
	v_lshl_add_u64 v[226:227], s[82:83], 0, v[164:165]
	global_load_lds_dwordx4 v[222:223], off
	v_lshl_add_u64 v[222:223], s[50:51], 0, v[162:163]
	s_mov_b32 m0, s93
	s_nop 0
	global_load_lds_dwordx4 v[222:223], off
	v_lshl_add_u64 v[222:223], s[82:83], 0, v[168:169]
	s_mov_b32 m0, s88
	s_nop 0
	global_load_lds_dwordx4 v[222:223], off
	s_mov_b32 m0, s94
	s_nop 0
	global_load_lds_dwordx4 v[226:227], off
	s_waitcnt vmcnt(8)
	s_waitcnt lgkmcnt(0)
	s_barrier
	s_setprio 1
	v_mfma_f32_16x16x32_bf16 v[94:97], v[46:49], v[192:195], v[94:97]
	v_mfma_f32_16x16x32_bf16 v[90:93], v[58:61], v[192:195], v[90:93]
	v_mfma_f32_16x16x32_bf16 v[54:57], v[46:49], v[204:207], v[54:57]
	v_mfma_f32_16x16x32_bf16 v[42:45], v[58:61], v[204:207], v[42:45]
	v_mfma_f32_16x16x32_bf16 v[30:33], v[46:49], v[212:215], v[30:33]
	v_mfma_f32_16x16x32_bf16 v[26:29], v[58:61], v[212:215], v[26:29]
	v_mfma_f32_16x16x32_bf16 v[14:17], v[46:49], v[240:243], v[14:17]
	v_mfma_f32_16x16x32_bf16 v[10:13], v[58:61], v[240:243], v[10:13]
	v_mfma_f32_16x16x32_bf16 v[94:97], v[50:53], v[200:203], v[94:97]
	v_mfma_f32_16x16x32_bf16 v[90:93], v[62:65], v[200:203], v[90:93]
	v_mfma_f32_16x16x32_bf16 v[54:57], v[50:53], v[208:211], v[54:57]
	v_mfma_f32_16x16x32_bf16 v[42:45], v[62:65], v[208:211], v[42:45]
	v_mfma_f32_16x16x32_bf16 v[30:33], v[50:53], v[236:239], v[30:33]
	v_mfma_f32_16x16x32_bf16 v[26:29], v[62:65], v[236:239], v[26:29]
	v_mfma_f32_16x16x32_bf16 v[14:17], v[50:53], v[244:247], v[14:17]
	v_mfma_f32_16x16x32_bf16 v[10:13], v[62:65], v[244:247], v[10:13]
	v_mfma_f32_16x16x32_bf16 v[38:41], v[74:77], v[204:207], v[38:41]
	v_mfma_f32_16x16x32_bf16 v[34:37], v[82:85], v[204:207], v[34:37]
	v_mfma_f32_16x16x32_bf16 v[22:25], v[74:77], v[212:215], v[22:25]
	v_mfma_f32_16x16x32_bf16 v[18:21], v[82:85], v[212:215], v[18:21]
	v_mfma_f32_16x16x32_bf16 v[6:9], v[74:77], v[240:243], v[6:9]
	v_mfma_f32_16x16x32_bf16 v[2:5], v[82:85], v[240:243], v[2:5]
	v_mfma_f32_16x16x32_bf16 v[46:49], v[74:77], v[192:195], v[70:73]
	v_mfma_f32_16x16x32_bf16 v[50:53], v[82:85], v[192:195], v[66:69]
	v_mfma_f32_16x16x32_bf16 v[38:41], v[78:81], v[208:211], v[38:41]
	v_mfma_f32_16x16x32_bf16 v[34:37], v[86:89], v[208:211], v[34:37]
	v_mfma_f32_16x16x32_bf16 v[22:25], v[78:81], v[236:239], v[22:25]
	v_mfma_f32_16x16x32_bf16 v[18:21], v[86:89], v[236:239], v[18:21]
	v_mfma_f32_16x16x32_bf16 v[6:9], v[78:81], v[244:247], v[6:9]
	v_mfma_f32_16x16x32_bf16 v[2:5], v[86:89], v[244:247], v[2:5]
	v_mfma_f32_16x16x32_bf16 v[46:49], v[78:81], v[200:203], v[46:49]
	v_mfma_f32_16x16x32_bf16 v[50:53], v[86:89], v[200:203], v[50:53]
	s_setprio 0
	s_barrier
	v_or_b32_e32 v0, 0x18000, v220
	v_add_u32_e32 v62, 0x18400, v220
	ds_read_b128 v[58:61], v0
	ds_read_b128 v[62:65], v62
	v_add_u32_e32 v0, 0x18800, v220
	v_add_u32_e32 v70, 0x18c00, v220
	ds_read_b128 v[66:69], v0
	ds_read_b128 v[70:73], v70
	v_or_b32_e32 v0, 0x1c000, v220
	v_add_u32_e32 v78, 0x1c400, v220
	ds_read_b128 v[74:77], v0
	ds_read_b128 v[78:81], v78
	v_add_u32_e32 v0, 0x1c800, v220
	v_add_u32_e32 v86, 0x1cc00, v220
	ds_read_b128 v[82:85], v0
	ds_read_b128 v[86:89], v86
	s_add_u32 s50, s82, 0x40000
	s_addc_u32 s51, s83, 0
	s_mov_b32 m0, s95
	v_lshl_add_u64 v[228:229], s[50:51], 0, v[168:169]
	ds_read_b128 v[192:195], v219 offset:32768
	ds_read_b128 v[200:203], v219 offset:33792
	ds_read_b128 v[204:207], v219 offset:34816
	ds_read_b128 v[208:211], v219 offset:35840
	ds_read_b128 v[212:215], v219 offset:36864
	ds_read_b128 v[236:239], v219 offset:37888
	ds_read_b128 v[240:243], v219 offset:38912
	ds_read_b128 v[244:247], v219 offset:39936
	global_load_lds_dwordx4 v[228:229], off
	v_lshl_add_u64 v[228:229], s[50:51], 0, v[164:165]
	s_mov_b32 m0, s0
	s_nop 0
	global_load_lds_dwordx4 v[228:229], off
	s_waitcnt vmcnt(8)
	s_waitcnt lgkmcnt(0)
	s_barrier
	s_setprio 1
	v_mfma_f32_16x16x32_bf16 v[158:161], v[58:61], v[192:195], v[158:161]
	v_mfma_f32_16x16x32_bf16 v[154:157], v[66:69], v[192:195], v[154:157]
	v_mfma_f32_16x16x32_bf16 v[142:145], v[58:61], v[204:207], v[142:145]
	v_mfma_f32_16x16x32_bf16 v[138:141], v[66:69], v[204:207], v[138:141]
	v_mfma_f32_16x16x32_bf16 v[126:129], v[58:61], v[212:215], v[126:129]
	v_mfma_f32_16x16x32_bf16 v[122:125], v[66:69], v[212:215], v[122:125]
	v_mfma_f32_16x16x32_bf16 v[110:113], v[58:61], v[240:243], v[110:113]
	v_mfma_f32_16x16x32_bf16 v[106:109], v[66:69], v[240:243], v[106:109]
	v_mfma_f32_16x16x32_bf16 v[158:161], v[62:65], v[200:203], v[158:161]
	v_mfma_f32_16x16x32_bf16 v[154:157], v[70:73], v[200:203], v[154:157]
	v_mfma_f32_16x16x32_bf16 v[142:145], v[62:65], v[208:211], v[142:145]
	v_mfma_f32_16x16x32_bf16 v[138:141], v[70:73], v[208:211], v[138:141]
	v_mfma_f32_16x16x32_bf16 v[126:129], v[62:65], v[236:239], v[126:129]
	v_mfma_f32_16x16x32_bf16 v[122:125], v[70:73], v[236:239], v[122:125]
	v_mfma_f32_16x16x32_bf16 v[110:113], v[62:65], v[244:247], v[110:113]
	v_mfma_f32_16x16x32_bf16 v[106:109], v[70:73], v[244:247], v[106:109]
	v_mfma_f32_16x16x32_bf16 v[150:153], v[74:77], v[192:195], v[150:153]
	v_mfma_f32_16x16x32_bf16 v[146:149], v[82:85], v[192:195], v[146:149]
	v_mfma_f32_16x16x32_bf16 v[134:137], v[74:77], v[204:207], v[134:137]
	v_mfma_f32_16x16x32_bf16 v[130:133], v[82:85], v[204:207], v[130:133]
	v_mfma_f32_16x16x32_bf16 v[118:121], v[74:77], v[212:215], v[118:121]
	v_mfma_f32_16x16x32_bf16 v[114:117], v[82:85], v[212:215], v[114:117]
	v_mfma_f32_16x16x32_bf16 v[102:105], v[74:77], v[240:243], v[102:105]
	v_mfma_f32_16x16x32_bf16 v[98:101], v[82:85], v[240:243], v[98:101]
	v_mfma_f32_16x16x32_bf16 v[150:153], v[78:81], v[200:203], v[150:153]
	v_mfma_f32_16x16x32_bf16 v[146:149], v[86:89], v[200:203], v[146:149]
	v_mfma_f32_16x16x32_bf16 v[134:137], v[78:81], v[208:211], v[134:137]
	v_mfma_f32_16x16x32_bf16 v[130:133], v[86:89], v[208:211], v[130:133]
	v_mfma_f32_16x16x32_bf16 v[118:121], v[78:81], v[236:239], v[118:121]
	v_mfma_f32_16x16x32_bf16 v[114:117], v[86:89], v[236:239], v[114:117]
	v_mfma_f32_16x16x32_bf16 v[102:105], v[78:81], v[244:247], v[102:105]
	v_mfma_f32_16x16x32_bf16 v[98:101], v[86:89], v[244:247], v[98:101]
	s_setprio 0
	s_barrier
	s_mov_b32 m0, s1
	v_lshl_add_u64 v[182:183], v[182:183], 0, s[18:19]
	s_add_u32 s50, s66, 0x40080
	ds_read_b128 v[192:195], v219 offset:49152
	ds_read_b128 v[200:203], v219 offset:50176
	ds_read_b128 v[204:207], v219 offset:51200
	ds_read_b128 v[208:211], v219 offset:52224
	ds_read_b128 v[212:215], v219 offset:53248
	ds_read_b128 v[236:239], v219 offset:54272
	ds_read_b128 v[240:243], v219 offset:55296
	ds_read_b128 v[244:247], v219 offset:56320
	global_load_lds_dwordx4 v[182:183], off
	v_lshl_add_u64 v[182:183], v[216:217], 0, s[18:19]
	s_mov_b32 m0, s14
	s_addc_u32 s51, s67, 0
	global_load_lds_dwordx4 v[182:183], off
	v_lshl_add_u64 v[182:183], s[50:51], 0, v[166:167]
	s_mov_b32 m0, s34
	s_nop 0
	global_load_lds_dwordx4 v[182:183], off
	v_lshl_add_u64 v[182:183], s[50:51], 0, v[162:163]
	s_mov_b32 m0, s35
	s_nop 0
	global_load_lds_dwordx4 v[182:183], off
	v_lshl_add_u64 v[182:183], v[222:223], 0, s[18:19]
	s_mov_b32 m0, s15
	s_nop 0
	global_load_lds_dwordx4 v[182:183], off
	v_lshl_add_u64 v[182:183], v[226:227], 0, s[18:19]
	s_mov_b32 m0, s31
	s_nop 0
	global_load_lds_dwordx4 v[182:183], off
	s_waitcnt vmcnt(8)
	s_waitcnt lgkmcnt(0)
	s_barrier
	s_setprio 1
	v_mfma_f32_16x16x32_bf16 v[94:97], v[58:61], v[192:195], v[94:97]
	v_mfma_f32_16x16x32_bf16 v[90:93], v[66:69], v[192:195], v[90:93]
	v_mfma_f32_16x16x32_bf16 v[54:57], v[58:61], v[204:207], v[54:57]
	v_mfma_f32_16x16x32_bf16 v[42:45], v[66:69], v[204:207], v[42:45]
	v_mfma_f32_16x16x32_bf16 v[30:33], v[58:61], v[212:215], v[30:33]
	v_mfma_f32_16x16x32_bf16 v[26:29], v[66:69], v[212:215], v[26:29]
	v_mfma_f32_16x16x32_bf16 v[14:17], v[58:61], v[240:243], v[14:17]
	v_mfma_f32_16x16x32_bf16 v[10:13], v[66:69], v[240:243], v[10:13]
	v_mfma_f32_16x16x32_bf16 v[94:97], v[62:65], v[200:203], v[94:97]
	v_mfma_f32_16x16x32_bf16 v[90:93], v[70:73], v[200:203], v[90:93]
	v_mfma_f32_16x16x32_bf16 v[54:57], v[62:65], v[208:211], v[54:57]
	v_mfma_f32_16x16x32_bf16 v[42:45], v[70:73], v[208:211], v[42:45]
	v_mfma_f32_16x16x32_bf16 v[30:33], v[62:65], v[236:239], v[30:33]
	v_mfma_f32_16x16x32_bf16 v[26:29], v[70:73], v[236:239], v[26:29]
	v_mfma_f32_16x16x32_bf16 v[14:17], v[62:65], v[244:247], v[14:17]
	v_mfma_f32_16x16x32_bf16 v[10:13], v[70:73], v[244:247], v[10:13]
	v_mfma_f32_16x16x32_bf16 v[46:49], v[74:77], v[192:195], v[46:49]
	v_mfma_f32_16x16x32_bf16 v[70:73], v[78:81], v[200:203], v[46:49]
	v_mfma_f32_16x16x32_bf16 v[46:49], v[82:85], v[192:195], v[50:53]
	v_mfma_f32_16x16x32_bf16 v[38:41], v[74:77], v[204:207], v[38:41]
	v_mfma_f32_16x16x32_bf16 v[34:37], v[82:85], v[204:207], v[34:37]
	v_mfma_f32_16x16x32_bf16 v[22:25], v[74:77], v[212:215], v[22:25]
	v_mfma_f32_16x16x32_bf16 v[18:21], v[82:85], v[212:215], v[18:21]
	v_mfma_f32_16x16x32_bf16 v[6:9], v[74:77], v[240:243], v[6:9]
	v_mfma_f32_16x16x32_bf16 v[2:5], v[82:85], v[240:243], v[2:5]
	v_mfma_f32_16x16x32_bf16 v[66:69], v[86:89], v[200:203], v[46:49]
	v_mfma_f32_16x16x32_bf16 v[38:41], v[78:81], v[208:211], v[38:41]
	v_mfma_f32_16x16x32_bf16 v[34:37], v[86:89], v[208:211], v[34:37]
	v_mfma_f32_16x16x32_bf16 v[22:25], v[78:81], v[236:239], v[22:25]
	v_mfma_f32_16x16x32_bf16 v[18:21], v[86:89], v[236:239], v[18:21]
	v_mfma_f32_16x16x32_bf16 v[6:9], v[78:81], v[244:247], v[6:9]
	v_mfma_f32_16x16x32_bf16 v[2:5], v[86:89], v[244:247], v[2:5]
	s_setprio 0
	s_barrier
	s_add_i32 vcc_hi, vcc_hi, 2
	s_add_u32 s40, s40, 0x100
	s_addc_u32 s41, s41, 0
	s_add_u32 s59, s59, 0x100
	s_addc_u32 vcc_lo, vcc_lo, 0
	s_cmp_gt_u32 vcc_hi, 13
	s_cbranch_scc0 .LBB0_357
	v_readlane_b32 s40, v253, 55
	v_readlane_b32 s41, v253, 56
	s_and_b64 vcc, exec, s[40:41]
	s_cbranch_vccz .LBB0_360
	s_barrier

.LBB0_397:
	s_add_u32 s52, s48, s50
	s_addc_u32 s53, s49, s51
	v_or_b32_e32 v146, 0x10000, v145
	v_add_u32_e32 v150, 0x10400, v145
	v_add_u32_e32 v154, 0x10800, v145
	v_add_u32_e32 v158, 0x10c00, v145
	v_or_b32_e32 v162, 0x14000, v145
	v_add_u32_e32 v166, 0x14400, v145
	v_add_u32_e32 v170, 0x14800, v145
	v_add_u32_e32 v174, 0x14c00, v145
	s_add_u32 s52, s52, 0x100
	ds_read_b128 v[146:149], v146
	ds_read_b128 v[150:153], v150
	ds_read_b128 v[154:157], v154
	ds_read_b128 v[158:161], v158
	ds_read_b128 v[162:165], v162
	ds_read_b128 v[166:169], v166
	ds_read_b128 v[170:173], v170
	ds_read_b128 v[174:177], v174
	s_addc_u32 s53, s53, 0
	s_add_u32 s93, s39, s50
	s_addc_u32 s94, s41, s51
	s_cmpk_eq_i32 s50, 0x700
	s_cselect_b32 s55, s90, s53
	s_cselect_b32 s54, s91, s52
	s_cselect_b32 s53, s45, s94
	s_cselect_b32 s52, s44, s93
	v_lshl_add_u64 v[194:195], v[140:141], 0, s[50:51]
	s_add_i32 m0, s57, 0xc000
	ds_read_b128 v[178:181], v144
	ds_read_b128 v[182:185], v144 offset:1024
	ds_read_b128 v[186:189], v144 offset:2048
	ds_read_b128 v[190:193], v144 offset:3072
	ds_read_b128 v[200:203], v144 offset:4096
	ds_read_b128 v[204:207], v144 offset:5120
	ds_read_b128 v[208:211], v144 offset:6144
	ds_read_b128 v[212:215], v144 offset:7168
	global_load_lds_dwordx4 v[194:195], off
	v_lshl_add_u64 v[194:195], v[142:143], 0, s[50:51]
	s_add_i32 m0, s57, 0xe000
	s_nop 0
	global_load_lds_dwordx4 v[194:195], off
	s_waitcnt vmcnt(8)
	s_waitcnt lgkmcnt(0)
	s_barrier
	s_setprio 1
	v_mfma_f32_16x16x32_bf16 v[126:129], v[146:149], v[178:181], v[126:129]
	v_mfma_f32_16x16x32_bf16 v[122:125], v[154:157], v[178:181], v[122:125]
	v_mfma_f32_16x16x32_bf16 v[110:113], v[146:149], v[186:189], v[110:113]
	v_mfma_f32_16x16x32_bf16 v[106:109], v[154:157], v[186:189], v[106:109]
	v_mfma_f32_16x16x32_bf16 v[94:97], v[146:149], v[200:203], v[94:97]
	v_mfma_f32_16x16x32_bf16 v[90:93], v[154:157], v[200:203], v[90:93]
	v_mfma_f32_16x16x32_bf16 v[78:81], v[146:149], v[208:211], v[78:81]
	v_mfma_f32_16x16x32_bf16 v[74:77], v[154:157], v[208:211], v[74:77]
	v_mfma_f32_16x16x32_bf16 v[126:129], v[150:153], v[182:185], v[126:129]
	v_mfma_f32_16x16x32_bf16 v[122:125], v[158:161], v[182:185], v[122:125]
	v_mfma_f32_16x16x32_bf16 v[110:113], v[150:153], v[190:193], v[110:113]
	v_mfma_f32_16x16x32_bf16 v[106:109], v[158:161], v[190:193], v[106:109]
	v_mfma_f32_16x16x32_bf16 v[94:97], v[150:153], v[204:207], v[94:97]
	v_mfma_f32_16x16x32_bf16 v[90:93], v[158:161], v[204:207], v[90:93]
	v_mfma_f32_16x16x32_bf16 v[78:81], v[150:153], v[212:215], v[78:81]
	v_mfma_f32_16x16x32_bf16 v[74:77], v[158:161], v[212:215], v[74:77]
	v_mfma_f32_16x16x32_bf16 v[118:121], v[162:165], v[178:181], v[118:121]
	v_mfma_f32_16x16x32_bf16 v[114:117], v[170:173], v[178:181], v[114:117]
	v_mfma_f32_16x16x32_bf16 v[102:105], v[162:165], v[186:189], v[102:105]
	v_mfma_f32_16x16x32_bf16 v[98:101], v[170:173], v[186:189], v[98:101]
	v_mfma_f32_16x16x32_bf16 v[86:89], v[162:165], v[200:203], v[86:89]
	v_mfma_f32_16x16x32_bf16 v[82:85], v[170:173], v[200:203], v[82:85]
	v_mfma_f32_16x16x32_bf16 v[70:73], v[162:165], v[208:211], v[70:73]
	v_mfma_f32_16x16x32_bf16 v[66:69], v[170:173], v[208:211], v[66:69]
	v_mfma_f32_16x16x32_bf16 v[118:121], v[166:169], v[182:185], v[118:121]
	v_mfma_f32_16x16x32_bf16 v[114:117], v[174:177], v[182:185], v[114:117]
	v_mfma_f32_16x16x32_bf16 v[102:105], v[166:169], v[190:193], v[102:105]
	v_mfma_f32_16x16x32_bf16 v[98:101], v[174:177], v[190:193], v[98:101]
	v_mfma_f32_16x16x32_bf16 v[86:89], v[166:169], v[204:207], v[86:89]
	v_mfma_f32_16x16x32_bf16 v[82:85], v[174:177], v[204:207], v[82:85]
	v_mfma_f32_16x16x32_bf16 v[70:73], v[166:169], v[212:215], v[70:73]
	v_mfma_f32_16x16x32_bf16 v[66:69], v[174:177], v[212:215], v[66:69]
	s_setprio 0
	s_barrier
	s_mov_b32 m0, s58
	v_lshl_add_u64 v[194:195], s[52:53], 0, v[0:1]
	s_add_u32 s94, s52, 0x40000
	ds_read_b128 v[178:181], v144 offset:16384
	ds_read_b128 v[182:185], v144 offset:17408
	ds_read_b128 v[186:189], v144 offset:18432
	ds_read_b128 v[190:193], v144 offset:19456
	ds_read_b128 v[200:203], v144 offset:20480
	ds_read_b128 v[204:207], v144 offset:21504
	ds_read_b128 v[208:211], v144 offset:22528
	ds_read_b128 v[212:215], v144 offset:23552
	global_load_lds_dwordx4 v[194:195], off
	v_lshl_add_u64 v[216:217], s[52:53], 0, v[130:131]
	s_mov_b32 m0, s59
	s_addc_u32 s95, s53, 0
	global_load_lds_dwordx4 v[216:217], off
	v_lshl_add_u64 v[218:219], s[94:95], 0, v[0:1]
	s_mov_b32 m0, s60
	v_lshl_add_u64 v[220:221], s[54:55], 0, v[132:133]
	global_load_lds_dwordx4 v[218:219], off
	v_lshl_add_u64 v[218:219], s[94:95], 0, v[130:131]
	s_mov_b32 m0, s61
	s_nop 0
	global_load_lds_dwordx4 v[218:219], off
	v_lshl_add_u64 v[218:219], s[54:55], 0, v[134:135]
	s_mov_b32 m0, s57
	s_nop 0
	global_load_lds_dwordx4 v[218:219], off
	s_mov_b32 m0, s64
	s_nop 0
	global_load_lds_dwordx4 v[220:221], off
	s_waitcnt vmcnt(8)
	s_waitcnt lgkmcnt(0)
	s_barrier
	s_setprio 1
	v_mfma_f32_16x16x32_bf16 v[62:65], v[146:149], v[178:181], v[62:65]
	v_mfma_f32_16x16x32_bf16 v[58:61], v[154:157], v[178:181], v[58:61]
	v_mfma_f32_16x16x32_bf16 v[46:49], v[146:149], v[186:189], v[46:49]
	v_mfma_f32_16x16x32_bf16 v[42:45], v[154:157], v[186:189], v[42:45]
	v_mfma_f32_16x16x32_bf16 v[30:33], v[146:149], v[200:203], v[30:33]
	v_mfma_f32_16x16x32_bf16 v[26:29], v[154:157], v[200:203], v[26:29]
	v_mfma_f32_16x16x32_bf16 v[14:17], v[146:149], v[208:211], v[14:17]
	v_mfma_f32_16x16x32_bf16 v[10:13], v[154:157], v[208:211], v[10:13]
	v_mfma_f32_16x16x32_bf16 v[62:65], v[150:153], v[182:185], v[62:65]
	v_mfma_f32_16x16x32_bf16 v[58:61], v[158:161], v[182:185], v[58:61]
	v_mfma_f32_16x16x32_bf16 v[46:49], v[150:153], v[190:193], v[46:49]
	v_mfma_f32_16x16x32_bf16 v[42:45], v[158:161], v[190:193], v[42:45]
	v_mfma_f32_16x16x32_bf16 v[30:33], v[150:153], v[204:207], v[30:33]
	v_mfma_f32_16x16x32_bf16 v[26:29], v[158:161], v[204:207], v[26:29]
	v_mfma_f32_16x16x32_bf16 v[14:17], v[150:153], v[212:215], v[14:17]
	v_mfma_f32_16x16x32_bf16 v[10:13], v[158:161], v[212:215], v[10:13]
	v_mfma_f32_16x16x32_bf16 v[54:57], v[162:165], v[178:181], v[54:57]
	v_mfma_f32_16x16x32_bf16 v[50:53], v[170:173], v[178:181], v[50:53]
	v_mfma_f32_16x16x32_bf16 v[38:41], v[162:165], v[186:189], v[38:41]
	v_mfma_f32_16x16x32_bf16 v[34:37], v[170:173], v[186:189], v[34:37]
	v_mfma_f32_16x16x32_bf16 v[22:25], v[162:165], v[200:203], v[22:25]
	v_mfma_f32_16x16x32_bf16 v[18:21], v[170:173], v[200:203], v[18:21]
	v_mfma_f32_16x16x32_bf16 v[6:9], v[162:165], v[208:211], v[6:9]
	v_mfma_f32_16x16x32_bf16 v[2:5], v[170:173], v[208:211], v[2:5]
	v_mfma_f32_16x16x32_bf16 v[54:57], v[166:169], v[182:185], v[54:57]
	v_mfma_f32_16x16x32_bf16 v[50:53], v[174:177], v[182:185], v[50:53]
	v_mfma_f32_16x16x32_bf16 v[38:41], v[166:169], v[190:193], v[38:41]
	v_mfma_f32_16x16x32_bf16 v[34:37], v[174:177], v[190:193], v[34:37]
	v_mfma_f32_16x16x32_bf16 v[22:25], v[166:169], v[204:207], v[22:25]
	v_mfma_f32_16x16x32_bf16 v[18:21], v[174:177], v[204:207], v[18:21]
	v_mfma_f32_16x16x32_bf16 v[6:9], v[166:169], v[212:215], v[6:9]
	v_mfma_f32_16x16x32_bf16 v[2:5], v[174:177], v[212:215], v[2:5]
	s_setprio 0
	s_barrier
	v_or_b32_e32 v146, 0x18000, v145
	v_add_u32_e32 v150, 0x18400, v145
	v_add_u32_e32 v154, 0x18800, v145
	v_add_u32_e32 v158, 0x18c00, v145
	v_or_b32_e32 v162, 0x1c000, v145
	v_add_u32_e32 v166, 0x1c400, v145
	v_add_u32_e32 v170, 0x1c800, v145
	v_add_u32_e32 v174, 0x1cc00, v145
	ds_read_b128 v[146:149], v146
	ds_read_b128 v[150:153], v150
	ds_read_b128 v[154:157], v154
	ds_read_b128 v[158:161], v158
	ds_read_b128 v[162:165], v162
	ds_read_b128 v[166:169], v166
	ds_read_b128 v[170:173], v170
	ds_read_b128 v[174:177], v174
	s_add_u32 s54, s54, 0x40000
	s_addc_u32 s55, s55, 0
	s_mov_b32 m0, s65
	v_lshl_add_u64 v[222:223], s[54:55], 0, v[134:135]
	ds_read_b128 v[178:181], v144 offset:32768
	ds_read_b128 v[182:185], v144 offset:33792
	ds_read_b128 v[186:189], v144 offset:34816
	ds_read_b128 v[190:193], v144 offset:35840
	ds_read_b128 v[200:203], v144 offset:36864
	ds_read_b128 v[204:207], v144 offset:37888
	ds_read_b128 v[208:211], v144 offset:38912
	ds_read_b128 v[212:215], v144 offset:39936
	global_load_lds_dwordx4 v[222:223], off
	v_lshl_add_u64 v[222:223], s[54:55], 0, v[132:133]
	s_mov_b32 m0, s66
	s_nop 0
	global_load_lds_dwordx4 v[222:223], off
	s_waitcnt vmcnt(8)
	s_waitcnt lgkmcnt(0)
	s_barrier
	s_setprio 1
	v_mfma_f32_16x16x32_bf16 v[126:129], v[146:149], v[178:181], v[126:129]
	v_mfma_f32_16x16x32_bf16 v[122:125], v[154:157], v[178:181], v[122:125]
	v_mfma_f32_16x16x32_bf16 v[110:113], v[146:149], v[186:189], v[110:113]
	v_mfma_f32_16x16x32_bf16 v[106:109], v[154:157], v[186:189], v[106:109]
	v_mfma_f32_16x16x32_bf16 v[94:97], v[146:149], v[200:203], v[94:97]
	v_mfma_f32_16x16x32_bf16 v[90:93], v[154:157], v[200:203], v[90:93]
	v_mfma_f32_16x16x32_bf16 v[78:81], v[146:149], v[208:211], v[78:81]
	v_mfma_f32_16x16x32_bf16 v[74:77], v[154:157], v[208:211], v[74:77]
	v_mfma_f32_16x16x32_bf16 v[126:129], v[150:153], v[182:185], v[126:129]
	v_mfma_f32_16x16x32_bf16 v[122:125], v[158:161], v[182:185], v[122:125]
	v_mfma_f32_16x16x32_bf16 v[110:113], v[150:153], v[190:193], v[110:113]
	v_mfma_f32_16x16x32_bf16 v[106:109], v[158:161], v[190:193], v[106:109]
	v_mfma_f32_16x16x32_bf16 v[94:97], v[150:153], v[204:207], v[94:97]
	v_mfma_f32_16x16x32_bf16 v[90:93], v[158:161], v[204:207], v[90:93]
	v_mfma_f32_16x16x32_bf16 v[78:81], v[150:153], v[212:215], v[78:81]
	v_mfma_f32_16x16x32_bf16 v[74:77], v[158:161], v[212:215], v[74:77]
	v_mfma_f32_16x16x32_bf16 v[118:121], v[162:165], v[178:181], v[118:121]
	v_mfma_f32_16x16x32_bf16 v[114:117], v[170:173], v[178:181], v[114:117]
	v_mfma_f32_16x16x32_bf16 v[102:105], v[162:165], v[186:189], v[102:105]
	v_mfma_f32_16x16x32_bf16 v[98:101], v[170:173], v[186:189], v[98:101]
	v_mfma_f32_16x16x32_bf16 v[86:89], v[162:165], v[200:203], v[86:89]
	v_mfma_f32_16x16x32_bf16 v[82:85], v[170:173], v[200:203], v[82:85]
	v_mfma_f32_16x16x32_bf16 v[70:73], v[162:165], v[208:211], v[70:73]
	v_mfma_f32_16x16x32_bf16 v[66:69], v[170:173], v[208:211], v[66:69]
	v_mfma_f32_16x16x32_bf16 v[118:121], v[166:169], v[182:185], v[118:121]
	v_mfma_f32_16x16x32_bf16 v[114:117], v[174:177], v[182:185], v[114:117]
	v_mfma_f32_16x16x32_bf16 v[102:105], v[166:169], v[190:193], v[102:105]
	v_mfma_f32_16x16x32_bf16 v[98:101], v[174:177], v[190:193], v[98:101]
	v_mfma_f32_16x16x32_bf16 v[86:89], v[166:169], v[204:207], v[86:89]
	v_mfma_f32_16x16x32_bf16 v[82:85], v[174:177], v[204:207], v[82:85]
	v_mfma_f32_16x16x32_bf16 v[70:73], v[166:169], v[212:215], v[70:73]
	v_mfma_f32_16x16x32_bf16 v[66:69], v[174:177], v[212:215], v[66:69]
	s_setprio 0
	s_barrier
	s_mov_b32 m0, s67
	v_lshl_add_u64 v[194:195], v[194:195], 0, s[18:19]
	s_add_u32 s52, s52, 0x40080
	ds_read_b128 v[178:181], v144 offset:49152
	ds_read_b128 v[182:185], v144 offset:50176
	ds_read_b128 v[186:189], v144 offset:51200
	ds_read_b128 v[190:193], v144 offset:52224
	ds_read_b128 v[200:203], v144 offset:53248
	ds_read_b128 v[204:207], v144 offset:54272
	ds_read_b128 v[208:211], v144 offset:55296
	ds_read_b128 v[212:215], v144 offset:56320
	global_load_lds_dwordx4 v[194:195], off
	v_lshl_add_u64 v[194:195], v[216:217], 0, s[18:19]
	s_mov_b32 m0, s80
	s_addc_u32 s53, s53, 0
	global_load_lds_dwordx4 v[194:195], off
	v_lshl_add_u64 v[194:195], s[52:53], 0, v[0:1]
	s_mov_b32 m0, s84
	s_nop 0
	global_load_lds_dwordx4 v[194:195], off
	v_lshl_add_u64 v[194:195], s[52:53], 0, v[130:131]
	s_mov_b32 m0, s85
	s_nop 0
	global_load_lds_dwordx4 v[194:195], off
	v_lshl_add_u64 v[194:195], v[218:219], 0, s[18:19]
	s_mov_b32 m0, s82
	s_nop 0
	global_load_lds_dwordx4 v[194:195], off
	v_lshl_add_u64 v[194:195], v[220:221], 0, s[18:19]
	s_mov_b32 m0, s83
	s_nop 0
	global_load_lds_dwordx4 v[194:195], off
	s_waitcnt vmcnt(8)
	s_waitcnt lgkmcnt(0)
	s_barrier
	s_setprio 1
	v_mfma_f32_16x16x32_bf16 v[62:65], v[146:149], v[178:181], v[62:65]
	v_mfma_f32_16x16x32_bf16 v[58:61], v[154:157], v[178:181], v[58:61]
	v_mfma_f32_16x16x32_bf16 v[46:49], v[146:149], v[186:189], v[46:49]
	v_mfma_f32_16x16x32_bf16 v[42:45], v[154:157], v[186:189], v[42:45]
	v_mfma_f32_16x16x32_bf16 v[30:33], v[146:149], v[200:203], v[30:33]
	v_mfma_f32_16x16x32_bf16 v[26:29], v[154:157], v[200:203], v[26:29]
	v_mfma_f32_16x16x32_bf16 v[14:17], v[146:149], v[208:211], v[14:17]
	v_mfma_f32_16x16x32_bf16 v[10:13], v[154:157], v[208:211], v[10:13]
	v_mfma_f32_16x16x32_bf16 v[62:65], v[150:153], v[182:185], v[62:65]
	v_mfma_f32_16x16x32_bf16 v[58:61], v[158:161], v[182:185], v[58:61]
	v_mfma_f32_16x16x32_bf16 v[46:49], v[150:153], v[190:193], v[46:49]
	v_mfma_f32_16x16x32_bf16 v[42:45], v[158:161], v[190:193], v[42:45]
	v_mfma_f32_16x16x32_bf16 v[30:33], v[150:153], v[204:207], v[30:33]
	v_mfma_f32_16x16x32_bf16 v[26:29], v[158:161], v[204:207], v[26:29]
	v_mfma_f32_16x16x32_bf16 v[14:17], v[150:153], v[212:215], v[14:17]
	v_mfma_f32_16x16x32_bf16 v[10:13], v[158:161], v[212:215], v[10:13]
	v_mfma_f32_16x16x32_bf16 v[54:57], v[162:165], v[178:181], v[54:57]
	v_mfma_f32_16x16x32_bf16 v[50:53], v[170:173], v[178:181], v[50:53]
	v_mfma_f32_16x16x32_bf16 v[38:41], v[162:165], v[186:189], v[38:41]
	v_mfma_f32_16x16x32_bf16 v[34:37], v[170:173], v[186:189], v[34:37]
	v_mfma_f32_16x16x32_bf16 v[22:25], v[162:165], v[200:203], v[22:25]
	v_mfma_f32_16x16x32_bf16 v[18:21], v[170:173], v[200:203], v[18:21]
	v_mfma_f32_16x16x32_bf16 v[6:9], v[162:165], v[208:211], v[6:9]
	v_mfma_f32_16x16x32_bf16 v[2:5], v[170:173], v[208:211], v[2:5]
	v_mfma_f32_16x16x32_bf16 v[54:57], v[166:169], v[182:185], v[54:57]
	v_mfma_f32_16x16x32_bf16 v[50:53], v[174:177], v[182:185], v[50:53]
	v_mfma_f32_16x16x32_bf16 v[38:41], v[166:169], v[190:193], v[38:41]
	v_mfma_f32_16x16x32_bf16 v[34:37], v[174:177], v[190:193], v[34:37]
	v_mfma_f32_16x16x32_bf16 v[22:25], v[166:169], v[204:207], v[22:25]
	v_mfma_f32_16x16x32_bf16 v[18:21], v[174:177], v[204:207], v[18:21]
	v_mfma_f32_16x16x32_bf16 v[6:9], v[166:169], v[212:215], v[6:9]
	v_mfma_f32_16x16x32_bf16 v[2:5], v[174:177], v[212:215], v[2:5]
	s_setprio 0
	s_barrier
	s_add_i32 s92, s92, 2
	s_add_u32 s50, s50, 0x100
	s_addc_u32 s51, s51, 0
	s_cmp_gt_u32 s92, 13
	s_cbranch_scc0 .LBB0_397
	s_and_b64 vcc, exec, s[14:15]
	s_cbranch_vccz .LBB0_400
	s_barrier

.LBB0_438:
	v_or_b32_e32 v163, 0x10000, v162
	v_add_u32_e32 v168, 0x10400, v162
	ds_read_b128 v[164:167], v163
	ds_read_b128 v[168:171], v168
	v_add_u32_e32 v163, 0x10800, v162
	v_add_u32_e32 v176, 0x10c00, v162
	s_add_u32 s50, s16, s48
	ds_read_b128 v[172:175], v163
	ds_read_b128 v[176:179], v176
	v_or_b32_e32 v163, 0x14000, v162
	v_add_u32_e32 v184, 0x14400, v162
	s_addc_u32 s51, s17, s49
	ds_read_b128 v[180:183], v163
	ds_read_b128 v[184:187], v184
	v_add_u32_e32 v163, 0x14800, v162
	v_add_u32_e32 v192, 0x14c00, v162
	s_add_u32 s50, s50, 0x100
	ds_read_b128 v[188:191], v163
	ds_read_b128 v[192:195], v192
	s_addc_u32 s51, s51, 0
	s_add_u32 s91, s41, s48
	s_addc_u32 s92, s89, s49
	s_cmpk_eq_i32 s48, 0x700
	s_cselect_b32 s53, s29, s51
	s_cselect_b32 s52, s39, s50
	s_cselect_b32 s51, s45, s92
	s_cselect_b32 s50, s44, s91
	v_lshl_add_u64 v[226:227], v[156:157], 0, s[48:49]
	s_add_i32 m0, s58, 0xc000
	ds_read_b128 v[200:203], v161
	ds_read_b128 v[204:207], v161 offset:1024
	ds_read_b128 v[208:211], v161 offset:2048
	ds_read_b128 v[212:215], v161 offset:3072
	ds_read_b128 v[216:219], v161 offset:4096
	ds_read_b128 v[220:223], v161 offset:5120
	ds_read_b128 v[236:239], v161 offset:6144
	ds_read_b128 v[240:243], v161 offset:7168
	global_load_lds_dwordx4 v[226:227], off
	v_lshl_add_u64 v[226:227], v[158:159], 0, s[48:49]
	s_add_i32 m0, s58, 0xe000
	s_nop 0
	global_load_lds_dwordx4 v[226:227], off
	s_waitcnt vmcnt(8)
	s_waitcnt lgkmcnt(0)
	s_barrier
	s_setprio 1
	v_mfma_f32_16x16x32_bf16 v[126:129], v[164:167], v[200:203], v[126:129]
	v_mfma_f32_16x16x32_bf16 v[122:125], v[172:175], v[200:203], v[122:125]
	v_mfma_f32_16x16x32_bf16 v[110:113], v[164:167], v[208:211], v[110:113]
	v_mfma_f32_16x16x32_bf16 v[106:109], v[172:175], v[208:211], v[106:109]
	v_mfma_f32_16x16x32_bf16 v[94:97], v[164:167], v[216:219], v[94:97]
	v_mfma_f32_16x16x32_bf16 v[90:93], v[172:175], v[216:219], v[90:93]
	v_mfma_f32_16x16x32_bf16 v[86:89], v[164:167], v[236:239], v[86:89]
	v_mfma_f32_16x16x32_bf16 v[78:81], v[172:175], v[236:239], v[78:81]
	v_mfma_f32_16x16x32_bf16 v[126:129], v[168:171], v[204:207], v[126:129]
	v_mfma_f32_16x16x32_bf16 v[122:125], v[176:179], v[204:207], v[122:125]
	v_mfma_f32_16x16x32_bf16 v[110:113], v[168:171], v[212:215], v[110:113]
	v_mfma_f32_16x16x32_bf16 v[106:109], v[176:179], v[212:215], v[106:109]
	v_mfma_f32_16x16x32_bf16 v[94:97], v[168:171], v[220:223], v[94:97]
	v_mfma_f32_16x16x32_bf16 v[90:93], v[176:179], v[220:223], v[90:93]
	v_mfma_f32_16x16x32_bf16 v[86:89], v[168:171], v[240:243], v[86:89]
	v_mfma_f32_16x16x32_bf16 v[78:81], v[176:179], v[240:243], v[78:81]
	v_mfma_f32_16x16x32_bf16 v[118:121], v[180:183], v[200:203], v[118:121]
	v_mfma_f32_16x16x32_bf16 v[114:117], v[188:191], v[200:203], v[114:117]
	v_mfma_f32_16x16x32_bf16 v[102:105], v[180:183], v[208:211], v[102:105]
	v_mfma_f32_16x16x32_bf16 v[98:101], v[188:191], v[208:211], v[98:101]
	v_mfma_f32_16x16x32_bf16 v[82:85], v[180:183], v[216:219], v[82:85]
	v_mfma_f32_16x16x32_bf16 v[74:77], v[188:191], v[216:219], v[74:77]
	v_mfma_f32_16x16x32_bf16 v[70:73], v[180:183], v[236:239], v[70:73]
	v_mfma_f32_16x16x32_bf16 v[66:69], v[188:191], v[236:239], v[66:69]
	v_mfma_f32_16x16x32_bf16 v[118:121], v[184:187], v[204:207], v[118:121]
	v_mfma_f32_16x16x32_bf16 v[114:117], v[192:195], v[204:207], v[114:117]
	v_mfma_f32_16x16x32_bf16 v[102:105], v[184:187], v[212:215], v[102:105]
	v_mfma_f32_16x16x32_bf16 v[98:101], v[192:195], v[212:215], v[98:101]
	v_mfma_f32_16x16x32_bf16 v[82:85], v[184:187], v[220:223], v[82:85]
	v_mfma_f32_16x16x32_bf16 v[74:77], v[192:195], v[220:223], v[74:77]
	v_mfma_f32_16x16x32_bf16 v[70:73], v[184:187], v[240:243], v[70:73]
	v_mfma_f32_16x16x32_bf16 v[66:69], v[192:195], v[240:243], v[66:69]
	s_setprio 0
	s_barrier
	s_mov_b32 m0, s59
	v_lshl_add_u64 v[226:227], s[50:51], 0, v[0:1]
	s_add_u32 s92, s50, 0x40000
	ds_read_b128 v[200:203], v161 offset:16384
	ds_read_b128 v[204:207], v161 offset:17408
	ds_read_b128 v[208:211], v161 offset:18432
	ds_read_b128 v[212:215], v161 offset:19456
	ds_read_b128 v[216:219], v161 offset:20480
	ds_read_b128 v[220:223], v161 offset:21504
	ds_read_b128 v[236:239], v161 offset:22528
	ds_read_b128 v[240:243], v161 offset:23552
	global_load_lds_dwordx4 v[226:227], off
	v_lshl_add_u64 v[244:245], s[50:51], 0, v[142:143]
	s_mov_b32 m0, s60
	s_addc_u32 s93, s51, 0
	global_load_lds_dwordx4 v[244:245], off
	v_lshl_add_u64 v[246:247], s[92:93], 0, v[0:1]
	s_mov_b32 m0, s61
	v_lshl_add_u64 v[248:249], s[52:53], 0, v[144:145]
	global_load_lds_dwordx4 v[246:247], off
	v_lshl_add_u64 v[246:247], s[92:93], 0, v[142:143]
	s_mov_b32 m0, s62
	s_nop 0
	global_load_lds_dwordx4 v[246:247], off
	v_lshl_add_u64 v[246:247], s[52:53], 0, v[148:149]
	s_mov_b32 m0, s58
	s_nop 0
	global_load_lds_dwordx4 v[246:247], off
	s_mov_b32 m0, s63
	s_nop 0
	global_load_lds_dwordx4 v[248:249], off
	s_waitcnt vmcnt(8)
	s_waitcnt lgkmcnt(0)
	s_barrier
	s_setprio 1
	v_mfma_f32_16x16x32_bf16 v[62:65], v[164:167], v[200:203], v[62:65]
	v_mfma_f32_16x16x32_bf16 v[58:61], v[172:175], v[200:203], v[58:61]
	v_mfma_f32_16x16x32_bf16 v[54:57], v[164:167], v[208:211], v[54:57]
	v_mfma_f32_16x16x32_bf16 v[46:49], v[172:175], v[208:211], v[46:49]
	v_mfma_f32_16x16x32_bf16 v[30:33], v[164:167], v[216:219], v[30:33]
	v_mfma_f32_16x16x32_bf16 v[26:29], v[172:175], v[216:219], v[26:29]
	v_mfma_f32_16x16x32_bf16 v[22:25], v[164:167], v[236:239], v[22:25]
	v_mfma_f32_16x16x32_bf16 v[14:17], v[172:175], v[236:239], v[14:17]
	v_mfma_f32_16x16x32_bf16 v[62:65], v[168:171], v[204:207], v[62:65]
	v_mfma_f32_16x16x32_bf16 v[58:61], v[176:179], v[204:207], v[58:61]
	v_mfma_f32_16x16x32_bf16 v[54:57], v[168:171], v[212:215], v[54:57]
	v_mfma_f32_16x16x32_bf16 v[46:49], v[176:179], v[212:215], v[46:49]
	v_mfma_f32_16x16x32_bf16 v[30:33], v[168:171], v[220:223], v[30:33]
	v_mfma_f32_16x16x32_bf16 v[26:29], v[176:179], v[220:223], v[26:29]
	v_mfma_f32_16x16x32_bf16 v[22:25], v[168:171], v[240:243], v[22:25]
	v_mfma_f32_16x16x32_bf16 v[14:17], v[176:179], v[240:243], v[14:17]
	v_mfma_f32_16x16x32_bf16 v[50:53], v[180:183], v[200:203], v[50:53]
	v_mfma_f32_16x16x32_bf16 v[42:45], v[188:191], v[200:203], v[42:45]
	v_mfma_f32_16x16x32_bf16 v[38:41], v[180:183], v[208:211], v[38:41]
	v_mfma_f32_16x16x32_bf16 v[34:37], v[188:191], v[208:211], v[34:37]
	v_mfma_f32_16x16x32_bf16 v[18:21], v[180:183], v[216:219], v[18:21]
	v_mfma_f32_16x16x32_bf16 v[10:13], v[188:191], v[216:219], v[10:13]
	v_mfma_f32_16x16x32_bf16 v[6:9], v[180:183], v[236:239], v[6:9]
	v_mfma_f32_16x16x32_bf16 v[2:5], v[188:191], v[236:239], v[2:5]
	v_mfma_f32_16x16x32_bf16 v[50:53], v[184:187], v[204:207], v[50:53]
	v_mfma_f32_16x16x32_bf16 v[42:45], v[192:195], v[204:207], v[42:45]
	v_mfma_f32_16x16x32_bf16 v[38:41], v[184:187], v[212:215], v[38:41]
	v_mfma_f32_16x16x32_bf16 v[34:37], v[192:195], v[212:215], v[34:37]
	v_mfma_f32_16x16x32_bf16 v[18:21], v[184:187], v[220:223], v[18:21]
	v_mfma_f32_16x16x32_bf16 v[10:13], v[192:195], v[220:223], v[10:13]
	v_mfma_f32_16x16x32_bf16 v[6:9], v[184:187], v[240:243], v[6:9]
	v_mfma_f32_16x16x32_bf16 v[2:5], v[192:195], v[240:243], v[2:5]
	s_setprio 0
	s_barrier
	v_or_b32_e32 v163, 0x18000, v162
	v_add_u32_e32 v168, 0x18400, v162
	ds_read_b128 v[164:167], v163
	ds_read_b128 v[168:171], v168
	v_add_u32_e32 v163, 0x18800, v162
	v_add_u32_e32 v176, 0x18c00, v162
	ds_read_b128 v[172:175], v163
	ds_read_b128 v[176:179], v176
	v_or_b32_e32 v163, 0x1c000, v162
	v_add_u32_e32 v184, 0x1c400, v162
	ds_read_b128 v[180:183], v163
	ds_read_b128 v[184:187], v184
	v_add_u32_e32 v163, 0x1c800, v162
	v_add_u32_e32 v192, 0x1cc00, v162
	ds_read_b128 v[188:191], v163
	ds_read_b128 v[192:195], v192
	s_add_u32 s52, s52, 0x40000
	s_addc_u32 s53, s53, 0
	s_mov_b32 m0, s64
	v_lshl_add_u64 v[228:229], s[52:53], 0, v[148:149]
	ds_read_b128 v[200:203], v161 offset:32768
	ds_read_b128 v[204:207], v161 offset:33792
	ds_read_b128 v[208:211], v161 offset:34816
	ds_read_b128 v[212:215], v161 offset:35840
	ds_read_b128 v[216:219], v161 offset:36864
	ds_read_b128 v[220:223], v161 offset:37888
	ds_read_b128 v[236:239], v161 offset:38912
	ds_read_b128 v[240:243], v161 offset:39936
	global_load_lds_dwordx4 v[228:229], off
	v_lshl_add_u64 v[228:229], s[52:53], 0, v[144:145]
	s_mov_b32 m0, s65
	s_nop 0
	global_load_lds_dwordx4 v[228:229], off
	s_waitcnt vmcnt(8)
	s_waitcnt lgkmcnt(0)
	s_barrier
	s_setprio 1
	v_mfma_f32_16x16x32_bf16 v[126:129], v[164:167], v[200:203], v[126:129]
	v_mfma_f32_16x16x32_bf16 v[122:125], v[172:175], v[200:203], v[122:125]
	v_mfma_f32_16x16x32_bf16 v[110:113], v[164:167], v[208:211], v[110:113]
	v_mfma_f32_16x16x32_bf16 v[106:109], v[172:175], v[208:211], v[106:109]
	v_mfma_f32_16x16x32_bf16 v[94:97], v[164:167], v[216:219], v[94:97]
	v_mfma_f32_16x16x32_bf16 v[90:93], v[172:175], v[216:219], v[90:93]
	v_mfma_f32_16x16x32_bf16 v[86:89], v[164:167], v[236:239], v[86:89]
	v_mfma_f32_16x16x32_bf16 v[78:81], v[172:175], v[236:239], v[78:81]
	v_mfma_f32_16x16x32_bf16 v[126:129], v[168:171], v[204:207], v[126:129]
	v_mfma_f32_16x16x32_bf16 v[122:125], v[176:179], v[204:207], v[122:125]
	v_mfma_f32_16x16x32_bf16 v[110:113], v[168:171], v[212:215], v[110:113]
	v_mfma_f32_16x16x32_bf16 v[106:109], v[176:179], v[212:215], v[106:109]
	v_mfma_f32_16x16x32_bf16 v[94:97], v[168:171], v[220:223], v[94:97]
	v_mfma_f32_16x16x32_bf16 v[90:93], v[176:179], v[220:223], v[90:93]
	v_mfma_f32_16x16x32_bf16 v[86:89], v[168:171], v[240:243], v[86:89]
	v_mfma_f32_16x16x32_bf16 v[78:81], v[176:179], v[240:243], v[78:81]
	v_mfma_f32_16x16x32_bf16 v[118:121], v[180:183], v[200:203], v[118:121]
	v_mfma_f32_16x16x32_bf16 v[114:117], v[188:191], v[200:203], v[114:117]
	v_mfma_f32_16x16x32_bf16 v[102:105], v[180:183], v[208:211], v[102:105]
	v_mfma_f32_16x16x32_bf16 v[98:101], v[188:191], v[208:211], v[98:101]
	v_mfma_f32_16x16x32_bf16 v[82:85], v[180:183], v[216:219], v[82:85]
	v_mfma_f32_16x16x32_bf16 v[74:77], v[188:191], v[216:219], v[74:77]
	v_mfma_f32_16x16x32_bf16 v[70:73], v[180:183], v[236:239], v[70:73]
	v_mfma_f32_16x16x32_bf16 v[66:69], v[188:191], v[236:239], v[66:69]
	v_mfma_f32_16x16x32_bf16 v[118:121], v[184:187], v[204:207], v[118:121]
	v_mfma_f32_16x16x32_bf16 v[114:117], v[192:195], v[204:207], v[114:117]
	v_mfma_f32_16x16x32_bf16 v[102:105], v[184:187], v[212:215], v[102:105]
	v_mfma_f32_16x16x32_bf16 v[98:101], v[192:195], v[212:215], v[98:101]
	v_mfma_f32_16x16x32_bf16 v[82:85], v[184:187], v[220:223], v[82:85]
	v_mfma_f32_16x16x32_bf16 v[74:77], v[192:195], v[220:223], v[74:77]
	v_mfma_f32_16x16x32_bf16 v[70:73], v[184:187], v[240:243], v[70:73]
	v_mfma_f32_16x16x32_bf16 v[66:69], v[192:195], v[240:243], v[66:69]
	s_setprio 0
	s_barrier
	s_mov_b32 m0, s66
	v_lshl_add_u64 v[226:227], v[226:227], 0, s[18:19]
	s_add_u32 s50, s50, 0x40080
	ds_read_b128 v[200:203], v161 offset:49152
	ds_read_b128 v[204:207], v161 offset:50176
	ds_read_b128 v[208:211], v161 offset:51200
	ds_read_b128 v[212:215], v161 offset:52224
	ds_read_b128 v[216:219], v161 offset:53248
	ds_read_b128 v[220:223], v161 offset:54272
	ds_read_b128 v[236:239], v161 offset:55296
	ds_read_b128 v[240:243], v161 offset:56320
	global_load_lds_dwordx4 v[226:227], off
	v_lshl_add_u64 v[226:227], v[244:245], 0, s[18:19]
	s_mov_b32 m0, s67
	s_addc_u32 s51, s51, 0
	global_load_lds_dwordx4 v[226:227], off
	v_lshl_add_u64 v[226:227], s[50:51], 0, v[0:1]
	s_mov_b32 m0, s83
	s_nop 0
	global_load_lds_dwordx4 v[226:227], off
	v_lshl_add_u64 v[226:227], s[50:51], 0, v[142:143]
	s_mov_b32 m0, s84
	s_nop 0
	global_load_lds_dwordx4 v[226:227], off
	v_lshl_add_u64 v[226:227], v[246:247], 0, s[18:19]
	s_mov_b32 m0, s80
	s_nop 0
	global_load_lds_dwordx4 v[226:227], off
	v_lshl_add_u64 v[226:227], v[248:249], 0, s[18:19]
	s_mov_b32 m0, s82
	s_nop 0
	global_load_lds_dwordx4 v[226:227], off
	s_waitcnt vmcnt(8)
	s_waitcnt lgkmcnt(0)
	s_barrier
	s_setprio 1
	v_mfma_f32_16x16x32_bf16 v[62:65], v[164:167], v[200:203], v[62:65]
	v_mfma_f32_16x16x32_bf16 v[58:61], v[172:175], v[200:203], v[58:61]
	v_mfma_f32_16x16x32_bf16 v[54:57], v[164:167], v[208:211], v[54:57]
	v_mfma_f32_16x16x32_bf16 v[46:49], v[172:175], v[208:211], v[46:49]
	v_mfma_f32_16x16x32_bf16 v[30:33], v[164:167], v[216:219], v[30:33]
	v_mfma_f32_16x16x32_bf16 v[26:29], v[172:175], v[216:219], v[26:29]
	v_mfma_f32_16x16x32_bf16 v[22:25], v[164:167], v[236:239], v[22:25]
	v_mfma_f32_16x16x32_bf16 v[14:17], v[172:175], v[236:239], v[14:17]
	v_mfma_f32_16x16x32_bf16 v[62:65], v[168:171], v[204:207], v[62:65]
	v_mfma_f32_16x16x32_bf16 v[58:61], v[176:179], v[204:207], v[58:61]
	v_mfma_f32_16x16x32_bf16 v[54:57], v[168:171], v[212:215], v[54:57]
	v_mfma_f32_16x16x32_bf16 v[46:49], v[176:179], v[212:215], v[46:49]
	v_mfma_f32_16x16x32_bf16 v[30:33], v[168:171], v[220:223], v[30:33]
	v_mfma_f32_16x16x32_bf16 v[26:29], v[176:179], v[220:223], v[26:29]
	v_mfma_f32_16x16x32_bf16 v[22:25], v[168:171], v[240:243], v[22:25]
	v_mfma_f32_16x16x32_bf16 v[14:17], v[176:179], v[240:243], v[14:17]
	v_mfma_f32_16x16x32_bf16 v[50:53], v[180:183], v[200:203], v[50:53]
	v_mfma_f32_16x16x32_bf16 v[42:45], v[188:191], v[200:203], v[42:45]
	v_mfma_f32_16x16x32_bf16 v[38:41], v[180:183], v[208:211], v[38:41]
	v_mfma_f32_16x16x32_bf16 v[34:37], v[188:191], v[208:211], v[34:37]
	v_mfma_f32_16x16x32_bf16 v[18:21], v[180:183], v[216:219], v[18:21]
	v_mfma_f32_16x16x32_bf16 v[10:13], v[188:191], v[216:219], v[10:13]
	v_mfma_f32_16x16x32_bf16 v[6:9], v[180:183], v[236:239], v[6:9]
	v_mfma_f32_16x16x32_bf16 v[2:5], v[188:191], v[236:239], v[2:5]
	v_mfma_f32_16x16x32_bf16 v[50:53], v[184:187], v[204:207], v[50:53]
	v_mfma_f32_16x16x32_bf16 v[42:45], v[192:195], v[204:207], v[42:45]
	v_mfma_f32_16x16x32_bf16 v[38:41], v[184:187], v[212:215], v[38:41]
	v_mfma_f32_16x16x32_bf16 v[34:37], v[192:195], v[212:215], v[34:37]
	v_mfma_f32_16x16x32_bf16 v[18:21], v[184:187], v[220:223], v[18:21]
	v_mfma_f32_16x16x32_bf16 v[10:13], v[192:195], v[220:223], v[10:13]
	v_mfma_f32_16x16x32_bf16 v[6:9], v[184:187], v[240:243], v[6:9]
	v_mfma_f32_16x16x32_bf16 v[2:5], v[192:195], v[240:243], v[2:5]
	s_setprio 0
	s_barrier
	s_add_i32 s90, s90, 2
	s_add_u32 s48, s48, 0x100
	s_addc_u32 s49, s49, 0
	s_cmp_gt_u32 s90, 13
	s_cbranch_scc0 .LBB0_438
	s_add_u32 s48, s41, 0xffffff00
	s_addc_u32 s49, s89, -1
	s_and_b64 vcc, exec, s[36:37]
	s_movk_i32 s90, 0xfea0
	s_cbranch_vccnz .LBB0_441
	v_lshl_add_u32 v2, s38, 8, v160
	v_ashrrev_i32_e32 v3, 31, v2
	v_lshl_add_u64 v[2:3], v[2:3], 3, s[14:15]
	global_load_dwordx2 v[150:151], v[2:3], off nt
	global_load_dwordx2 v[146:147], v[2:3], off offset:128 nt
	global_load_dwordx2 v[140:141], v[2:3], off offset:256 nt
	global_load_dwordx2 v[138:139], v[2:3], off offset:384 nt
	global_load_dwordx2 v[136:137], v[2:3], off offset:1024 nt
	global_load_dwordx2 v[134:135], v[2:3], off offset:1152 nt
	global_load_dwordx2 v[132:133], v[2:3], off offset:1280 nt
	global_load_dwordx2 v[130:131], v[2:3], off offset:1408 nt
	v_mov_b32_e32 v2, 0
	s_mov_b32 s0, s40
	s_mov_b32 s34, s38
	s_mov_b64 s[16:17], s[46:47]
	s_mov_b32 s85, s88
	v_mov_b32_e32 v3, v2
	v_mov_b32_e32 v4, v2
	v_mov_b32_e32 v5, v2
	v_mov_b32_e32 v6, v2
	v_mov_b32_e32 v7, v2
	v_mov_b32_e32 v8, v2
	v_mov_b32_e32 v9, v2
	v_mov_b32_e32 v10, v2
	v_mov_b32_e32 v11, v2
	v_mov_b32_e32 v12, v2
	v_mov_b32_e32 v13, v2
	v_mov_b32_e32 v18, v2
	v_mov_b32_e32 v19, v2
	v_mov_b32_e32 v20, v2
	v_mov_b32_e32 v21, v2
	v_mov_b32_e32 v34, v2
	v_mov_b32_e32 v35, v2
	v_mov_b32_e32 v36, v2
	v_mov_b32_e32 v37, v2
	v_mov_b32_e32 v38, v2
	v_mov_b32_e32 v39, v2
	v_mov_b32_e32 v40, v2
	v_mov_b32_e32 v41, v2
	v_mov_b32_e32 v42, v2
	v_mov_b32_e32 v43, v2
	v_mov_b32_e32 v44, v2
	v_mov_b32_e32 v45, v2
	v_mov_b32_e32 v50, v2
	v_mov_b32_e32 v51, v2
	v_mov_b32_e32 v52, v2
	v_mov_b32_e32 v53, v2
	v_mov_b32_e32 v14, v2
	v_mov_b32_e32 v15, v2
	v_mov_b32_e32 v16, v2
	v_mov_b32_e32 v17, v2
	v_mov_b32_e32 v22, v2
	v_mov_b32_e32 v23, v2
	v_mov_b32_e32 v24, v2
	v_mov_b32_e32 v25, v2
	v_mov_b32_e32 v26, v2
	v_mov_b32_e32 v27, v2
	v_mov_b32_e32 v28, v2
	v_mov_b32_e32 v29, v2
	v_mov_b32_e32 v30, v2
	v_mov_b32_e32 v31, v2
	v_mov_b32_e32 v32, v2
	v_mov_b32_e32 v33, v2
	v_mov_b32_e32 v46, v2
	v_mov_b32_e32 v47, v2
	v_mov_b32_e32 v48, v2
	v_mov_b32_e32 v49, v2
	v_mov_b32_e32 v54, v2
	v_mov_b32_e32 v55, v2
	v_mov_b32_e32 v56, v2
	v_mov_b32_e32 v57, v2
	v_mov_b32_e32 v58, v2
	v_mov_b32_e32 v59, v2
	v_mov_b32_e32 v60, v2
	v_mov_b32_e32 v61, v2
	v_mov_b32_e32 v62, v2
	v_mov_b32_e32 v63, v2
	v_mov_b32_e32 v64, v2
	v_mov_b32_e32 v65, v2
	v_mov_b32_e32 v66, v2
	v_mov_b32_e32 v67, v2
	v_mov_b32_e32 v68, v2
	v_mov_b32_e32 v69, v2
	v_mov_b32_e32 v70, v2
	v_mov_b32_e32 v71, v2
	v_mov_b32_e32 v72, v2
	v_mov_b32_e32 v73, v2
	v_mov_b32_e32 v74, v2
	v_mov_b32_e32 v75, v2
	v_mov_b32_e32 v76, v2
	v_mov_b32_e32 v77, v2
	v_mov_b32_e32 v82, v2
	v_mov_b32_e32 v83, v2
	v_mov_b32_e32 v84, v2
	v_mov_b32_e32 v85, v2
	v_mov_b32_e32 v98, v2
	v_mov_b32_e32 v99, v2
	v_mov_b32_e32 v100, v2
	v_mov_b32_e32 v101, v2
	v_mov_b32_e32 v102, v2
	v_mov_b32_e32 v103, v2
	v_mov_b32_e32 v104, v2
	v_mov_b32_e32 v105, v2
	v_mov_b32_e32 v114, v2
	v_mov_b32_e32 v115, v2
	v_mov_b32_e32 v116, v2
	v_mov_b32_e32 v117, v2
	v_mov_b32_e32 v118, v2
	v_mov_b32_e32 v119, v2
	v_mov_b32_e32 v120, v2
	v_mov_b32_e32 v121, v2
	v_mov_b32_e32 v78, v2
	v_mov_b32_e32 v79, v2
	v_mov_b32_e32 v80, v2
	v_mov_b32_e32 v81, v2
	v_mov_b32_e32 v86, v2
	v_mov_b32_e32 v87, v2
	v_mov_b32_e32 v88, v2
	v_mov_b32_e32 v89, v2
	v_mov_b32_e32 v90, v2
	v_mov_b32_e32 v91, v2
	v_mov_b32_e32 v92, v2
	v_mov_b32_e32 v93, v2
	v_mov_b32_e32 v94, v2
	v_mov_b32_e32 v95, v2
	v_mov_b32_e32 v96, v2
	v_mov_b32_e32 v97, v2
	v_mov_b32_e32 v106, v2
	v_mov_b32_e32 v107, v2
	v_mov_b32_e32 v108, v2
	v_mov_b32_e32 v109, v2
	v_mov_b32_e32 v110, v2
	v_mov_b32_e32 v111, v2
	v_mov_b32_e32 v112, v2
	v_mov_b32_e32 v113, v2
	v_mov_b32_e32 v122, v2
	v_mov_b32_e32 v123, v2
	v_mov_b32_e32 v124, v2
	v_mov_b32_e32 v125, v2
	v_mov_b32_e32 v126, v2
	v_mov_b32_e32 v127, v2
	v_mov_b32_e32 v128, v2
	v_mov_b32_e32 v129, v2
	s_branch .LBB0_442

.LBB0_496:
	s_add_u32 s36, s48, s52
	s_addc_u32 s37, s49, s53
	v_or_b32_e32 v146, 0x10000, v145
	v_add_u32_e32 v150, 0x10400, v145
	v_add_u32_e32 v154, 0x10800, v145
	v_add_u32_e32 v158, 0x10c00, v145
	v_or_b32_e32 v162, 0x14000, v145
	v_add_u32_e32 v166, 0x14400, v145
	v_add_u32_e32 v170, 0x14800, v145
	v_add_u32_e32 v174, 0x14c00, v145
	s_add_u32 s36, s36, 0x100
	ds_read_b128 v[146:149], v146
	ds_read_b128 v[150:153], v150
	ds_read_b128 v[154:157], v154
	ds_read_b128 v[158:161], v158
	ds_read_b128 v[162:165], v162
	ds_read_b128 v[166:169], v166
	ds_read_b128 v[170:173], v170
	ds_read_b128 v[174:177], v174
	s_addc_u32 s37, s37, 0
	s_add_u32 s54, s92, s52
	s_addc_u32 s55, s93, s53
	s_cmpk_eq_i32 s52, 0x700
	s_cselect_b32 s57, s39, s37
	s_cselect_b32 s56, s94, s36
	s_cselect_b32 s55, s41, s55
	s_cselect_b32 s54, s95, s54
	v_lshl_add_u64 v[194:195], v[140:141], 0, s[52:53]
	s_add_i32 m0, s17, 0xc000
	ds_read_b128 v[178:181], v144
	ds_read_b128 v[182:185], v144 offset:1024
	ds_read_b128 v[186:189], v144 offset:2048
	ds_read_b128 v[190:193], v144 offset:3072
	ds_read_b128 v[200:203], v144 offset:4096
	ds_read_b128 v[204:207], v144 offset:5120
	ds_read_b128 v[208:211], v144 offset:6144
	ds_read_b128 v[212:215], v144 offset:7168
	global_load_lds_dwordx4 v[194:195], off
	v_lshl_add_u64 v[194:195], v[142:143], 0, s[52:53]
	s_add_i32 m0, s17, 0xe000
	s_nop 0
	global_load_lds_dwordx4 v[194:195], off
	s_waitcnt vmcnt(8)
	s_waitcnt lgkmcnt(0)
	s_barrier
	s_setprio 1
	v_mfma_f32_16x16x32_bf16 v[126:129], v[146:149], v[178:181], v[126:129]
	v_mfma_f32_16x16x32_bf16 v[122:125], v[154:157], v[178:181], v[122:125]
	v_mfma_f32_16x16x32_bf16 v[110:113], v[146:149], v[186:189], v[110:113]
	v_mfma_f32_16x16x32_bf16 v[106:109], v[154:157], v[186:189], v[106:109]
	v_mfma_f32_16x16x32_bf16 v[94:97], v[146:149], v[200:203], v[94:97]
	v_mfma_f32_16x16x32_bf16 v[90:93], v[154:157], v[200:203], v[90:93]
	v_mfma_f32_16x16x32_bf16 v[78:81], v[146:149], v[208:211], v[78:81]
	v_mfma_f32_16x16x32_bf16 v[74:77], v[154:157], v[208:211], v[74:77]
	v_mfma_f32_16x16x32_bf16 v[126:129], v[150:153], v[182:185], v[126:129]
	v_mfma_f32_16x16x32_bf16 v[122:125], v[158:161], v[182:185], v[122:125]
	v_mfma_f32_16x16x32_bf16 v[110:113], v[150:153], v[190:193], v[110:113]
	v_mfma_f32_16x16x32_bf16 v[106:109], v[158:161], v[190:193], v[106:109]
	v_mfma_f32_16x16x32_bf16 v[94:97], v[150:153], v[204:207], v[94:97]
	v_mfma_f32_16x16x32_bf16 v[90:93], v[158:161], v[204:207], v[90:93]
	v_mfma_f32_16x16x32_bf16 v[78:81], v[150:153], v[212:215], v[78:81]
	v_mfma_f32_16x16x32_bf16 v[74:77], v[158:161], v[212:215], v[74:77]
	v_mfma_f32_16x16x32_bf16 v[118:121], v[162:165], v[178:181], v[118:121]
	v_mfma_f32_16x16x32_bf16 v[114:117], v[170:173], v[178:181], v[114:117]
	v_mfma_f32_16x16x32_bf16 v[102:105], v[162:165], v[186:189], v[102:105]
	v_mfma_f32_16x16x32_bf16 v[98:101], v[170:173], v[186:189], v[98:101]
	v_mfma_f32_16x16x32_bf16 v[86:89], v[162:165], v[200:203], v[86:89]
	v_mfma_f32_16x16x32_bf16 v[82:85], v[170:173], v[200:203], v[82:85]
	v_mfma_f32_16x16x32_bf16 v[70:73], v[162:165], v[208:211], v[70:73]
	v_mfma_f32_16x16x32_bf16 v[66:69], v[170:173], v[208:211], v[66:69]
	v_mfma_f32_16x16x32_bf16 v[118:121], v[166:169], v[182:185], v[118:121]
	v_mfma_f32_16x16x32_bf16 v[114:117], v[174:177], v[182:185], v[114:117]
	v_mfma_f32_16x16x32_bf16 v[102:105], v[166:169], v[190:193], v[102:105]
	v_mfma_f32_16x16x32_bf16 v[98:101], v[174:177], v[190:193], v[98:101]
	v_mfma_f32_16x16x32_bf16 v[86:89], v[166:169], v[204:207], v[86:89]
	v_mfma_f32_16x16x32_bf16 v[82:85], v[174:177], v[204:207], v[82:85]
	v_mfma_f32_16x16x32_bf16 v[70:73], v[166:169], v[212:215], v[70:73]
	v_mfma_f32_16x16x32_bf16 v[66:69], v[174:177], v[212:215], v[66:69]
	s_setprio 0
	s_barrier
	s_mov_b32 m0, s60
	v_lshl_add_u64 v[194:195], s[54:55], 0, v[0:1]
	s_add_u32 s36, s54, 0x40000
	ds_read_b128 v[178:181], v144 offset:16384
	ds_read_b128 v[182:185], v144 offset:17408
	ds_read_b128 v[186:189], v144 offset:18432
	ds_read_b128 v[190:193], v144 offset:19456
	ds_read_b128 v[200:203], v144 offset:20480
	ds_read_b128 v[204:207], v144 offset:21504
	ds_read_b128 v[208:211], v144 offset:22528
	ds_read_b128 v[212:215], v144 offset:23552
	global_load_lds_dwordx4 v[194:195], off
	v_lshl_add_u64 v[216:217], s[54:55], 0, v[130:131]
	s_mov_b32 m0, s61
	s_addc_u32 s37, s55, 0
	global_load_lds_dwordx4 v[216:217], off
	v_lshl_add_u64 v[218:219], s[36:37], 0, v[0:1]
	s_mov_b32 m0, s62
	v_lshl_add_u64 v[220:221], s[56:57], 0, v[132:133]
	global_load_lds_dwordx4 v[218:219], off
	v_lshl_add_u64 v[218:219], s[36:37], 0, v[130:131]
	s_mov_b32 m0, s63
	s_nop 0
	global_load_lds_dwordx4 v[218:219], off
	v_lshl_add_u64 v[218:219], s[56:57], 0, v[134:135]
	s_mov_b32 m0, s17
	s_nop 0
	global_load_lds_dwordx4 v[218:219], off
	s_mov_b32 m0, s66
	s_nop 0
	global_load_lds_dwordx4 v[220:221], off
	s_waitcnt vmcnt(8)
	s_waitcnt lgkmcnt(0)
	s_barrier
	s_setprio 1
	v_mfma_f32_16x16x32_bf16 v[62:65], v[146:149], v[178:181], v[62:65]
	v_mfma_f32_16x16x32_bf16 v[58:61], v[154:157], v[178:181], v[58:61]
	v_mfma_f32_16x16x32_bf16 v[46:49], v[146:149], v[186:189], v[46:49]
	v_mfma_f32_16x16x32_bf16 v[42:45], v[154:157], v[186:189], v[42:45]
	v_mfma_f32_16x16x32_bf16 v[30:33], v[146:149], v[200:203], v[30:33]
	v_mfma_f32_16x16x32_bf16 v[26:29], v[154:157], v[200:203], v[26:29]
	v_mfma_f32_16x16x32_bf16 v[14:17], v[146:149], v[208:211], v[14:17]
	v_mfma_f32_16x16x32_bf16 v[10:13], v[154:157], v[208:211], v[10:13]
	v_mfma_f32_16x16x32_bf16 v[62:65], v[150:153], v[182:185], v[62:65]
	v_mfma_f32_16x16x32_bf16 v[58:61], v[158:161], v[182:185], v[58:61]
	v_mfma_f32_16x16x32_bf16 v[46:49], v[150:153], v[190:193], v[46:49]
	v_mfma_f32_16x16x32_bf16 v[42:45], v[158:161], v[190:193], v[42:45]
	v_mfma_f32_16x16x32_bf16 v[30:33], v[150:153], v[204:207], v[30:33]
	v_mfma_f32_16x16x32_bf16 v[26:29], v[158:161], v[204:207], v[26:29]
	v_mfma_f32_16x16x32_bf16 v[14:17], v[150:153], v[212:215], v[14:17]
	v_mfma_f32_16x16x32_bf16 v[10:13], v[158:161], v[212:215], v[10:13]
	v_mfma_f32_16x16x32_bf16 v[54:57], v[162:165], v[178:181], v[54:57]
	v_mfma_f32_16x16x32_bf16 v[50:53], v[170:173], v[178:181], v[50:53]
	v_mfma_f32_16x16x32_bf16 v[38:41], v[162:165], v[186:189], v[38:41]
	v_mfma_f32_16x16x32_bf16 v[34:37], v[170:173], v[186:189], v[34:37]
	v_mfma_f32_16x16x32_bf16 v[22:25], v[162:165], v[200:203], v[22:25]
	v_mfma_f32_16x16x32_bf16 v[18:21], v[170:173], v[200:203], v[18:21]
	v_mfma_f32_16x16x32_bf16 v[6:9], v[162:165], v[208:211], v[6:9]
	v_mfma_f32_16x16x32_bf16 v[2:5], v[170:173], v[208:211], v[2:5]
	v_mfma_f32_16x16x32_bf16 v[54:57], v[166:169], v[182:185], v[54:57]
	v_mfma_f32_16x16x32_bf16 v[50:53], v[174:177], v[182:185], v[50:53]
	v_mfma_f32_16x16x32_bf16 v[38:41], v[166:169], v[190:193], v[38:41]
	v_mfma_f32_16x16x32_bf16 v[34:37], v[174:177], v[190:193], v[34:37]
	v_mfma_f32_16x16x32_bf16 v[22:25], v[166:169], v[204:207], v[22:25]
	v_mfma_f32_16x16x32_bf16 v[18:21], v[174:177], v[204:207], v[18:21]
	v_mfma_f32_16x16x32_bf16 v[6:9], v[166:169], v[212:215], v[6:9]
	v_mfma_f32_16x16x32_bf16 v[2:5], v[174:177], v[212:215], v[2:5]
	s_setprio 0
	s_barrier
	v_or_b32_e32 v146, 0x18000, v145
	v_add_u32_e32 v150, 0x18400, v145
	v_add_u32_e32 v154, 0x18800, v145
	v_add_u32_e32 v158, 0x18c00, v145
	v_or_b32_e32 v162, 0x1c000, v145
	v_add_u32_e32 v166, 0x1c400, v145
	v_add_u32_e32 v170, 0x1c800, v145
	v_add_u32_e32 v174, 0x1cc00, v145
	ds_read_b128 v[146:149], v146
	ds_read_b128 v[150:153], v150
	ds_read_b128 v[154:157], v154
	ds_read_b128 v[158:161], v158
	ds_read_b128 v[162:165], v162
	ds_read_b128 v[166:169], v166
	ds_read_b128 v[170:173], v170
	ds_read_b128 v[174:177], v174
	s_add_u32 s36, s56, 0x40000
	s_addc_u32 s37, s57, 0
	s_mov_b32 m0, s67
	v_lshl_add_u64 v[222:223], s[36:37], 0, v[134:135]
	ds_read_b128 v[178:181], v144 offset:32768
	ds_read_b128 v[182:185], v144 offset:33792
	ds_read_b128 v[186:189], v144 offset:34816
	ds_read_b128 v[190:193], v144 offset:35840
	ds_read_b128 v[200:203], v144 offset:36864
	ds_read_b128 v[204:207], v144 offset:37888
	ds_read_b128 v[208:211], v144 offset:38912
	ds_read_b128 v[212:215], v144 offset:39936
	global_load_lds_dwordx4 v[222:223], off
	v_lshl_add_u64 v[222:223], s[36:37], 0, v[132:133]
	s_mov_b32 m0, s80
	s_nop 0
	global_load_lds_dwordx4 v[222:223], off
	s_waitcnt vmcnt(8)
	s_waitcnt lgkmcnt(0)
	s_barrier
	s_setprio 1
	v_mfma_f32_16x16x32_bf16 v[126:129], v[146:149], v[178:181], v[126:129]
	v_mfma_f32_16x16x32_bf16 v[122:125], v[154:157], v[178:181], v[122:125]
	v_mfma_f32_16x16x32_bf16 v[110:113], v[146:149], v[186:189], v[110:113]
	v_mfma_f32_16x16x32_bf16 v[106:109], v[154:157], v[186:189], v[106:109]
	v_mfma_f32_16x16x32_bf16 v[94:97], v[146:149], v[200:203], v[94:97]
	v_mfma_f32_16x16x32_bf16 v[90:93], v[154:157], v[200:203], v[90:93]
	v_mfma_f32_16x16x32_bf16 v[78:81], v[146:149], v[208:211], v[78:81]
	v_mfma_f32_16x16x32_bf16 v[74:77], v[154:157], v[208:211], v[74:77]
	v_mfma_f32_16x16x32_bf16 v[126:129], v[150:153], v[182:185], v[126:129]
	v_mfma_f32_16x16x32_bf16 v[122:125], v[158:161], v[182:185], v[122:125]
	v_mfma_f32_16x16x32_bf16 v[110:113], v[150:153], v[190:193], v[110:113]
	v_mfma_f32_16x16x32_bf16 v[106:109], v[158:161], v[190:193], v[106:109]
	v_mfma_f32_16x16x32_bf16 v[94:97], v[150:153], v[204:207], v[94:97]
	v_mfma_f32_16x16x32_bf16 v[90:93], v[158:161], v[204:207], v[90:93]
	v_mfma_f32_16x16x32_bf16 v[78:81], v[150:153], v[212:215], v[78:81]
	v_mfma_f32_16x16x32_bf16 v[74:77], v[158:161], v[212:215], v[74:77]
	v_mfma_f32_16x16x32_bf16 v[118:121], v[162:165], v[178:181], v[118:121]
	v_mfma_f32_16x16x32_bf16 v[114:117], v[170:173], v[178:181], v[114:117]
	v_mfma_f32_16x16x32_bf16 v[102:105], v[162:165], v[186:189], v[102:105]
	v_mfma_f32_16x16x32_bf16 v[98:101], v[170:173], v[186:189], v[98:101]
	v_mfma_f32_16x16x32_bf16 v[86:89], v[162:165], v[200:203], v[86:89]
	v_mfma_f32_16x16x32_bf16 v[82:85], v[170:173], v[200:203], v[82:85]
	v_mfma_f32_16x16x32_bf16 v[70:73], v[162:165], v[208:211], v[70:73]
	v_mfma_f32_16x16x32_bf16 v[66:69], v[170:173], v[208:211], v[66:69]
	v_mfma_f32_16x16x32_bf16 v[118:121], v[166:169], v[182:185], v[118:121]
	v_mfma_f32_16x16x32_bf16 v[114:117], v[174:177], v[182:185], v[114:117]
	v_mfma_f32_16x16x32_bf16 v[102:105], v[166:169], v[190:193], v[102:105]
	v_mfma_f32_16x16x32_bf16 v[98:101], v[174:177], v[190:193], v[98:101]
	v_mfma_f32_16x16x32_bf16 v[86:89], v[166:169], v[204:207], v[86:89]
	v_mfma_f32_16x16x32_bf16 v[82:85], v[174:177], v[204:207], v[82:85]
	v_mfma_f32_16x16x32_bf16 v[70:73], v[166:169], v[212:215], v[70:73]
	v_mfma_f32_16x16x32_bf16 v[66:69], v[174:177], v[212:215], v[66:69]
	s_setprio 0
	s_barrier
	s_mov_b32 m0, s82
	v_lshl_add_u64 v[194:195], v[194:195], 0, s[18:19]
	s_add_u32 s36, s54, 0x40080
	ds_read_b128 v[178:181], v144 offset:49152
	ds_read_b128 v[182:185], v144 offset:50176
	ds_read_b128 v[186:189], v144 offset:51200
	ds_read_b128 v[190:193], v144 offset:52224
	ds_read_b128 v[200:203], v144 offset:53248
	ds_read_b128 v[204:207], v144 offset:54272
	ds_read_b128 v[208:211], v144 offset:55296
	ds_read_b128 v[212:215], v144 offset:56320
	global_load_lds_dwordx4 v[194:195], off
	v_lshl_add_u64 v[194:195], v[216:217], 0, s[18:19]
	s_mov_b32 m0, s83
	s_addc_u32 s37, s55, 0
	global_load_lds_dwordx4 v[194:195], off
	v_lshl_add_u64 v[194:195], s[36:37], 0, v[0:1]
	s_mov_b32 m0, s88
	s_nop 0
	global_load_lds_dwordx4 v[194:195], off
	v_lshl_add_u64 v[194:195], s[36:37], 0, v[130:131]
	s_mov_b32 m0, s89
	s_nop 0
	global_load_lds_dwordx4 v[194:195], off
	v_lshl_add_u64 v[194:195], v[218:219], 0, s[18:19]
	s_mov_b32 m0, s84
	s_nop 0
	global_load_lds_dwordx4 v[194:195], off
	v_lshl_add_u64 v[194:195], v[220:221], 0, s[18:19]
	s_mov_b32 m0, s85
	s_nop 0
	global_load_lds_dwordx4 v[194:195], off
	s_waitcnt vmcnt(8)
	s_waitcnt lgkmcnt(0)
	s_barrier
	s_setprio 1
	v_mfma_f32_16x16x32_bf16 v[62:65], v[146:149], v[178:181], v[62:65]
	v_mfma_f32_16x16x32_bf16 v[58:61], v[154:157], v[178:181], v[58:61]
	v_mfma_f32_16x16x32_bf16 v[46:49], v[146:149], v[186:189], v[46:49]
	v_mfma_f32_16x16x32_bf16 v[42:45], v[154:157], v[186:189], v[42:45]
	v_mfma_f32_16x16x32_bf16 v[30:33], v[146:149], v[200:203], v[30:33]
	v_mfma_f32_16x16x32_bf16 v[26:29], v[154:157], v[200:203], v[26:29]
	v_mfma_f32_16x16x32_bf16 v[14:17], v[146:149], v[208:211], v[14:17]
	v_mfma_f32_16x16x32_bf16 v[10:13], v[154:157], v[208:211], v[10:13]
	v_mfma_f32_16x16x32_bf16 v[62:65], v[150:153], v[182:185], v[62:65]
	v_mfma_f32_16x16x32_bf16 v[58:61], v[158:161], v[182:185], v[58:61]
	v_mfma_f32_16x16x32_bf16 v[46:49], v[150:153], v[190:193], v[46:49]
	v_mfma_f32_16x16x32_bf16 v[42:45], v[158:161], v[190:193], v[42:45]
	v_mfma_f32_16x16x32_bf16 v[30:33], v[150:153], v[204:207], v[30:33]
	v_mfma_f32_16x16x32_bf16 v[26:29], v[158:161], v[204:207], v[26:29]
	v_mfma_f32_16x16x32_bf16 v[14:17], v[150:153], v[212:215], v[14:17]
	v_mfma_f32_16x16x32_bf16 v[10:13], v[158:161], v[212:215], v[10:13]
	v_mfma_f32_16x16x32_bf16 v[54:57], v[162:165], v[178:181], v[54:57]
	v_mfma_f32_16x16x32_bf16 v[50:53], v[170:173], v[178:181], v[50:53]
	v_mfma_f32_16x16x32_bf16 v[38:41], v[162:165], v[186:189], v[38:41]
	v_mfma_f32_16x16x32_bf16 v[34:37], v[170:173], v[186:189], v[34:37]
	v_mfma_f32_16x16x32_bf16 v[22:25], v[162:165], v[200:203], v[22:25]
	v_mfma_f32_16x16x32_bf16 v[18:21], v[170:173], v[200:203], v[18:21]
	v_mfma_f32_16x16x32_bf16 v[6:9], v[162:165], v[208:211], v[6:9]
	v_mfma_f32_16x16x32_bf16 v[2:5], v[170:173], v[208:211], v[2:5]
	v_mfma_f32_16x16x32_bf16 v[54:57], v[166:169], v[182:185], v[54:57]
	v_mfma_f32_16x16x32_bf16 v[50:53], v[174:177], v[182:185], v[50:53]
	v_mfma_f32_16x16x32_bf16 v[38:41], v[166:169], v[190:193], v[38:41]
	v_mfma_f32_16x16x32_bf16 v[34:37], v[174:177], v[190:193], v[34:37]
	v_mfma_f32_16x16x32_bf16 v[22:25], v[166:169], v[204:207], v[22:25]
	v_mfma_f32_16x16x32_bf16 v[18:21], v[174:177], v[204:207], v[18:21]
	v_mfma_f32_16x16x32_bf16 v[6:9], v[166:169], v[212:215], v[6:9]
	v_mfma_f32_16x16x32_bf16 v[2:5], v[174:177], v[212:215], v[2:5]
	s_setprio 0
	s_barrier
	s_add_i32 vcc_lo, vcc_lo, 2
	s_add_u32 s52, s52, 0x100
	s_addc_u32 s53, s53, 0
	s_cmp_gt_u32 vcc_lo, 13
	s_cbranch_scc0 .LBB0_496
	s_and_b64 vcc, exec, s[14:15]
	s_cbranch_vccz .LBB0_499
	s_barrier

.LBB0_535:
	s_add_u32 s0, s42, s52
	s_addc_u32 s1, s43, s53
	v_or_b32_e32 v146, 0x10000, v145
	v_add_u32_e32 v150, 0x10400, v145
	v_add_u32_e32 v154, 0x10800, v145
	v_add_u32_e32 v158, 0x10c00, v145
	v_or_b32_e32 v162, 0x14000, v145
	v_add_u32_e32 v166, 0x14400, v145
	v_add_u32_e32 v170, 0x14800, v145
	v_add_u32_e32 v174, 0x14c00, v145
	s_add_u32 s0, s0, 0x100
	ds_read_b128 v[146:149], v146
	ds_read_b128 v[150:153], v150
	ds_read_b128 v[154:157], v154
	ds_read_b128 v[158:161], v158
	ds_read_b128 v[162:165], v162
	ds_read_b128 v[166:169], v166
	ds_read_b128 v[170:173], v170
	ds_read_b128 v[174:177], v174
	s_addc_u32 s1, s1, 0
	s_add_u32 s54, s29, s52
	s_addc_u32 s55, s93, s53
	s_cmpk_eq_i32 s52, 0x700
	s_cselect_b32 s57, s39, s1
	s_cselect_b32 s56, s94, s0
	s_cselect_b32 s55, s41, s55
	s_cselect_b32 s54, s95, s54
	v_lshl_add_u64 v[194:195], v[140:141], 0, s[52:53]
	s_add_i32 m0, s37, 0xc000
	ds_read_b128 v[178:181], v144
	ds_read_b128 v[182:185], v144 offset:1024
	ds_read_b128 v[186:189], v144 offset:2048
	ds_read_b128 v[190:193], v144 offset:3072
	ds_read_b128 v[200:203], v144 offset:4096
	ds_read_b128 v[204:207], v144 offset:5120
	ds_read_b128 v[208:211], v144 offset:6144
	ds_read_b128 v[212:215], v144 offset:7168
	global_load_lds_dwordx4 v[194:195], off
	v_lshl_add_u64 v[194:195], v[142:143], 0, s[52:53]
	s_add_i32 m0, s37, 0xe000
	s_nop 0
	global_load_lds_dwordx4 v[194:195], off
	s_waitcnt vmcnt(8)
	s_waitcnt lgkmcnt(0)
	s_barrier
	s_setprio 1
	v_mfma_f32_16x16x32_bf16 v[126:129], v[146:149], v[178:181], v[126:129]
	v_mfma_f32_16x16x32_bf16 v[122:125], v[154:157], v[178:181], v[122:125]
	v_mfma_f32_16x16x32_bf16 v[110:113], v[146:149], v[186:189], v[110:113]
	v_mfma_f32_16x16x32_bf16 v[106:109], v[154:157], v[186:189], v[106:109]
	v_mfma_f32_16x16x32_bf16 v[94:97], v[146:149], v[200:203], v[94:97]
	v_mfma_f32_16x16x32_bf16 v[90:93], v[154:157], v[200:203], v[90:93]
	v_mfma_f32_16x16x32_bf16 v[78:81], v[146:149], v[208:211], v[78:81]
	v_mfma_f32_16x16x32_bf16 v[74:77], v[154:157], v[208:211], v[74:77]
	v_mfma_f32_16x16x32_bf16 v[126:129], v[150:153], v[182:185], v[126:129]
	v_mfma_f32_16x16x32_bf16 v[122:125], v[158:161], v[182:185], v[122:125]
	v_mfma_f32_16x16x32_bf16 v[110:113], v[150:153], v[190:193], v[110:113]
	v_mfma_f32_16x16x32_bf16 v[106:109], v[158:161], v[190:193], v[106:109]
	v_mfma_f32_16x16x32_bf16 v[94:97], v[150:153], v[204:207], v[94:97]
	v_mfma_f32_16x16x32_bf16 v[90:93], v[158:161], v[204:207], v[90:93]
	v_mfma_f32_16x16x32_bf16 v[78:81], v[150:153], v[212:215], v[78:81]
	v_mfma_f32_16x16x32_bf16 v[74:77], v[158:161], v[212:215], v[74:77]
	v_mfma_f32_16x16x32_bf16 v[118:121], v[162:165], v[178:181], v[118:121]
	v_mfma_f32_16x16x32_bf16 v[114:117], v[170:173], v[178:181], v[114:117]
	v_mfma_f32_16x16x32_bf16 v[102:105], v[162:165], v[186:189], v[102:105]
	v_mfma_f32_16x16x32_bf16 v[98:101], v[170:173], v[186:189], v[98:101]
	v_mfma_f32_16x16x32_bf16 v[86:89], v[162:165], v[200:203], v[86:89]
	v_mfma_f32_16x16x32_bf16 v[82:85], v[170:173], v[200:203], v[82:85]
	v_mfma_f32_16x16x32_bf16 v[70:73], v[162:165], v[208:211], v[70:73]
	v_mfma_f32_16x16x32_bf16 v[66:69], v[170:173], v[208:211], v[66:69]
	v_mfma_f32_16x16x32_bf16 v[118:121], v[166:169], v[182:185], v[118:121]
	v_mfma_f32_16x16x32_bf16 v[114:117], v[174:177], v[182:185], v[114:117]
	v_mfma_f32_16x16x32_bf16 v[102:105], v[166:169], v[190:193], v[102:105]
	v_mfma_f32_16x16x32_bf16 v[98:101], v[174:177], v[190:193], v[98:101]
	v_mfma_f32_16x16x32_bf16 v[86:89], v[166:169], v[204:207], v[86:89]
	v_mfma_f32_16x16x32_bf16 v[82:85], v[174:177], v[204:207], v[82:85]
	v_mfma_f32_16x16x32_bf16 v[70:73], v[166:169], v[212:215], v[70:73]
	v_mfma_f32_16x16x32_bf16 v[66:69], v[174:177], v[212:215], v[66:69]
	s_setprio 0
	s_barrier
	s_mov_b32 m0, s62
	v_lshl_add_u64 v[194:195], s[54:55], 0, v[0:1]
	s_add_u32 s0, s54, 0x40000
	ds_read_b128 v[178:181], v144 offset:16384
	ds_read_b128 v[182:185], v144 offset:17408
	ds_read_b128 v[186:189], v144 offset:18432
	ds_read_b128 v[190:193], v144 offset:19456
	ds_read_b128 v[200:203], v144 offset:20480
	ds_read_b128 v[204:207], v144 offset:21504
	ds_read_b128 v[208:211], v144 offset:22528
	ds_read_b128 v[212:215], v144 offset:23552
	global_load_lds_dwordx4 v[194:195], off
	v_lshl_add_u64 v[216:217], s[54:55], 0, v[130:131]
	s_mov_b32 m0, s63
	s_addc_u32 s1, s55, 0
	global_load_lds_dwordx4 v[216:217], off
	v_lshl_add_u64 v[218:219], s[0:1], 0, v[0:1]
	s_mov_b32 m0, s64
	v_lshl_add_u64 v[220:221], s[56:57], 0, v[132:133]
	global_load_lds_dwordx4 v[218:219], off
	v_lshl_add_u64 v[218:219], s[0:1], 0, v[130:131]
	s_mov_b32 m0, s65
	s_nop 0
	global_load_lds_dwordx4 v[218:219], off
	v_lshl_add_u64 v[218:219], s[56:57], 0, v[134:135]
	s_mov_b32 m0, s37
	s_nop 0
	global_load_lds_dwordx4 v[218:219], off
	s_mov_b32 m0, s66
	s_nop 0
	global_load_lds_dwordx4 v[220:221], off
	s_waitcnt vmcnt(8)
	s_waitcnt lgkmcnt(0)
	s_barrier
	s_setprio 1
	v_mfma_f32_16x16x32_bf16 v[62:65], v[146:149], v[178:181], v[62:65]
	v_mfma_f32_16x16x32_bf16 v[58:61], v[154:157], v[178:181], v[58:61]
	v_mfma_f32_16x16x32_bf16 v[46:49], v[146:149], v[186:189], v[46:49]
	v_mfma_f32_16x16x32_bf16 v[42:45], v[154:157], v[186:189], v[42:45]
	v_mfma_f32_16x16x32_bf16 v[30:33], v[146:149], v[200:203], v[30:33]
	v_mfma_f32_16x16x32_bf16 v[26:29], v[154:157], v[200:203], v[26:29]
	v_mfma_f32_16x16x32_bf16 v[14:17], v[146:149], v[208:211], v[14:17]
	v_mfma_f32_16x16x32_bf16 v[10:13], v[154:157], v[208:211], v[10:13]
	v_mfma_f32_16x16x32_bf16 v[62:65], v[150:153], v[182:185], v[62:65]
	v_mfma_f32_16x16x32_bf16 v[58:61], v[158:161], v[182:185], v[58:61]
	v_mfma_f32_16x16x32_bf16 v[46:49], v[150:153], v[190:193], v[46:49]
	v_mfma_f32_16x16x32_bf16 v[42:45], v[158:161], v[190:193], v[42:45]
	v_mfma_f32_16x16x32_bf16 v[30:33], v[150:153], v[204:207], v[30:33]
	v_mfma_f32_16x16x32_bf16 v[26:29], v[158:161], v[204:207], v[26:29]
	v_mfma_f32_16x16x32_bf16 v[14:17], v[150:153], v[212:215], v[14:17]
	v_mfma_f32_16x16x32_bf16 v[10:13], v[158:161], v[212:215], v[10:13]
	v_mfma_f32_16x16x32_bf16 v[54:57], v[162:165], v[178:181], v[54:57]
	v_mfma_f32_16x16x32_bf16 v[50:53], v[170:173], v[178:181], v[50:53]
	v_mfma_f32_16x16x32_bf16 v[38:41], v[162:165], v[186:189], v[38:41]
	v_mfma_f32_16x16x32_bf16 v[34:37], v[170:173], v[186:189], v[34:37]
	v_mfma_f32_16x16x32_bf16 v[22:25], v[162:165], v[200:203], v[22:25]
	v_mfma_f32_16x16x32_bf16 v[18:21], v[170:173], v[200:203], v[18:21]
	v_mfma_f32_16x16x32_bf16 v[6:9], v[162:165], v[208:211], v[6:9]
	v_mfma_f32_16x16x32_bf16 v[2:5], v[170:173], v[208:211], v[2:5]
	v_mfma_f32_16x16x32_bf16 v[54:57], v[166:169], v[182:185], v[54:57]
	v_mfma_f32_16x16x32_bf16 v[50:53], v[174:177], v[182:185], v[50:53]
	v_mfma_f32_16x16x32_bf16 v[38:41], v[166:169], v[190:193], v[38:41]
	v_mfma_f32_16x16x32_bf16 v[34:37], v[174:177], v[190:193], v[34:37]
	v_mfma_f32_16x16x32_bf16 v[22:25], v[166:169], v[204:207], v[22:25]
	v_mfma_f32_16x16x32_bf16 v[18:21], v[174:177], v[204:207], v[18:21]
	v_mfma_f32_16x16x32_bf16 v[6:9], v[166:169], v[212:215], v[6:9]
	v_mfma_f32_16x16x32_bf16 v[2:5], v[174:177], v[212:215], v[2:5]
	s_setprio 0
	s_barrier
	v_or_b32_e32 v146, 0x18000, v145
	v_add_u32_e32 v150, 0x18400, v145
	v_add_u32_e32 v154, 0x18800, v145
	v_add_u32_e32 v158, 0x18c00, v145
	v_or_b32_e32 v162, 0x1c000, v145
	v_add_u32_e32 v166, 0x1c400, v145
	v_add_u32_e32 v170, 0x1c800, v145
	v_add_u32_e32 v174, 0x1cc00, v145
	ds_read_b128 v[146:149], v146
	ds_read_b128 v[150:153], v150
	ds_read_b128 v[154:157], v154
	ds_read_b128 v[158:161], v158
	ds_read_b128 v[162:165], v162
	ds_read_b128 v[166:169], v166
	ds_read_b128 v[170:173], v170
	ds_read_b128 v[174:177], v174
	s_add_u32 s0, s56, 0x40000
	s_addc_u32 s1, s57, 0
	s_mov_b32 m0, s67
	v_lshl_add_u64 v[222:223], s[0:1], 0, v[134:135]
	ds_read_b128 v[178:181], v144 offset:32768
	ds_read_b128 v[182:185], v144 offset:33792
	ds_read_b128 v[186:189], v144 offset:34816
	ds_read_b128 v[190:193], v144 offset:35840
	ds_read_b128 v[200:203], v144 offset:36864
	ds_read_b128 v[204:207], v144 offset:37888
	ds_read_b128 v[208:211], v144 offset:38912
	ds_read_b128 v[212:215], v144 offset:39936
	global_load_lds_dwordx4 v[222:223], off
	v_lshl_add_u64 v[222:223], s[0:1], 0, v[132:133]
	s_mov_b32 m0, s80
	s_nop 0
	global_load_lds_dwordx4 v[222:223], off
	s_waitcnt vmcnt(8)
	s_waitcnt lgkmcnt(0)
	s_barrier
	s_setprio 1
	v_mfma_f32_16x16x32_bf16 v[126:129], v[146:149], v[178:181], v[126:129]
	v_mfma_f32_16x16x32_bf16 v[122:125], v[154:157], v[178:181], v[122:125]
	v_mfma_f32_16x16x32_bf16 v[110:113], v[146:149], v[186:189], v[110:113]
	v_mfma_f32_16x16x32_bf16 v[106:109], v[154:157], v[186:189], v[106:109]
	v_mfma_f32_16x16x32_bf16 v[94:97], v[146:149], v[200:203], v[94:97]
	v_mfma_f32_16x16x32_bf16 v[90:93], v[154:157], v[200:203], v[90:93]
	v_mfma_f32_16x16x32_bf16 v[78:81], v[146:149], v[208:211], v[78:81]
	v_mfma_f32_16x16x32_bf16 v[74:77], v[154:157], v[208:211], v[74:77]
	v_mfma_f32_16x16x32_bf16 v[126:129], v[150:153], v[182:185], v[126:129]
	v_mfma_f32_16x16x32_bf16 v[122:125], v[158:161], v[182:185], v[122:125]
	v_mfma_f32_16x16x32_bf16 v[110:113], v[150:153], v[190:193], v[110:113]
	v_mfma_f32_16x16x32_bf16 v[106:109], v[158:161], v[190:193], v[106:109]
	v_mfma_f32_16x16x32_bf16 v[94:97], v[150:153], v[204:207], v[94:97]
	v_mfma_f32_16x16x32_bf16 v[90:93], v[158:161], v[204:207], v[90:93]
	v_mfma_f32_16x16x32_bf16 v[78:81], v[150:153], v[212:215], v[78:81]
	v_mfma_f32_16x16x32_bf16 v[74:77], v[158:161], v[212:215], v[74:77]
	v_mfma_f32_16x16x32_bf16 v[118:121], v[162:165], v[178:181], v[118:121]
	v_mfma_f32_16x16x32_bf16 v[114:117], v[170:173], v[178:181], v[114:117]
	v_mfma_f32_16x16x32_bf16 v[102:105], v[162:165], v[186:189], v[102:105]
	v_mfma_f32_16x16x32_bf16 v[98:101], v[170:173], v[186:189], v[98:101]
	v_mfma_f32_16x16x32_bf16 v[86:89], v[162:165], v[200:203], v[86:89]
	v_mfma_f32_16x16x32_bf16 v[82:85], v[170:173], v[200:203], v[82:85]
	v_mfma_f32_16x16x32_bf16 v[70:73], v[162:165], v[208:211], v[70:73]
	v_mfma_f32_16x16x32_bf16 v[66:69], v[170:173], v[208:211], v[66:69]
	v_mfma_f32_16x16x32_bf16 v[118:121], v[166:169], v[182:185], v[118:121]
	v_mfma_f32_16x16x32_bf16 v[114:117], v[174:177], v[182:185], v[114:117]
	v_mfma_f32_16x16x32_bf16 v[102:105], v[166:169], v[190:193], v[102:105]
	v_mfma_f32_16x16x32_bf16 v[98:101], v[174:177], v[190:193], v[98:101]
	v_mfma_f32_16x16x32_bf16 v[86:89], v[166:169], v[204:207], v[86:89]
	v_mfma_f32_16x16x32_bf16 v[82:85], v[174:177], v[204:207], v[82:85]
	v_mfma_f32_16x16x32_bf16 v[70:73], v[166:169], v[212:215], v[70:73]
	v_mfma_f32_16x16x32_bf16 v[66:69], v[174:177], v[212:215], v[66:69]
	s_setprio 0
	s_barrier
	s_mov_b32 m0, s82
	v_lshl_add_u64 v[194:195], v[194:195], 0, s[18:19]
	s_add_u32 s0, s54, 0x40080
	ds_read_b128 v[178:181], v144 offset:49152
	ds_read_b128 v[182:185], v144 offset:50176
	ds_read_b128 v[186:189], v144 offset:51200
	ds_read_b128 v[190:193], v144 offset:52224
	ds_read_b128 v[200:203], v144 offset:53248
	ds_read_b128 v[204:207], v144 offset:54272
	ds_read_b128 v[208:211], v144 offset:55296
	ds_read_b128 v[212:215], v144 offset:56320
	global_load_lds_dwordx4 v[194:195], off
	v_lshl_add_u64 v[194:195], v[216:217], 0, s[18:19]
	s_mov_b32 m0, s83
	s_addc_u32 s1, s55, 0
	global_load_lds_dwordx4 v[194:195], off
	v_lshl_add_u64 v[194:195], s[0:1], 0, v[0:1]
	s_mov_b32 m0, s88
	s_nop 0
	global_load_lds_dwordx4 v[194:195], off
	v_lshl_add_u64 v[194:195], s[0:1], 0, v[130:131]
	s_mov_b32 m0, s89
	s_nop 0
	global_load_lds_dwordx4 v[194:195], off
	v_lshl_add_u64 v[194:195], v[218:219], 0, s[18:19]
	s_mov_b32 m0, s84
	s_nop 0
	global_load_lds_dwordx4 v[194:195], off
	v_lshl_add_u64 v[194:195], v[220:221], 0, s[18:19]
	s_mov_b32 m0, s85
	s_nop 0
	global_load_lds_dwordx4 v[194:195], off
	s_waitcnt vmcnt(8)
	s_waitcnt lgkmcnt(0)
	s_barrier
	s_setprio 1
	v_mfma_f32_16x16x32_bf16 v[62:65], v[146:149], v[178:181], v[62:65]
	v_mfma_f32_16x16x32_bf16 v[58:61], v[154:157], v[178:181], v[58:61]
	v_mfma_f32_16x16x32_bf16 v[46:49], v[146:149], v[186:189], v[46:49]
	v_mfma_f32_16x16x32_bf16 v[42:45], v[154:157], v[186:189], v[42:45]
	v_mfma_f32_16x16x32_bf16 v[30:33], v[146:149], v[200:203], v[30:33]
	v_mfma_f32_16x16x32_bf16 v[26:29], v[154:157], v[200:203], v[26:29]
	v_mfma_f32_16x16x32_bf16 v[14:17], v[146:149], v[208:211], v[14:17]
	v_mfma_f32_16x16x32_bf16 v[10:13], v[154:157], v[208:211], v[10:13]
	v_mfma_f32_16x16x32_bf16 v[62:65], v[150:153], v[182:185], v[62:65]
	v_mfma_f32_16x16x32_bf16 v[58:61], v[158:161], v[182:185], v[58:61]
	v_mfma_f32_16x16x32_bf16 v[46:49], v[150:153], v[190:193], v[46:49]
	v_mfma_f32_16x16x32_bf16 v[42:45], v[158:161], v[190:193], v[42:45]
	v_mfma_f32_16x16x32_bf16 v[30:33], v[150:153], v[204:207], v[30:33]
	v_mfma_f32_16x16x32_bf16 v[26:29], v[158:161], v[204:207], v[26:29]
	v_mfma_f32_16x16x32_bf16 v[14:17], v[150:153], v[212:215], v[14:17]
	v_mfma_f32_16x16x32_bf16 v[10:13], v[158:161], v[212:215], v[10:13]
	v_mfma_f32_16x16x32_bf16 v[54:57], v[162:165], v[178:181], v[54:57]
	v_mfma_f32_16x16x32_bf16 v[50:53], v[170:173], v[178:181], v[50:53]
	v_mfma_f32_16x16x32_bf16 v[38:41], v[162:165], v[186:189], v[38:41]
	v_mfma_f32_16x16x32_bf16 v[34:37], v[170:173], v[186:189], v[34:37]
	v_mfma_f32_16x16x32_bf16 v[22:25], v[162:165], v[200:203], v[22:25]
	v_mfma_f32_16x16x32_bf16 v[18:21], v[170:173], v[200:203], v[18:21]
	v_mfma_f32_16x16x32_bf16 v[6:9], v[162:165], v[208:211], v[6:9]
	v_mfma_f32_16x16x32_bf16 v[2:5], v[170:173], v[208:211], v[2:5]
	v_mfma_f32_16x16x32_bf16 v[54:57], v[166:169], v[182:185], v[54:57]
	v_mfma_f32_16x16x32_bf16 v[50:53], v[174:177], v[182:185], v[50:53]
	v_mfma_f32_16x16x32_bf16 v[38:41], v[166:169], v[190:193], v[38:41]
	v_mfma_f32_16x16x32_bf16 v[34:37], v[174:177], v[190:193], v[34:37]
	v_mfma_f32_16x16x32_bf16 v[22:25], v[166:169], v[204:207], v[22:25]
	v_mfma_f32_16x16x32_bf16 v[18:21], v[174:177], v[204:207], v[18:21]
	v_mfma_f32_16x16x32_bf16 v[6:9], v[166:169], v[212:215], v[6:9]
	v_mfma_f32_16x16x32_bf16 v[2:5], v[174:177], v[212:215], v[2:5]
	s_setprio 0
	s_barrier
	s_add_i32 vcc_lo, vcc_lo, 2
	s_add_u32 s52, s52, 0x100
	s_addc_u32 s53, s53, 0
	s_cmp_gt_u32 vcc_lo, 13
	s_cbranch_scc0 .LBB0_535
	s_and_b64 vcc, exec, s[16:17]
	s_cbranch_vccz .LBB0_538
	s_barrier

.LBB0_851:
	v_or_b32_e32 v0, 0x10000, v237
	v_add_u32_e32 v134, 0x10400, v237
	ds_read_b128 v[130:133], v0
	ds_read_b128 v[134:137], v134
	v_add_u32_e32 v0, 0x10800, v237
	v_add_u32_e32 v142, 0x10c00, v237
	ds_read_b128 v[138:141], v0
	ds_read_b128 v[142:145], v142
	v_or_b32_e32 v0, 0x14000, v237
	v_add_u32_e32 v150, 0x14400, v237
	ds_read_b128 v[146:149], v0
	ds_read_b128 v[150:153], v150
	v_add_u32_e32 v0, 0x14800, v237
	v_add_u32_e32 v158, 0x14c00, v237
	ds_read_b128 v[154:157], v0
	ds_read_b128 v[158:161], v158
	s_add_u32 s43, s54, 0xfffe0080
	s_addc_u32 s45, s55, -1
	s_cmp_eq_u32 s41, 4
	s_cselect_b32 s59, s49, s45
	s_cselect_b32 s58, s48, s43
	s_cselect_b32 s57, s51, s39
	s_cselect_b32 s56, s50, s29
	v_lshl_add_u64 v[210:211], s[54:55], 0, v[206:207]
	s_add_i32 m0, s61, 0xc000
	ds_read_b128 v[162:165], v236
	ds_read_b128 v[166:169], v236 offset:1024
	ds_read_b128 v[170:173], v236 offset:2048
	ds_read_b128 v[174:177], v236 offset:3072
	ds_read_b128 v[178:181], v236 offset:4096
	ds_read_b128 v[182:185], v236 offset:5120
	ds_read_b128 v[186:189], v236 offset:6144
	ds_read_b128 v[190:193], v236 offset:7168
	global_load_lds_dwordx4 v[210:211], off
	v_lshl_add_u64 v[210:211], s[54:55], 0, v[208:209]
	s_add_i32 m0, s61, 0xe000
	s_nop 0
	global_load_lds_dwordx4 v[210:211], off
	s_waitcnt vmcnt(8)
	s_waitcnt lgkmcnt(0)
	s_barrier
	s_setprio 1
	v_mfma_f32_16x16x32_bf16 v[126:129], v[130:133], v[162:165], v[126:129]
	v_mfma_f32_16x16x32_bf16 v[122:125], v[138:141], v[162:165], v[122:125]
	v_mfma_f32_16x16x32_bf16 v[118:121], v[130:133], v[170:173], v[118:121]
	v_mfma_f32_16x16x32_bf16 v[114:117], v[138:141], v[170:173], v[114:117]
	v_mfma_f32_16x16x32_bf16 v[110:113], v[130:133], v[178:181], v[110:113]
	v_mfma_f32_16x16x32_bf16 v[106:109], v[138:141], v[178:181], v[106:109]
	v_mfma_f32_16x16x32_bf16 v[102:105], v[130:133], v[186:189], v[102:105]
	v_mfma_f32_16x16x32_bf16 v[98:101], v[138:141], v[186:189], v[98:101]
	v_mfma_f32_16x16x32_bf16 v[126:129], v[134:137], v[166:169], v[126:129]
	v_mfma_f32_16x16x32_bf16 v[122:125], v[142:145], v[166:169], v[122:125]
	v_mfma_f32_16x16x32_bf16 v[118:121], v[134:137], v[174:177], v[118:121]
	v_mfma_f32_16x16x32_bf16 v[114:117], v[142:145], v[174:177], v[114:117]
	v_mfma_f32_16x16x32_bf16 v[110:113], v[134:137], v[182:185], v[110:113]
	v_mfma_f32_16x16x32_bf16 v[106:109], v[142:145], v[182:185], v[106:109]
	v_mfma_f32_16x16x32_bf16 v[102:105], v[134:137], v[190:193], v[102:105]
	v_mfma_f32_16x16x32_bf16 v[98:101], v[142:145], v[190:193], v[98:101]
	v_mfma_f32_16x16x32_bf16 v[94:97], v[146:149], v[162:165], v[94:97]
	v_mfma_f32_16x16x32_bf16 v[90:93], v[154:157], v[162:165], v[90:93]
	v_mfma_f32_16x16x32_bf16 v[86:89], v[146:149], v[170:173], v[86:89]
	v_mfma_f32_16x16x32_bf16 v[82:85], v[154:157], v[170:173], v[82:85]
	v_mfma_f32_16x16x32_bf16 v[78:81], v[146:149], v[178:181], v[78:81]
	v_mfma_f32_16x16x32_bf16 v[74:77], v[154:157], v[178:181], v[74:77]
	v_mfma_f32_16x16x32_bf16 v[70:73], v[146:149], v[186:189], v[70:73]
	v_mfma_f32_16x16x32_bf16 v[66:69], v[154:157], v[186:189], v[66:69]
	v_mfma_f32_16x16x32_bf16 v[94:97], v[150:153], v[166:169], v[94:97]
	v_mfma_f32_16x16x32_bf16 v[90:93], v[158:161], v[166:169], v[90:93]
	v_mfma_f32_16x16x32_bf16 v[86:89], v[150:153], v[174:177], v[86:89]
	v_mfma_f32_16x16x32_bf16 v[82:85], v[158:161], v[174:177], v[82:85]
	v_mfma_f32_16x16x32_bf16 v[78:81], v[150:153], v[182:185], v[78:81]
	v_mfma_f32_16x16x32_bf16 v[74:77], v[158:161], v[182:185], v[74:77]
	v_mfma_f32_16x16x32_bf16 v[70:73], v[150:153], v[190:193], v[70:73]
	v_mfma_f32_16x16x32_bf16 v[66:69], v[158:161], v[190:193], v[66:69]
	s_setprio 0
	s_barrier
	s_mov_b32 m0, s62
	v_lshl_add_u64 v[210:211], s[56:57], 0, v[200:201]
	s_add_u32 vcc_lo, s56, 0x20000
	ds_read_b128 v[162:165], v236 offset:16384
	ds_read_b128 v[166:169], v236 offset:17408
	ds_read_b128 v[170:173], v236 offset:18432
	ds_read_b128 v[174:177], v236 offset:19456
	ds_read_b128 v[178:181], v236 offset:20480
	ds_read_b128 v[182:185], v236 offset:21504
	ds_read_b128 v[186:189], v236 offset:22528
	ds_read_b128 v[190:193], v236 offset:23552
	global_load_lds_dwordx4 v[210:211], off
	v_lshl_add_u64 v[212:213], s[56:57], 0, v[204:205]
	s_mov_b32 m0, s63
	s_addc_u32 vcc_hi, s57, 0
	global_load_lds_dwordx4 v[212:213], off
	v_lshl_add_u64 v[214:215], vcc, 0, v[200:201]
	s_mov_b32 m0, s64
	v_lshl_add_u64 v[216:217], s[58:59], 0, v[202:203]
	global_load_lds_dwordx4 v[214:215], off
	v_lshl_add_u64 v[214:215], vcc, 0, v[204:205]
	s_mov_b32 m0, s65
	s_nop 0
	global_load_lds_dwordx4 v[214:215], off
	v_lshl_add_u64 v[214:215], s[58:59], 0, v[194:195]
	s_mov_b32 m0, s61
	s_nop 0
	global_load_lds_dwordx4 v[214:215], off
	s_mov_b32 m0, s66
	s_nop 0
	global_load_lds_dwordx4 v[216:217], off
	s_waitcnt vmcnt(8)
	s_waitcnt lgkmcnt(0)
	s_barrier
	s_setprio 1
	v_mfma_f32_16x16x32_bf16 v[62:65], v[130:133], v[162:165], v[62:65]
	v_mfma_f32_16x16x32_bf16 v[58:61], v[138:141], v[162:165], v[58:61]
	v_mfma_f32_16x16x32_bf16 v[54:57], v[130:133], v[170:173], v[54:57]
	v_mfma_f32_16x16x32_bf16 v[50:53], v[138:141], v[170:173], v[50:53]
	v_mfma_f32_16x16x32_bf16 v[46:49], v[130:133], v[178:181], v[46:49]
	v_mfma_f32_16x16x32_bf16 v[42:45], v[138:141], v[178:181], v[42:45]
	v_mfma_f32_16x16x32_bf16 v[38:41], v[130:133], v[186:189], v[38:41]
	v_mfma_f32_16x16x32_bf16 v[34:37], v[138:141], v[186:189], v[34:37]
	v_mfma_f32_16x16x32_bf16 v[62:65], v[134:137], v[166:169], v[62:65]
	v_mfma_f32_16x16x32_bf16 v[58:61], v[142:145], v[166:169], v[58:61]
	v_mfma_f32_16x16x32_bf16 v[54:57], v[134:137], v[174:177], v[54:57]
	v_mfma_f32_16x16x32_bf16 v[50:53], v[142:145], v[174:177], v[50:53]
	v_mfma_f32_16x16x32_bf16 v[46:49], v[134:137], v[182:185], v[46:49]
	v_mfma_f32_16x16x32_bf16 v[42:45], v[142:145], v[182:185], v[42:45]
	v_mfma_f32_16x16x32_bf16 v[38:41], v[134:137], v[190:193], v[38:41]
	v_mfma_f32_16x16x32_bf16 v[34:37], v[142:145], v[190:193], v[34:37]
	v_mfma_f32_16x16x32_bf16 v[30:33], v[146:149], v[162:165], v[30:33]
	v_mfma_f32_16x16x32_bf16 v[26:29], v[154:157], v[162:165], v[26:29]
	v_mfma_f32_16x16x32_bf16 v[22:25], v[146:149], v[170:173], v[22:25]
	v_mfma_f32_16x16x32_bf16 v[18:21], v[154:157], v[170:173], v[18:21]
	v_mfma_f32_16x16x32_bf16 v[14:17], v[146:149], v[178:181], v[14:17]
	v_mfma_f32_16x16x32_bf16 v[10:13], v[154:157], v[178:181], v[10:13]
	v_mfma_f32_16x16x32_bf16 v[6:9], v[146:149], v[186:189], v[6:9]
	v_mfma_f32_16x16x32_bf16 v[2:5], v[154:157], v[186:189], v[2:5]
	v_mfma_f32_16x16x32_bf16 v[30:33], v[150:153], v[166:169], v[30:33]
	v_mfma_f32_16x16x32_bf16 v[26:29], v[158:161], v[166:169], v[26:29]
	v_mfma_f32_16x16x32_bf16 v[22:25], v[150:153], v[174:177], v[22:25]
	v_mfma_f32_16x16x32_bf16 v[18:21], v[158:161], v[174:177], v[18:21]
	v_mfma_f32_16x16x32_bf16 v[14:17], v[150:153], v[182:185], v[14:17]
	v_mfma_f32_16x16x32_bf16 v[10:13], v[158:161], v[182:185], v[10:13]
	v_mfma_f32_16x16x32_bf16 v[6:9], v[150:153], v[190:193], v[6:9]
	v_mfma_f32_16x16x32_bf16 v[2:5], v[158:161], v[190:193], v[2:5]
	s_setprio 0
	s_barrier
	v_or_b32_e32 v0, 0x18000, v237
	v_add_u32_e32 v134, 0x18400, v237
	ds_read_b128 v[130:133], v0
	ds_read_b128 v[134:137], v134
	v_add_u32_e32 v0, 0x18800, v237
	v_add_u32_e32 v142, 0x18c00, v237
	ds_read_b128 v[138:141], v0
	ds_read_b128 v[142:145], v142
	v_or_b32_e32 v0, 0x1c000, v237
	v_add_u32_e32 v150, 0x1c400, v237
	ds_read_b128 v[146:149], v0
	ds_read_b128 v[150:153], v150
	v_add_u32_e32 v0, 0x1c800, v237
	v_add_u32_e32 v158, 0x1cc00, v237
	ds_read_b128 v[154:157], v0
	ds_read_b128 v[158:161], v158
	s_add_u32 s58, s58, 0x20000
	s_addc_u32 s59, s59, 0
	s_mov_b32 m0, s67
	v_lshl_add_u64 v[218:219], s[58:59], 0, v[194:195]
	ds_read_b128 v[162:165], v236 offset:32768
	ds_read_b128 v[166:169], v236 offset:33792
	ds_read_b128 v[170:173], v236 offset:34816
	ds_read_b128 v[174:177], v236 offset:35840
	ds_read_b128 v[178:181], v236 offset:36864
	ds_read_b128 v[182:185], v236 offset:37888
	ds_read_b128 v[186:189], v236 offset:38912
	ds_read_b128 v[190:193], v236 offset:39936
	global_load_lds_dwordx4 v[218:219], off
	v_lshl_add_u64 v[218:219], s[58:59], 0, v[202:203]
	s_mov_b32 m0, s82
	s_nop 0
	global_load_lds_dwordx4 v[218:219], off
	s_waitcnt vmcnt(8)
	s_waitcnt lgkmcnt(0)
	s_barrier
	s_setprio 1
	v_mfma_f32_16x16x32_bf16 v[126:129], v[130:133], v[162:165], v[126:129]
	v_mfma_f32_16x16x32_bf16 v[122:125], v[138:141], v[162:165], v[122:125]
	v_mfma_f32_16x16x32_bf16 v[118:121], v[130:133], v[170:173], v[118:121]
	v_mfma_f32_16x16x32_bf16 v[114:117], v[138:141], v[170:173], v[114:117]
	v_mfma_f32_16x16x32_bf16 v[110:113], v[130:133], v[178:181], v[110:113]
	v_mfma_f32_16x16x32_bf16 v[106:109], v[138:141], v[178:181], v[106:109]
	v_mfma_f32_16x16x32_bf16 v[102:105], v[130:133], v[186:189], v[102:105]
	v_mfma_f32_16x16x32_bf16 v[98:101], v[138:141], v[186:189], v[98:101]
	v_mfma_f32_16x16x32_bf16 v[126:129], v[134:137], v[166:169], v[126:129]
	v_mfma_f32_16x16x32_bf16 v[122:125], v[142:145], v[166:169], v[122:125]
	v_mfma_f32_16x16x32_bf16 v[118:121], v[134:137], v[174:177], v[118:121]
	v_mfma_f32_16x16x32_bf16 v[114:117], v[142:145], v[174:177], v[114:117]
	v_mfma_f32_16x16x32_bf16 v[110:113], v[134:137], v[182:185], v[110:113]
	v_mfma_f32_16x16x32_bf16 v[106:109], v[142:145], v[182:185], v[106:109]
	v_mfma_f32_16x16x32_bf16 v[102:105], v[134:137], v[190:193], v[102:105]
	v_mfma_f32_16x16x32_bf16 v[98:101], v[142:145], v[190:193], v[98:101]
	v_mfma_f32_16x16x32_bf16 v[94:97], v[146:149], v[162:165], v[94:97]
	v_mfma_f32_16x16x32_bf16 v[90:93], v[154:157], v[162:165], v[90:93]
	v_mfma_f32_16x16x32_bf16 v[86:89], v[146:149], v[170:173], v[86:89]
	v_mfma_f32_16x16x32_bf16 v[82:85], v[154:157], v[170:173], v[82:85]
	v_mfma_f32_16x16x32_bf16 v[78:81], v[146:149], v[178:181], v[78:81]
	v_mfma_f32_16x16x32_bf16 v[74:77], v[154:157], v[178:181], v[74:77]
	v_mfma_f32_16x16x32_bf16 v[70:73], v[146:149], v[186:189], v[70:73]
	v_mfma_f32_16x16x32_bf16 v[66:69], v[154:157], v[186:189], v[66:69]
	v_mfma_f32_16x16x32_bf16 v[94:97], v[150:153], v[166:169], v[94:97]
	v_mfma_f32_16x16x32_bf16 v[90:93], v[158:161], v[166:169], v[90:93]
	v_mfma_f32_16x16x32_bf16 v[86:89], v[150:153], v[174:177], v[86:89]
	v_mfma_f32_16x16x32_bf16 v[82:85], v[158:161], v[174:177], v[82:85]
	v_mfma_f32_16x16x32_bf16 v[78:81], v[150:153], v[182:185], v[78:81]
	v_mfma_f32_16x16x32_bf16 v[74:77], v[158:161], v[182:185], v[74:77]
	v_mfma_f32_16x16x32_bf16 v[70:73], v[150:153], v[190:193], v[70:73]
	v_mfma_f32_16x16x32_bf16 v[66:69], v[158:161], v[190:193], v[66:69]
	s_setprio 0
	s_barrier
	s_mov_b32 m0, s88
	v_lshl_add_u64 v[210:211], v[210:211], 0, s[18:19]
	s_add_u32 s56, s56, 0x20080
	ds_read_b128 v[162:165], v236 offset:49152
	ds_read_b128 v[166:169], v236 offset:50176
	ds_read_b128 v[170:173], v236 offset:51200
	ds_read_b128 v[174:177], v236 offset:52224
	ds_read_b128 v[178:181], v236 offset:53248
	ds_read_b128 v[182:185], v236 offset:54272
	ds_read_b128 v[186:189], v236 offset:55296
	ds_read_b128 v[190:193], v236 offset:56320
	global_load_lds_dwordx4 v[210:211], off
	v_lshl_add_u64 v[210:211], v[212:213], 0, s[18:19]
	s_mov_b32 m0, s89
	s_addc_u32 s57, s57, 0
	global_load_lds_dwordx4 v[210:211], off
	v_lshl_add_u64 v[210:211], s[56:57], 0, v[200:201]
	s_mov_b32 m0, s92
	s_nop 0
	global_load_lds_dwordx4 v[210:211], off
	v_lshl_add_u64 v[210:211], s[56:57], 0, v[204:205]
	s_mov_b32 m0, s93
	s_nop 0
	global_load_lds_dwordx4 v[210:211], off
	v_lshl_add_u64 v[210:211], v[214:215], 0, s[18:19]
	s_mov_b32 m0, s90
	s_nop 0
	global_load_lds_dwordx4 v[210:211], off
	v_lshl_add_u64 v[210:211], v[216:217], 0, s[18:19]
	s_mov_b32 m0, s91
	s_nop 0
	global_load_lds_dwordx4 v[210:211], off
	s_waitcnt vmcnt(8)
	s_waitcnt lgkmcnt(0)
	s_barrier
	s_setprio 1
	v_mfma_f32_16x16x32_bf16 v[62:65], v[130:133], v[162:165], v[62:65]
	v_mfma_f32_16x16x32_bf16 v[58:61], v[138:141], v[162:165], v[58:61]
	v_mfma_f32_16x16x32_bf16 v[54:57], v[130:133], v[170:173], v[54:57]
	v_mfma_f32_16x16x32_bf16 v[50:53], v[138:141], v[170:173], v[50:53]
	v_mfma_f32_16x16x32_bf16 v[46:49], v[130:133], v[178:181], v[46:49]
	v_mfma_f32_16x16x32_bf16 v[42:45], v[138:141], v[178:181], v[42:45]
	v_mfma_f32_16x16x32_bf16 v[38:41], v[130:133], v[186:189], v[38:41]
	v_mfma_f32_16x16x32_bf16 v[34:37], v[138:141], v[186:189], v[34:37]
	v_mfma_f32_16x16x32_bf16 v[62:65], v[134:137], v[166:169], v[62:65]
	v_mfma_f32_16x16x32_bf16 v[58:61], v[142:145], v[166:169], v[58:61]
	v_mfma_f32_16x16x32_bf16 v[54:57], v[134:137], v[174:177], v[54:57]
	v_mfma_f32_16x16x32_bf16 v[50:53], v[142:145], v[174:177], v[50:53]
	v_mfma_f32_16x16x32_bf16 v[46:49], v[134:137], v[182:185], v[46:49]
	v_mfma_f32_16x16x32_bf16 v[42:45], v[142:145], v[182:185], v[42:45]
	v_mfma_f32_16x16x32_bf16 v[38:41], v[134:137], v[190:193], v[38:41]
	v_mfma_f32_16x16x32_bf16 v[34:37], v[142:145], v[190:193], v[34:37]
	v_mfma_f32_16x16x32_bf16 v[30:33], v[146:149], v[162:165], v[30:33]
	v_mfma_f32_16x16x32_bf16 v[26:29], v[154:157], v[162:165], v[26:29]
	v_mfma_f32_16x16x32_bf16 v[22:25], v[146:149], v[170:173], v[22:25]
	v_mfma_f32_16x16x32_bf16 v[18:21], v[154:157], v[170:173], v[18:21]
	v_mfma_f32_16x16x32_bf16 v[14:17], v[146:149], v[178:181], v[14:17]
	v_mfma_f32_16x16x32_bf16 v[10:13], v[154:157], v[178:181], v[10:13]
	v_mfma_f32_16x16x32_bf16 v[6:9], v[146:149], v[186:189], v[6:9]
	v_mfma_f32_16x16x32_bf16 v[2:5], v[154:157], v[186:189], v[2:5]
	v_mfma_f32_16x16x32_bf16 v[30:33], v[150:153], v[166:169], v[30:33]
	v_mfma_f32_16x16x32_bf16 v[26:29], v[158:161], v[166:169], v[26:29]
	v_mfma_f32_16x16x32_bf16 v[22:25], v[150:153], v[174:177], v[22:25]
	v_mfma_f32_16x16x32_bf16 v[18:21], v[158:161], v[174:177], v[18:21]
	v_mfma_f32_16x16x32_bf16 v[14:17], v[150:153], v[182:185], v[14:17]
	v_mfma_f32_16x16x32_bf16 v[10:13], v[158:161], v[182:185], v[10:13]
	v_mfma_f32_16x16x32_bf16 v[6:9], v[150:153], v[190:193], v[6:9]
	v_mfma_f32_16x16x32_bf16 v[2:5], v[158:161], v[190:193], v[2:5]
	s_setprio 0
	s_barrier
	s_add_i32 s41, s41, 2
	s_add_u32 s54, s54, 0x100
	s_addc_u32 s55, s55, 0
	s_add_u32 s29, s29, 0x100
	s_addc_u32 s39, s39, 0
	s_cmp_gt_u32 s41, 5
	s_cbranch_scc0 .LBB0_851
	s_and_b64 vcc, exec, s[16:17]
	s_cbranch_vccz .LBB0_854
	s_barrier

.LBB0_1058:
	v_or_b32_e32 v0, 0x10000, v162
	v_add_u32_e32 v158, 0x10400, v162
	ds_read_b128 v[164:167], v0
	ds_read_b128 v[168:171], v158
	v_add_u32_e32 v0, 0x10800, v162
	v_add_u32_e32 v158, 0x10c00, v162
	ds_read_b128 v[172:175], v0
	ds_read_b128 v[176:179], v158
	v_or_b32_e32 v0, 0x14000, v162
	v_add_u32_e32 v158, 0x14400, v162
	ds_read_b128 v[180:183], v0
	ds_read_b128 v[184:187], v158
	v_add_u32_e32 v0, 0x14800, v162
	v_add_u32_e32 v158, 0x14c00, v162
	ds_read_b128 v[188:191], v0
	ds_read_b128 v[192:195], v158
	s_add_u32 s48, s36, 0xfffc0080
	s_addc_u32 s49, s37, -1
	s_cmp_eq_u32 s90, 12
	s_cselect_b32 s51, s29, s49
	s_cselect_b32 s50, s39, s48
	s_cselect_b32 s49, s41, s89
	s_cselect_b32 s48, s85, s88
	v_lshl_add_u64 v[158:159], s[36:37], 0, v[138:139]
	s_add_i32 m0, s35, 0xc000
	ds_read_b128 v[200:203], v161
	ds_read_b128 v[204:207], v161 offset:1024
	ds_read_b128 v[208:211], v161 offset:2048
	ds_read_b128 v[212:215], v161 offset:3072
	ds_read_b128 v[216:219], v161 offset:4096
	ds_read_b128 v[220:223], v161 offset:5120
	ds_read_b128 v[236:239], v161 offset:6144
	ds_read_b128 v[240:243], v161 offset:7168
	global_load_lds_dwordx4 v[158:159], off
	v_lshl_add_u64 v[158:159], s[36:37], 0, v[140:141]
	s_add_i32 m0, s35, 0xe000
	s_nop 0
	global_load_lds_dwordx4 v[158:159], off
	s_waitcnt vmcnt(8)
	s_waitcnt lgkmcnt(0)
	s_barrier
	s_setprio 1
	v_mfma_f32_16x16x32_bf16 v[126:129], v[164:167], v[200:203], v[126:129]
	v_mfma_f32_16x16x32_bf16 v[122:125], v[172:175], v[200:203], v[122:125]
	v_mfma_f32_16x16x32_bf16 v[110:113], v[164:167], v[208:211], v[110:113]
	v_mfma_f32_16x16x32_bf16 v[106:109], v[172:175], v[208:211], v[106:109]
	v_mfma_f32_16x16x32_bf16 v[94:97], v[164:167], v[216:219], v[94:97]
	v_mfma_f32_16x16x32_bf16 v[90:93], v[172:175], v[216:219], v[90:93]
	v_mfma_f32_16x16x32_bf16 v[78:81], v[164:167], v[236:239], v[78:81]
	v_mfma_f32_16x16x32_bf16 v[74:77], v[172:175], v[236:239], v[74:77]
	v_mfma_f32_16x16x32_bf16 v[126:129], v[168:171], v[204:207], v[126:129]
	v_mfma_f32_16x16x32_bf16 v[122:125], v[176:179], v[204:207], v[122:125]
	v_mfma_f32_16x16x32_bf16 v[110:113], v[168:171], v[212:215], v[110:113]
	v_mfma_f32_16x16x32_bf16 v[106:109], v[176:179], v[212:215], v[106:109]
	v_mfma_f32_16x16x32_bf16 v[94:97], v[168:171], v[220:223], v[94:97]
	v_mfma_f32_16x16x32_bf16 v[90:93], v[176:179], v[220:223], v[90:93]
	v_mfma_f32_16x16x32_bf16 v[78:81], v[168:171], v[240:243], v[78:81]
	v_mfma_f32_16x16x32_bf16 v[74:77], v[176:179], v[240:243], v[74:77]
	v_mfma_f32_16x16x32_bf16 v[118:121], v[180:183], v[200:203], v[118:121]
	v_mfma_f32_16x16x32_bf16 v[114:117], v[188:191], v[200:203], v[114:117]
	v_mfma_f32_16x16x32_bf16 v[102:105], v[180:183], v[208:211], v[102:105]
	v_mfma_f32_16x16x32_bf16 v[98:101], v[188:191], v[208:211], v[98:101]
	v_mfma_f32_16x16x32_bf16 v[86:89], v[180:183], v[216:219], v[86:89]
	v_mfma_f32_16x16x32_bf16 v[82:85], v[188:191], v[216:219], v[82:85]
	v_mfma_f32_16x16x32_bf16 v[70:73], v[180:183], v[236:239], v[70:73]
	v_mfma_f32_16x16x32_bf16 v[66:69], v[188:191], v[236:239], v[66:69]
	v_mfma_f32_16x16x32_bf16 v[118:121], v[184:187], v[204:207], v[118:121]
	v_mfma_f32_16x16x32_bf16 v[114:117], v[192:195], v[204:207], v[114:117]
	v_mfma_f32_16x16x32_bf16 v[102:105], v[184:187], v[212:215], v[102:105]
	v_mfma_f32_16x16x32_bf16 v[98:101], v[192:195], v[212:215], v[98:101]
	v_mfma_f32_16x16x32_bf16 v[86:89], v[184:187], v[220:223], v[86:89]
	v_mfma_f32_16x16x32_bf16 v[82:85], v[192:195], v[220:223], v[82:85]
	v_mfma_f32_16x16x32_bf16 v[70:73], v[184:187], v[240:243], v[70:73]
	v_mfma_f32_16x16x32_bf16 v[66:69], v[192:195], v[240:243], v[66:69]
	s_setprio 0
	s_barrier
	s_mov_b32 m0, s53
	v_lshl_add_u64 v[158:159], s[48:49], 0, v[134:135]
	s_add_u32 s92, s48, 0x40000
	ds_read_b128 v[200:203], v161 offset:16384
	ds_read_b128 v[204:207], v161 offset:17408
	ds_read_b128 v[208:211], v161 offset:18432
	ds_read_b128 v[212:215], v161 offset:19456
	ds_read_b128 v[216:219], v161 offset:20480
	ds_read_b128 v[220:223], v161 offset:21504
	ds_read_b128 v[236:239], v161 offset:22528
	ds_read_b128 v[240:243], v161 offset:23552
	global_load_lds_dwordx4 v[158:159], off
	v_lshl_add_u64 v[226:227], s[48:49], 0, v[130:131]
	s_mov_b32 m0, s54
	s_addc_u32 s93, s49, 0
	global_load_lds_dwordx4 v[226:227], off
	v_lshl_add_u64 v[244:245], s[92:93], 0, v[134:135]
	s_mov_b32 m0, s55
	v_lshl_add_u64 v[246:247], s[50:51], 0, v[132:133]
	global_load_lds_dwordx4 v[244:245], off
	v_lshl_add_u64 v[244:245], s[92:93], 0, v[130:131]
	s_mov_b32 m0, s56
	s_nop 0
	global_load_lds_dwordx4 v[244:245], off
	v_lshl_add_u64 v[244:245], s[50:51], 0, v[136:137]
	s_mov_b32 m0, s35
	s_nop 0
	global_load_lds_dwordx4 v[244:245], off
	s_mov_b32 m0, s57
	s_nop 0
	global_load_lds_dwordx4 v[246:247], off
	s_waitcnt vmcnt(8)
	s_waitcnt lgkmcnt(0)
	s_barrier
	s_setprio 1
	v_mfma_f32_16x16x32_bf16 v[62:65], v[164:167], v[200:203], v[62:65]
	v_mfma_f32_16x16x32_bf16 v[58:61], v[172:175], v[200:203], v[58:61]
	v_mfma_f32_16x16x32_bf16 v[46:49], v[164:167], v[208:211], v[46:49]
	v_mfma_f32_16x16x32_bf16 v[42:45], v[172:175], v[208:211], v[42:45]
	v_mfma_f32_16x16x32_bf16 v[30:33], v[164:167], v[216:219], v[30:33]
	v_mfma_f32_16x16x32_bf16 v[26:29], v[172:175], v[216:219], v[26:29]
	v_mfma_f32_16x16x32_bf16 v[14:17], v[164:167], v[236:239], v[14:17]
	v_mfma_f32_16x16x32_bf16 v[10:13], v[172:175], v[236:239], v[10:13]
	v_mfma_f32_16x16x32_bf16 v[62:65], v[168:171], v[204:207], v[62:65]
	v_mfma_f32_16x16x32_bf16 v[58:61], v[176:179], v[204:207], v[58:61]
	v_mfma_f32_16x16x32_bf16 v[46:49], v[168:171], v[212:215], v[46:49]
	v_mfma_f32_16x16x32_bf16 v[42:45], v[176:179], v[212:215], v[42:45]
	v_mfma_f32_16x16x32_bf16 v[30:33], v[168:171], v[220:223], v[30:33]
	v_mfma_f32_16x16x32_bf16 v[26:29], v[176:179], v[220:223], v[26:29]
	v_mfma_f32_16x16x32_bf16 v[14:17], v[168:171], v[240:243], v[14:17]
	v_mfma_f32_16x16x32_bf16 v[10:13], v[176:179], v[240:243], v[10:13]
	v_mfma_f32_16x16x32_bf16 v[54:57], v[180:183], v[200:203], v[54:57]
	v_mfma_f32_16x16x32_bf16 v[50:53], v[188:191], v[200:203], v[50:53]
	v_mfma_f32_16x16x32_bf16 v[38:41], v[180:183], v[208:211], v[38:41]
	v_mfma_f32_16x16x32_bf16 v[34:37], v[188:191], v[208:211], v[34:37]
	v_mfma_f32_16x16x32_bf16 v[22:25], v[180:183], v[216:219], v[22:25]
	v_mfma_f32_16x16x32_bf16 v[18:21], v[188:191], v[216:219], v[18:21]
	v_mfma_f32_16x16x32_bf16 v[6:9], v[180:183], v[236:239], v[6:9]
	v_mfma_f32_16x16x32_bf16 v[2:5], v[188:191], v[236:239], v[2:5]
	v_mfma_f32_16x16x32_bf16 v[54:57], v[184:187], v[204:207], v[54:57]
	v_mfma_f32_16x16x32_bf16 v[50:53], v[192:195], v[204:207], v[50:53]
	v_mfma_f32_16x16x32_bf16 v[38:41], v[184:187], v[212:215], v[38:41]
	v_mfma_f32_16x16x32_bf16 v[34:37], v[192:195], v[212:215], v[34:37]
	v_mfma_f32_16x16x32_bf16 v[22:25], v[184:187], v[220:223], v[22:25]
	v_mfma_f32_16x16x32_bf16 v[18:21], v[192:195], v[220:223], v[18:21]
	v_mfma_f32_16x16x32_bf16 v[6:9], v[184:187], v[240:243], v[6:9]
	v_mfma_f32_16x16x32_bf16 v[2:5], v[192:195], v[240:243], v[2:5]
	s_setprio 0
	s_barrier
	v_or_b32_e32 v0, 0x18000, v162
	v_add_u32_e32 v163, 0x18400, v162
	ds_read_b128 v[164:167], v0
	ds_read_b128 v[168:171], v163
	v_add_u32_e32 v0, 0x18800, v162
	v_add_u32_e32 v163, 0x18c00, v162
	ds_read_b128 v[172:175], v0
	ds_read_b128 v[176:179], v163
	v_or_b32_e32 v0, 0x1c000, v162
	v_add_u32_e32 v163, 0x1c400, v162
	ds_read_b128 v[180:183], v0
	ds_read_b128 v[184:187], v163
	v_add_u32_e32 v0, 0x1c800, v162
	v_add_u32_e32 v163, 0x1cc00, v162
	ds_read_b128 v[188:191], v0
	ds_read_b128 v[192:195], v163
	s_add_u32 s50, s50, 0x40000
	s_addc_u32 s51, s51, 0
	s_mov_b32 m0, s58
	v_lshl_add_u64 v[248:249], s[50:51], 0, v[136:137]
	ds_read_b128 v[200:203], v161 offset:32768
	ds_read_b128 v[204:207], v161 offset:33792
	ds_read_b128 v[208:211], v161 offset:34816
	ds_read_b128 v[212:215], v161 offset:35840
	ds_read_b128 v[216:219], v161 offset:36864
	ds_read_b128 v[220:223], v161 offset:37888
	ds_read_b128 v[236:239], v161 offset:38912
	ds_read_b128 v[240:243], v161 offset:39936
	global_load_lds_dwordx4 v[248:249], off
	v_lshl_add_u64 v[248:249], s[50:51], 0, v[132:133]
	s_mov_b32 m0, s59
	s_nop 0
	global_load_lds_dwordx4 v[248:249], off
	s_waitcnt vmcnt(8)
	s_waitcnt lgkmcnt(0)
	s_barrier
	s_setprio 1
	v_mfma_f32_16x16x32_bf16 v[126:129], v[164:167], v[200:203], v[126:129]
	v_mfma_f32_16x16x32_bf16 v[122:125], v[172:175], v[200:203], v[122:125]
	v_mfma_f32_16x16x32_bf16 v[110:113], v[164:167], v[208:211], v[110:113]
	v_mfma_f32_16x16x32_bf16 v[106:109], v[172:175], v[208:211], v[106:109]
	v_mfma_f32_16x16x32_bf16 v[94:97], v[164:167], v[216:219], v[94:97]
	v_mfma_f32_16x16x32_bf16 v[90:93], v[172:175], v[216:219], v[90:93]
	v_mfma_f32_16x16x32_bf16 v[78:81], v[164:167], v[236:239], v[78:81]
	v_mfma_f32_16x16x32_bf16 v[74:77], v[172:175], v[236:239], v[74:77]
	v_mfma_f32_16x16x32_bf16 v[126:129], v[168:171], v[204:207], v[126:129]
	v_mfma_f32_16x16x32_bf16 v[122:125], v[176:179], v[204:207], v[122:125]
	v_mfma_f32_16x16x32_bf16 v[110:113], v[168:171], v[212:215], v[110:113]
	v_mfma_f32_16x16x32_bf16 v[106:109], v[176:179], v[212:215], v[106:109]
	v_mfma_f32_16x16x32_bf16 v[94:97], v[168:171], v[220:223], v[94:97]
	v_mfma_f32_16x16x32_bf16 v[90:93], v[176:179], v[220:223], v[90:93]
	v_mfma_f32_16x16x32_bf16 v[78:81], v[168:171], v[240:243], v[78:81]
	v_mfma_f32_16x16x32_bf16 v[74:77], v[176:179], v[240:243], v[74:77]
	v_mfma_f32_16x16x32_bf16 v[118:121], v[180:183], v[200:203], v[118:121]
	v_mfma_f32_16x16x32_bf16 v[114:117], v[188:191], v[200:203], v[114:117]
	v_mfma_f32_16x16x32_bf16 v[102:105], v[180:183], v[208:211], v[102:105]
	v_mfma_f32_16x16x32_bf16 v[98:101], v[188:191], v[208:211], v[98:101]
	v_mfma_f32_16x16x32_bf16 v[86:89], v[180:183], v[216:219], v[86:89]
	v_mfma_f32_16x16x32_bf16 v[82:85], v[188:191], v[216:219], v[82:85]
	v_mfma_f32_16x16x32_bf16 v[70:73], v[180:183], v[236:239], v[70:73]
	v_mfma_f32_16x16x32_bf16 v[66:69], v[188:191], v[236:239], v[66:69]
	v_mfma_f32_16x16x32_bf16 v[118:121], v[184:187], v[204:207], v[118:121]
	v_mfma_f32_16x16x32_bf16 v[114:117], v[192:195], v[204:207], v[114:117]
	v_mfma_f32_16x16x32_bf16 v[102:105], v[184:187], v[212:215], v[102:105]
	v_mfma_f32_16x16x32_bf16 v[98:101], v[192:195], v[212:215], v[98:101]
	v_mfma_f32_16x16x32_bf16 v[86:89], v[184:187], v[220:223], v[86:89]
	v_mfma_f32_16x16x32_bf16 v[82:85], v[192:195], v[220:223], v[82:85]
	v_mfma_f32_16x16x32_bf16 v[70:73], v[184:187], v[240:243], v[70:73]
	v_mfma_f32_16x16x32_bf16 v[66:69], v[192:195], v[240:243], v[66:69]
	s_setprio 0
	s_barrier
	s_mov_b32 m0, s62
	v_lshl_add_u64 v[158:159], v[158:159], 0, s[18:19]
	s_add_u32 s48, s48, 0x40080
	ds_read_b128 v[200:203], v161 offset:49152
	ds_read_b128 v[204:207], v161 offset:50176
	ds_read_b128 v[208:211], v161 offset:51200
	ds_read_b128 v[212:215], v161 offset:52224
	ds_read_b128 v[216:219], v161 offset:53248
	ds_read_b128 v[220:223], v161 offset:54272
	ds_read_b128 v[236:239], v161 offset:55296
	ds_read_b128 v[240:243], v161 offset:56320
	global_load_lds_dwordx4 v[158:159], off
	v_lshl_add_u64 v[158:159], v[226:227], 0, s[18:19]
	s_mov_b32 m0, s63
	s_addc_u32 s49, s49, 0
	global_load_lds_dwordx4 v[158:159], off
	v_lshl_add_u64 v[158:159], s[48:49], 0, v[134:135]
	s_mov_b32 m0, s66
	s_nop 0
	global_load_lds_dwordx4 v[158:159], off
	v_lshl_add_u64 v[158:159], s[48:49], 0, v[130:131]
	s_mov_b32 m0, s67
	s_nop 0
	global_load_lds_dwordx4 v[158:159], off
	v_lshl_add_u64 v[158:159], v[244:245], 0, s[18:19]
	s_mov_b32 m0, s64
	s_nop 0
	global_load_lds_dwordx4 v[158:159], off
	v_lshl_add_u64 v[158:159], v[246:247], 0, s[18:19]
	s_mov_b32 m0, s65
	s_nop 0
	global_load_lds_dwordx4 v[158:159], off
	s_waitcnt vmcnt(8)
	s_waitcnt lgkmcnt(0)
	s_barrier
	s_setprio 1
	v_mfma_f32_16x16x32_bf16 v[62:65], v[164:167], v[200:203], v[62:65]
	v_mfma_f32_16x16x32_bf16 v[58:61], v[172:175], v[200:203], v[58:61]
	v_mfma_f32_16x16x32_bf16 v[46:49], v[164:167], v[208:211], v[46:49]
	v_mfma_f32_16x16x32_bf16 v[42:45], v[172:175], v[208:211], v[42:45]
	v_mfma_f32_16x16x32_bf16 v[30:33], v[164:167], v[216:219], v[30:33]
	v_mfma_f32_16x16x32_bf16 v[26:29], v[172:175], v[216:219], v[26:29]
	v_mfma_f32_16x16x32_bf16 v[14:17], v[164:167], v[236:239], v[14:17]
	v_mfma_f32_16x16x32_bf16 v[10:13], v[172:175], v[236:239], v[10:13]
	v_mfma_f32_16x16x32_bf16 v[62:65], v[168:171], v[204:207], v[62:65]
	v_mfma_f32_16x16x32_bf16 v[58:61], v[176:179], v[204:207], v[58:61]
	v_mfma_f32_16x16x32_bf16 v[46:49], v[168:171], v[212:215], v[46:49]
	v_mfma_f32_16x16x32_bf16 v[42:45], v[176:179], v[212:215], v[42:45]
	v_mfma_f32_16x16x32_bf16 v[30:33], v[168:171], v[220:223], v[30:33]
	v_mfma_f32_16x16x32_bf16 v[26:29], v[176:179], v[220:223], v[26:29]
	v_mfma_f32_16x16x32_bf16 v[14:17], v[168:171], v[240:243], v[14:17]
	v_mfma_f32_16x16x32_bf16 v[10:13], v[176:179], v[240:243], v[10:13]
	v_mfma_f32_16x16x32_bf16 v[54:57], v[180:183], v[200:203], v[54:57]
	v_mfma_f32_16x16x32_bf16 v[50:53], v[188:191], v[200:203], v[50:53]
	v_mfma_f32_16x16x32_bf16 v[38:41], v[180:183], v[208:211], v[38:41]
	v_mfma_f32_16x16x32_bf16 v[34:37], v[188:191], v[208:211], v[34:37]
	v_mfma_f32_16x16x32_bf16 v[22:25], v[180:183], v[216:219], v[22:25]
	v_mfma_f32_16x16x32_bf16 v[18:21], v[188:191], v[216:219], v[18:21]
	v_mfma_f32_16x16x32_bf16 v[6:9], v[180:183], v[236:239], v[6:9]
	v_mfma_f32_16x16x32_bf16 v[2:5], v[188:191], v[236:239], v[2:5]
	v_mfma_f32_16x16x32_bf16 v[54:57], v[184:187], v[204:207], v[54:57]
	v_mfma_f32_16x16x32_bf16 v[50:53], v[192:195], v[204:207], v[50:53]
	v_mfma_f32_16x16x32_bf16 v[38:41], v[184:187], v[212:215], v[38:41]
	v_mfma_f32_16x16x32_bf16 v[34:37], v[192:195], v[212:215], v[34:37]
	v_mfma_f32_16x16x32_bf16 v[22:25], v[184:187], v[220:223], v[22:25]
	v_mfma_f32_16x16x32_bf16 v[18:21], v[192:195], v[220:223], v[18:21]
	v_mfma_f32_16x16x32_bf16 v[6:9], v[184:187], v[240:243], v[6:9]
	v_mfma_f32_16x16x32_bf16 v[2:5], v[192:195], v[240:243], v[2:5]
	s_setprio 0
	s_barrier
	s_add_i32 s90, s90, 2
	s_add_u32 s36, s36, 0x100
	s_addc_u32 s37, s37, 0
	s_add_u32 s88, s88, 0x100
	s_addc_u32 s89, s89, 0
	s_cmp_gt_u32 s90, 13
	s_cbranch_scc0 .LBB0_1058
	s_and_b64 vcc, exec, s[16:17]
	s_cbranch_vccz .LBB0_1061
	s_barrier

.LBB0_1195:
	s_add_u32 s58, s44, s52
	s_addc_u32 s59, s45, s53
	s_add_u32 s56, s58, 0x100
	s_addc_u32 s57, s59, 0
	s_and_b64 s[54:55], s[50:51], exec
	s_cselect_b32 s55, s17, s57
	s_cselect_b32 s54, s29, s56
	s_add_u32 s52, s42, s52
	s_addc_u32 s53, s43, s53
	v_or_b32_e32 v0, 0x10000, v141
	s_add_u32 s52, s52, 0x100
	ds_read_b128 v[142:145], v0
	v_add_u32_e32 v0, 0x10400, v141
	s_addc_u32 s53, s53, 0
	ds_read_b128 v[146:149], v0
	v_add_u32_e32 v0, 0x10800, v141
	s_and_b64 s[50:51], s[50:51], exec
	ds_read_b128 v[150:153], v0
	v_add_u32_e32 v0, 0x10c00, v141
	s_cselect_b32 s57, s39, s53
	s_cselect_b32 s56, s38, s52
	s_add_u32 s60, s58, 0x80080
	ds_read_b128 v[154:157], v0
	v_or_b32_e32 v0, 0x14000, v141
	s_addc_u32 s61, s59, 0
	s_add_i32 m0, s63, 0xc000
	s_add_i32 vcc_lo, s63, 0xe000
	ds_read_b128 v[158:161], v0
	v_add_u32_e32 v0, 0x14400, v141
	s_add_u32 s58, s56, 0x40000
	ds_read_b128 v[162:165], v0
	v_add_u32_e32 v0, 0x14800, v141
	s_addc_u32 s59, s57, 0
	ds_read_b128 v[166:169], v0
	v_add_u32_e32 v0, 0x14c00, v141
	s_add_u32 s52, s54, 0x80000
	ds_read_b128 v[170:173], v0
	s_addc_u32 s53, s55, 0
	s_add_u32 s50, s56, 0x40080
	s_addc_u32 s51, s57, 0
	v_lshl_add_u64 v[138:139], s[60:61], 0, v[136:137]
	ds_read_b128 v[174:177], v140
	ds_read_b128 v[178:181], v140 offset:1024
	ds_read_b128 v[182:185], v140 offset:2048
	ds_read_b128 v[186:189], v140 offset:3072
	ds_read_b128 v[190:193], v140 offset:4096
	ds_read_b128 v[200:203], v140 offset:5120
	ds_read_b128 v[204:207], v140 offset:6144
	ds_read_b128 v[208:211], v140 offset:7168
	global_load_lds_dwordx4 v[138:139], off
	v_lshl_add_u64 v[138:139], s[60:61], 0, v[132:133]
	s_mov_b32 m0, vcc_lo
	s_nop 0
	global_load_lds_dwordx4 v[138:139], off
	s_waitcnt vmcnt(8)
	s_waitcnt lgkmcnt(0)
	s_barrier
	s_setprio 1
	v_mfma_f32_16x16x32_bf16 v[126:129], v[142:145], v[174:177], v[126:129]
	v_mfma_f32_16x16x32_bf16 v[122:125], v[150:153], v[174:177], v[122:125]
	v_mfma_f32_16x16x32_bf16 v[118:121], v[142:145], v[182:185], v[118:121]
	v_mfma_f32_16x16x32_bf16 v[110:113], v[150:153], v[182:185], v[110:113]
	v_mfma_f32_16x16x32_bf16 v[102:105], v[142:145], v[190:193], v[102:105]
	v_mfma_f32_16x16x32_bf16 v[94:97], v[150:153], v[190:193], v[94:97]
	v_mfma_f32_16x16x32_bf16 v[86:89], v[142:145], v[204:207], v[86:89]
	v_mfma_f32_16x16x32_bf16 v[78:81], v[150:153], v[204:207], v[78:81]
	v_mfma_f32_16x16x32_bf16 v[126:129], v[146:149], v[178:181], v[126:129]
	v_mfma_f32_16x16x32_bf16 v[122:125], v[154:157], v[178:181], v[122:125]
	v_mfma_f32_16x16x32_bf16 v[118:121], v[146:149], v[186:189], v[118:121]
	v_mfma_f32_16x16x32_bf16 v[110:113], v[154:157], v[186:189], v[110:113]
	v_mfma_f32_16x16x32_bf16 v[102:105], v[146:149], v[200:203], v[102:105]
	v_mfma_f32_16x16x32_bf16 v[94:97], v[154:157], v[200:203], v[94:97]
	v_mfma_f32_16x16x32_bf16 v[86:89], v[146:149], v[208:211], v[86:89]
	v_mfma_f32_16x16x32_bf16 v[78:81], v[154:157], v[208:211], v[78:81]
	v_mfma_f32_16x16x32_bf16 v[114:117], v[158:161], v[174:177], v[114:117]
	v_mfma_f32_16x16x32_bf16 v[106:109], v[166:169], v[174:177], v[106:109]
	v_mfma_f32_16x16x32_bf16 v[98:101], v[158:161], v[182:185], v[98:101]
	v_mfma_f32_16x16x32_bf16 v[90:93], v[166:169], v[182:185], v[90:93]
	v_mfma_f32_16x16x32_bf16 v[82:85], v[158:161], v[190:193], v[82:85]
	v_mfma_f32_16x16x32_bf16 v[74:77], v[166:169], v[190:193], v[74:77]
	v_mfma_f32_16x16x32_bf16 v[70:73], v[158:161], v[204:207], v[70:73]
	v_mfma_f32_16x16x32_bf16 v[66:69], v[166:169], v[204:207], v[66:69]
	v_mfma_f32_16x16x32_bf16 v[114:117], v[162:165], v[178:181], v[114:117]
	v_mfma_f32_16x16x32_bf16 v[106:109], v[170:173], v[178:181], v[106:109]
	v_mfma_f32_16x16x32_bf16 v[98:101], v[162:165], v[186:189], v[98:101]
	v_mfma_f32_16x16x32_bf16 v[90:93], v[170:173], v[186:189], v[90:93]
	v_mfma_f32_16x16x32_bf16 v[82:85], v[162:165], v[200:203], v[82:85]
	v_mfma_f32_16x16x32_bf16 v[74:77], v[170:173], v[200:203], v[74:77]
	v_mfma_f32_16x16x32_bf16 v[70:73], v[162:165], v[208:211], v[70:73]
	v_mfma_f32_16x16x32_bf16 v[66:69], v[170:173], v[208:211], v[66:69]
	s_setprio 0
	s_barrier
	s_mov_b32 m0, s64
	v_lshl_add_u64 v[138:139], s[56:57], 0, v[134:135]
	ds_read_b128 v[174:177], v140 offset:16384
	ds_read_b128 v[178:181], v140 offset:17408
	ds_read_b128 v[182:185], v140 offset:18432
	ds_read_b128 v[186:189], v140 offset:19456
	ds_read_b128 v[190:193], v140 offset:20480
	ds_read_b128 v[200:203], v140 offset:21504
	ds_read_b128 v[204:207], v140 offset:22528
	ds_read_b128 v[208:211], v140 offset:23552
	global_load_lds_dwordx4 v[138:139], off
	v_lshl_add_u64 v[194:195], s[56:57], 0, v[130:131]
	s_mov_b32 m0, s65
	v_lshl_add_u64 v[212:213], s[58:59], 0, v[134:135]
	global_load_lds_dwordx4 v[194:195], off
	s_mov_b32 m0, s66
	v_lshl_add_u64 v[214:215], s[54:55], 0, v[132:133]
	global_load_lds_dwordx4 v[212:213], off
	v_lshl_add_u64 v[212:213], s[58:59], 0, v[130:131]
	s_mov_b32 m0, s67
	s_nop 0
	global_load_lds_dwordx4 v[212:213], off
	v_lshl_add_u64 v[212:213], s[54:55], 0, v[136:137]
	s_mov_b32 m0, s63
	s_nop 0
	global_load_lds_dwordx4 v[212:213], off
	s_mov_b32 m0, s80
	s_nop 0
	global_load_lds_dwordx4 v[214:215], off
	s_waitcnt vmcnt(8)
	s_waitcnt lgkmcnt(0)
	s_barrier
	s_setprio 1
	v_mfma_f32_16x16x32_bf16 v[62:65], v[142:145], v[174:177], v[62:65]
	v_mfma_f32_16x16x32_bf16 v[58:61], v[150:153], v[174:177], v[58:61]
	v_mfma_f32_16x16x32_bf16 v[54:57], v[142:145], v[182:185], v[54:57]
	v_mfma_f32_16x16x32_bf16 v[46:49], v[150:153], v[182:185], v[46:49]
	v_mfma_f32_16x16x32_bf16 v[38:41], v[142:145], v[190:193], v[38:41]
	v_mfma_f32_16x16x32_bf16 v[30:33], v[150:153], v[190:193], v[30:33]
	v_mfma_f32_16x16x32_bf16 v[22:25], v[142:145], v[204:207], v[22:25]
	v_mfma_f32_16x16x32_bf16 v[14:17], v[150:153], v[204:207], v[14:17]
	v_mfma_f32_16x16x32_bf16 v[62:65], v[146:149], v[178:181], v[62:65]
	v_mfma_f32_16x16x32_bf16 v[58:61], v[154:157], v[178:181], v[58:61]
	v_mfma_f32_16x16x32_bf16 v[54:57], v[146:149], v[186:189], v[54:57]
	v_mfma_f32_16x16x32_bf16 v[46:49], v[154:157], v[186:189], v[46:49]
	v_mfma_f32_16x16x32_bf16 v[38:41], v[146:149], v[200:203], v[38:41]
	v_mfma_f32_16x16x32_bf16 v[30:33], v[154:157], v[200:203], v[30:33]
	v_mfma_f32_16x16x32_bf16 v[22:25], v[146:149], v[208:211], v[22:25]
	v_mfma_f32_16x16x32_bf16 v[14:17], v[154:157], v[208:211], v[14:17]
	v_mfma_f32_16x16x32_bf16 v[50:53], v[158:161], v[174:177], v[50:53]
	v_mfma_f32_16x16x32_bf16 v[42:45], v[166:169], v[174:177], v[42:45]
	v_mfma_f32_16x16x32_bf16 v[34:37], v[158:161], v[182:185], v[34:37]
	v_mfma_f32_16x16x32_bf16 v[26:29], v[166:169], v[182:185], v[26:29]
	v_mfma_f32_16x16x32_bf16 v[18:21], v[158:161], v[190:193], v[18:21]
	v_mfma_f32_16x16x32_bf16 v[10:13], v[166:169], v[190:193], v[10:13]
	v_mfma_f32_16x16x32_bf16 v[6:9], v[158:161], v[204:207], v[6:9]
	v_mfma_f32_16x16x32_bf16 v[2:5], v[166:169], v[204:207], v[2:5]
	v_mfma_f32_16x16x32_bf16 v[50:53], v[162:165], v[178:181], v[50:53]
	v_mfma_f32_16x16x32_bf16 v[42:45], v[170:173], v[178:181], v[42:45]
	v_mfma_f32_16x16x32_bf16 v[34:37], v[162:165], v[186:189], v[34:37]
	v_mfma_f32_16x16x32_bf16 v[26:29], v[170:173], v[186:189], v[26:29]
	v_mfma_f32_16x16x32_bf16 v[18:21], v[162:165], v[200:203], v[18:21]
	v_mfma_f32_16x16x32_bf16 v[10:13], v[170:173], v[200:203], v[10:13]
	v_mfma_f32_16x16x32_bf16 v[6:9], v[162:165], v[208:211], v[6:9]
	v_mfma_f32_16x16x32_bf16 v[2:5], v[170:173], v[208:211], v[2:5]
	s_setprio 0
	s_barrier
	v_or_b32_e32 v0, 0x18000, v141
	v_add_u32_e32 v146, 0x18400, v141
	ds_read_b128 v[142:145], v0
	ds_read_b128 v[146:149], v146
	v_add_u32_e32 v0, 0x18800, v141
	v_add_u32_e32 v154, 0x18c00, v141
	ds_read_b128 v[150:153], v0
	ds_read_b128 v[154:157], v154
	v_or_b32_e32 v0, 0x1c000, v141
	v_add_u32_e32 v162, 0x1c400, v141
	ds_read_b128 v[158:161], v0
	ds_read_b128 v[162:165], v162
	v_add_u32_e32 v0, 0x1c800, v141
	v_add_u32_e32 v170, 0x1cc00, v141
	ds_read_b128 v[166:169], v0
	ds_read_b128 v[170:173], v170
	s_mov_b32 m0, s82
	v_lshl_add_u64 v[216:217], s[52:53], 0, v[136:137]
	ds_read_b128 v[174:177], v140 offset:32768
	ds_read_b128 v[178:181], v140 offset:33792
	ds_read_b128 v[182:185], v140 offset:34816
	ds_read_b128 v[186:189], v140 offset:35840
	ds_read_b128 v[190:193], v140 offset:36864
	ds_read_b128 v[200:203], v140 offset:37888
	ds_read_b128 v[204:207], v140 offset:38912
	ds_read_b128 v[208:211], v140 offset:39936
	global_load_lds_dwordx4 v[216:217], off
	v_lshl_add_u64 v[216:217], s[52:53], 0, v[132:133]
	s_mov_b32 m0, s83
	s_nop 0
	global_load_lds_dwordx4 v[216:217], off
	s_waitcnt vmcnt(8)
	s_waitcnt lgkmcnt(0)
	s_barrier
	s_setprio 1
	v_mfma_f32_16x16x32_bf16 v[126:129], v[142:145], v[174:177], v[126:129]
	v_mfma_f32_16x16x32_bf16 v[122:125], v[150:153], v[174:177], v[122:125]
	v_mfma_f32_16x16x32_bf16 v[118:121], v[142:145], v[182:185], v[118:121]
	v_mfma_f32_16x16x32_bf16 v[110:113], v[150:153], v[182:185], v[110:113]
	v_mfma_f32_16x16x32_bf16 v[102:105], v[142:145], v[190:193], v[102:105]
	v_mfma_f32_16x16x32_bf16 v[94:97], v[150:153], v[190:193], v[94:97]
	v_mfma_f32_16x16x32_bf16 v[86:89], v[142:145], v[204:207], v[86:89]
	v_mfma_f32_16x16x32_bf16 v[78:81], v[150:153], v[204:207], v[78:81]
	v_mfma_f32_16x16x32_bf16 v[126:129], v[146:149], v[178:181], v[126:129]
	v_mfma_f32_16x16x32_bf16 v[122:125], v[154:157], v[178:181], v[122:125]
	v_mfma_f32_16x16x32_bf16 v[118:121], v[146:149], v[186:189], v[118:121]
	v_mfma_f32_16x16x32_bf16 v[110:113], v[154:157], v[186:189], v[110:113]
	v_mfma_f32_16x16x32_bf16 v[102:105], v[146:149], v[200:203], v[102:105]
	v_mfma_f32_16x16x32_bf16 v[94:97], v[154:157], v[200:203], v[94:97]
	v_mfma_f32_16x16x32_bf16 v[86:89], v[146:149], v[208:211], v[86:89]
	v_mfma_f32_16x16x32_bf16 v[78:81], v[154:157], v[208:211], v[78:81]
	v_mfma_f32_16x16x32_bf16 v[114:117], v[158:161], v[174:177], v[114:117]
	v_mfma_f32_16x16x32_bf16 v[106:109], v[166:169], v[174:177], v[106:109]
	v_mfma_f32_16x16x32_bf16 v[98:101], v[158:161], v[182:185], v[98:101]
	v_mfma_f32_16x16x32_bf16 v[90:93], v[166:169], v[182:185], v[90:93]
	v_mfma_f32_16x16x32_bf16 v[82:85], v[158:161], v[190:193], v[82:85]
	v_mfma_f32_16x16x32_bf16 v[74:77], v[166:169], v[190:193], v[74:77]
	v_mfma_f32_16x16x32_bf16 v[70:73], v[158:161], v[204:207], v[70:73]
	v_mfma_f32_16x16x32_bf16 v[66:69], v[166:169], v[204:207], v[66:69]
	v_mfma_f32_16x16x32_bf16 v[114:117], v[162:165], v[178:181], v[114:117]
	v_mfma_f32_16x16x32_bf16 v[106:109], v[170:173], v[178:181], v[106:109]
	v_mfma_f32_16x16x32_bf16 v[98:101], v[162:165], v[186:189], v[98:101]
	v_mfma_f32_16x16x32_bf16 v[90:93], v[170:173], v[186:189], v[90:93]
	v_mfma_f32_16x16x32_bf16 v[82:85], v[162:165], v[200:203], v[82:85]
	v_mfma_f32_16x16x32_bf16 v[74:77], v[170:173], v[200:203], v[74:77]
	v_mfma_f32_16x16x32_bf16 v[70:73], v[162:165], v[208:211], v[70:73]
	v_mfma_f32_16x16x32_bf16 v[66:69], v[170:173], v[208:211], v[66:69]
	s_setprio 0
	s_barrier
	s_mov_b32 m0, s85
	v_lshl_add_u64 v[138:139], v[138:139], 0, s[18:19]
	ds_read_b128 v[174:177], v140 offset:49152
	ds_read_b128 v[178:181], v140 offset:50176
	ds_read_b128 v[182:185], v140 offset:51200
	ds_read_b128 v[186:189], v140 offset:52224
	ds_read_b128 v[190:193], v140 offset:53248
	ds_read_b128 v[200:203], v140 offset:54272
	ds_read_b128 v[204:207], v140 offset:55296
	ds_read_b128 v[208:211], v140 offset:56320
	global_load_lds_dwordx4 v[138:139], off
	v_lshl_add_u64 v[138:139], v[194:195], 0, s[18:19]
	s_mov_b32 m0, s88
	s_nop 0
	global_load_lds_dwordx4 v[138:139], off
	v_lshl_add_u64 v[138:139], s[50:51], 0, v[134:135]
	s_mov_b32 m0, s91
	s_nop 0
	global_load_lds_dwordx4 v[138:139], off
	v_lshl_add_u64 v[138:139], s[50:51], 0, v[130:131]
	s_mov_b32 m0, s92
	s_nop 0
	global_load_lds_dwordx4 v[138:139], off
	v_lshl_add_u64 v[138:139], v[212:213], 0, s[18:19]
	s_mov_b32 m0, s89
	s_nop 0
	global_load_lds_dwordx4 v[138:139], off
	v_lshl_add_u64 v[138:139], v[214:215], 0, s[18:19]
	s_mov_b32 m0, s90
	s_nop 0
	global_load_lds_dwordx4 v[138:139], off
	s_waitcnt vmcnt(8)
	s_waitcnt lgkmcnt(0)
	s_barrier
	s_setprio 1
	v_mfma_f32_16x16x32_bf16 v[62:65], v[142:145], v[174:177], v[62:65]
	v_mfma_f32_16x16x32_bf16 v[58:61], v[150:153], v[174:177], v[58:61]
	v_mfma_f32_16x16x32_bf16 v[54:57], v[142:145], v[182:185], v[54:57]
	v_mfma_f32_16x16x32_bf16 v[46:49], v[150:153], v[182:185], v[46:49]
	v_mfma_f32_16x16x32_bf16 v[38:41], v[142:145], v[190:193], v[38:41]
	v_mfma_f32_16x16x32_bf16 v[30:33], v[150:153], v[190:193], v[30:33]
	v_mfma_f32_16x16x32_bf16 v[22:25], v[142:145], v[204:207], v[22:25]
	v_mfma_f32_16x16x32_bf16 v[14:17], v[150:153], v[204:207], v[14:17]
	v_mfma_f32_16x16x32_bf16 v[62:65], v[146:149], v[178:181], v[62:65]
	v_mfma_f32_16x16x32_bf16 v[58:61], v[154:157], v[178:181], v[58:61]
	v_mfma_f32_16x16x32_bf16 v[54:57], v[146:149], v[186:189], v[54:57]
	v_mfma_f32_16x16x32_bf16 v[46:49], v[154:157], v[186:189], v[46:49]
	v_mfma_f32_16x16x32_bf16 v[38:41], v[146:149], v[200:203], v[38:41]
	v_mfma_f32_16x16x32_bf16 v[30:33], v[154:157], v[200:203], v[30:33]
	v_mfma_f32_16x16x32_bf16 v[22:25], v[146:149], v[208:211], v[22:25]
	v_mfma_f32_16x16x32_bf16 v[14:17], v[154:157], v[208:211], v[14:17]
	v_mfma_f32_16x16x32_bf16 v[50:53], v[158:161], v[174:177], v[50:53]
	v_mfma_f32_16x16x32_bf16 v[42:45], v[166:169], v[174:177], v[42:45]
	v_mfma_f32_16x16x32_bf16 v[34:37], v[158:161], v[182:185], v[34:37]
	v_mfma_f32_16x16x32_bf16 v[26:29], v[166:169], v[182:185], v[26:29]
	v_mfma_f32_16x16x32_bf16 v[18:21], v[158:161], v[190:193], v[18:21]
	v_mfma_f32_16x16x32_bf16 v[10:13], v[166:169], v[190:193], v[10:13]
	v_mfma_f32_16x16x32_bf16 v[6:9], v[158:161], v[204:207], v[6:9]
	v_mfma_f32_16x16x32_bf16 v[2:5], v[166:169], v[204:207], v[2:5]
	v_mfma_f32_16x16x32_bf16 v[50:53], v[162:165], v[178:181], v[50:53]
	v_mfma_f32_16x16x32_bf16 v[42:45], v[170:173], v[178:181], v[42:45]
	v_mfma_f32_16x16x32_bf16 v[34:37], v[162:165], v[186:189], v[34:37]
	v_mfma_f32_16x16x32_bf16 v[26:29], v[170:173], v[186:189], v[26:29]
	v_mfma_f32_16x16x32_bf16 v[18:21], v[162:165], v[200:203], v[18:21]
	v_mfma_f32_16x16x32_bf16 v[10:13], v[170:173], v[200:203], v[10:13]
	v_mfma_f32_16x16x32_bf16 v[6:9], v[162:165], v[208:211], v[6:9]
	v_mfma_f32_16x16x32_bf16 v[2:5], v[170:173], v[208:211], v[2:5]
	s_setprio 0
	s_barrier
	s_andn2_b64 vcc, exec, s[48:49]
	s_mov_b64 s[50:51], -1
	s_mov_b64 s[48:49], 0
	s_mov_b64 s[52:53], 0x100
	s_cbranch_vccz .LBB0_1195
	s_and_b64 vcc, exec, s[14:15]
	s_cbranch_vccz .LBB0_1198
	s_barrier

.LBB0_1213:
	s_add_u32 s58, s40, s52
	s_addc_u32 s59, s41, s53
	s_add_u32 s56, s58, 0x100
	s_addc_u32 s57, s59, 0
	s_and_b64 s[54:55], s[50:51], exec
	s_cselect_b32 s55, s43, s57
	s_cselect_b32 s54, s42, s56
	s_add_u32 s52, s38, s52
	s_addc_u32 s53, s39, s53
	v_or_b32_e32 v0, 0x10000, v139
	s_add_u32 s52, s52, 0x100
	ds_read_b128 v[140:143], v0
	v_add_u32_e32 v0, 0x10400, v139
	s_addc_u32 s53, s53, 0
	ds_read_b128 v[144:147], v0
	v_add_u32_e32 v0, 0x10800, v139
	s_and_b64 s[50:51], s[50:51], exec
	ds_read_b128 v[148:151], v0
	v_add_u32_e32 v0, 0x10c00, v139
	s_cselect_b32 s57, s37, s53
	s_cselect_b32 s56, s29, s52
	s_add_u32 s60, s58, 0x40080
	ds_read_b128 v[152:155], v0
	v_or_b32_e32 v0, 0x14000, v139
	s_addc_u32 s61, s59, 0
	s_add_i32 m0, s63, 0xc000
	s_add_i32 vcc_lo, s63, 0xe000
	ds_read_b128 v[156:159], v0
	v_add_u32_e32 v0, 0x14400, v139
	s_add_u32 s58, s56, 0x80000
	ds_read_b128 v[160:163], v0
	v_add_u32_e32 v0, 0x14800, v139
	s_addc_u32 s59, s57, 0
	ds_read_b128 v[164:167], v0
	v_add_u32_e32 v0, 0x14c00, v139
	s_add_u32 s52, s54, 0x40000
	ds_read_b128 v[168:171], v0
	s_addc_u32 s53, s55, 0
	s_add_u32 s50, s56, 0x80080
	s_addc_u32 s51, s57, 0
	v_lshl_add_u64 v[208:209], s[60:61], 0, v[136:137]
	ds_read_b128 v[172:175], v138
	ds_read_b128 v[176:179], v138 offset:1024
	ds_read_b128 v[180:183], v138 offset:2048
	ds_read_b128 v[184:187], v138 offset:3072
	ds_read_b128 v[188:191], v138 offset:4096
	ds_read_b128 v[192:195], v138 offset:5120
	ds_read_b128 v[200:203], v138 offset:6144
	ds_read_b128 v[204:207], v138 offset:7168
	global_load_lds_dwordx4 v[208:209], off
	v_lshl_add_u64 v[208:209], s[60:61], 0, v[132:133]
	s_mov_b32 m0, vcc_lo
	s_nop 0
	global_load_lds_dwordx4 v[208:209], off
	s_waitcnt vmcnt(8)
	s_waitcnt lgkmcnt(0)
	s_barrier
	s_setprio 1
	v_mfma_f32_16x16x32_bf16 v[126:129], v[140:143], v[172:175], v[126:129]
	v_mfma_f32_16x16x32_bf16 v[122:125], v[148:151], v[172:175], v[122:125]
	v_mfma_f32_16x16x32_bf16 v[118:121], v[140:143], v[180:183], v[118:121]
	v_mfma_f32_16x16x32_bf16 v[114:117], v[148:151], v[180:183], v[114:117]
	v_mfma_f32_16x16x32_bf16 v[102:105], v[140:143], v[188:191], v[102:105]
	v_mfma_f32_16x16x32_bf16 v[98:101], v[148:151], v[188:191], v[98:101]
	v_mfma_f32_16x16x32_bf16 v[86:89], v[140:143], v[200:203], v[86:89]
	v_mfma_f32_16x16x32_bf16 v[82:85], v[148:151], v[200:203], v[82:85]
	v_mfma_f32_16x16x32_bf16 v[126:129], v[144:147], v[176:179], v[126:129]
	v_mfma_f32_16x16x32_bf16 v[122:125], v[152:155], v[176:179], v[122:125]
	v_mfma_f32_16x16x32_bf16 v[118:121], v[144:147], v[184:187], v[118:121]
	v_mfma_f32_16x16x32_bf16 v[114:117], v[152:155], v[184:187], v[114:117]
	v_mfma_f32_16x16x32_bf16 v[102:105], v[144:147], v[192:195], v[102:105]
	v_mfma_f32_16x16x32_bf16 v[98:101], v[152:155], v[192:195], v[98:101]
	v_mfma_f32_16x16x32_bf16 v[86:89], v[144:147], v[204:207], v[86:89]
	v_mfma_f32_16x16x32_bf16 v[82:85], v[152:155], v[204:207], v[82:85]
	v_mfma_f32_16x16x32_bf16 v[110:113], v[156:159], v[172:175], v[110:113]
	v_mfma_f32_16x16x32_bf16 v[106:109], v[164:167], v[172:175], v[106:109]
	v_mfma_f32_16x16x32_bf16 v[94:97], v[156:159], v[180:183], v[94:97]
	v_mfma_f32_16x16x32_bf16 v[90:93], v[164:167], v[180:183], v[90:93]
	v_mfma_f32_16x16x32_bf16 v[78:81], v[156:159], v[188:191], v[78:81]
	v_mfma_f32_16x16x32_bf16 v[74:77], v[164:167], v[188:191], v[74:77]
	v_mfma_f32_16x16x32_bf16 v[70:73], v[156:159], v[200:203], v[70:73]
	v_mfma_f32_16x16x32_bf16 v[66:69], v[164:167], v[200:203], v[66:69]
	v_mfma_f32_16x16x32_bf16 v[110:113], v[160:163], v[176:179], v[110:113]
	v_mfma_f32_16x16x32_bf16 v[106:109], v[168:171], v[176:179], v[106:109]
	v_mfma_f32_16x16x32_bf16 v[94:97], v[160:163], v[184:187], v[94:97]
	v_mfma_f32_16x16x32_bf16 v[90:93], v[168:171], v[184:187], v[90:93]
	v_mfma_f32_16x16x32_bf16 v[78:81], v[160:163], v[192:195], v[78:81]
	v_mfma_f32_16x16x32_bf16 v[74:77], v[168:171], v[192:195], v[74:77]
	v_mfma_f32_16x16x32_bf16 v[70:73], v[160:163], v[204:207], v[70:73]
	v_mfma_f32_16x16x32_bf16 v[66:69], v[168:171], v[204:207], v[66:69]
	s_setprio 0
	s_barrier
	s_mov_b32 m0, s64
	v_lshl_add_u64 v[208:209], s[56:57], 0, v[134:135]
	ds_read_b128 v[172:175], v138 offset:16384
	ds_read_b128 v[176:179], v138 offset:17408
	ds_read_b128 v[180:183], v138 offset:18432
	ds_read_b128 v[184:187], v138 offset:19456
	ds_read_b128 v[188:191], v138 offset:20480
	ds_read_b128 v[192:195], v138 offset:21504
	ds_read_b128 v[200:203], v138 offset:22528
	ds_read_b128 v[204:207], v138 offset:23552
	global_load_lds_dwordx4 v[208:209], off
	v_lshl_add_u64 v[210:211], s[56:57], 0, v[130:131]
	s_mov_b32 m0, s65
	v_lshl_add_u64 v[212:213], s[58:59], 0, v[134:135]
	global_load_lds_dwordx4 v[210:211], off
	s_mov_b32 m0, s66
	v_lshl_add_u64 v[214:215], s[54:55], 0, v[132:133]
	global_load_lds_dwordx4 v[212:213], off
	v_lshl_add_u64 v[212:213], s[58:59], 0, v[130:131]
	s_mov_b32 m0, s67
	s_nop 0
	global_load_lds_dwordx4 v[212:213], off
	v_lshl_add_u64 v[212:213], s[54:55], 0, v[136:137]
	s_mov_b32 m0, s63
	s_nop 0
	global_load_lds_dwordx4 v[212:213], off
	s_mov_b32 m0, s80
	s_nop 0
	global_load_lds_dwordx4 v[214:215], off
	s_waitcnt vmcnt(8)
	s_waitcnt lgkmcnt(0)
	s_barrier
	s_setprio 1
	v_mfma_f32_16x16x32_bf16 v[62:65], v[140:143], v[172:175], v[62:65]
	v_mfma_f32_16x16x32_bf16 v[58:61], v[148:151], v[172:175], v[58:61]
	v_mfma_f32_16x16x32_bf16 v[54:57], v[140:143], v[180:183], v[54:57]
	v_mfma_f32_16x16x32_bf16 v[50:53], v[148:151], v[180:183], v[50:53]
	v_mfma_f32_16x16x32_bf16 v[38:41], v[140:143], v[188:191], v[38:41]
	v_mfma_f32_16x16x32_bf16 v[34:37], v[148:151], v[188:191], v[34:37]
	v_mfma_f32_16x16x32_bf16 v[22:25], v[140:143], v[200:203], v[22:25]
	v_mfma_f32_16x16x32_bf16 v[18:21], v[148:151], v[200:203], v[18:21]
	v_mfma_f32_16x16x32_bf16 v[62:65], v[144:147], v[176:179], v[62:65]
	v_mfma_f32_16x16x32_bf16 v[58:61], v[152:155], v[176:179], v[58:61]
	v_mfma_f32_16x16x32_bf16 v[54:57], v[144:147], v[184:187], v[54:57]
	v_mfma_f32_16x16x32_bf16 v[50:53], v[152:155], v[184:187], v[50:53]
	v_mfma_f32_16x16x32_bf16 v[38:41], v[144:147], v[192:195], v[38:41]
	v_mfma_f32_16x16x32_bf16 v[34:37], v[152:155], v[192:195], v[34:37]
	v_mfma_f32_16x16x32_bf16 v[22:25], v[144:147], v[204:207], v[22:25]
	v_mfma_f32_16x16x32_bf16 v[18:21], v[152:155], v[204:207], v[18:21]
	v_mfma_f32_16x16x32_bf16 v[46:49], v[156:159], v[172:175], v[46:49]
	v_mfma_f32_16x16x32_bf16 v[42:45], v[164:167], v[172:175], v[42:45]
	v_mfma_f32_16x16x32_bf16 v[30:33], v[156:159], v[180:183], v[30:33]
	v_mfma_f32_16x16x32_bf16 v[26:29], v[164:167], v[180:183], v[26:29]
	v_mfma_f32_16x16x32_bf16 v[14:17], v[156:159], v[188:191], v[14:17]
	v_mfma_f32_16x16x32_bf16 v[10:13], v[164:167], v[188:191], v[10:13]
	v_mfma_f32_16x16x32_bf16 v[6:9], v[156:159], v[200:203], v[6:9]
	v_mfma_f32_16x16x32_bf16 v[2:5], v[164:167], v[200:203], v[2:5]
	v_mfma_f32_16x16x32_bf16 v[46:49], v[160:163], v[176:179], v[46:49]
	v_mfma_f32_16x16x32_bf16 v[42:45], v[168:171], v[176:179], v[42:45]
	v_mfma_f32_16x16x32_bf16 v[30:33], v[160:163], v[184:187], v[30:33]
	v_mfma_f32_16x16x32_bf16 v[26:29], v[168:171], v[184:187], v[26:29]
	v_mfma_f32_16x16x32_bf16 v[14:17], v[160:163], v[192:195], v[14:17]
	v_mfma_f32_16x16x32_bf16 v[10:13], v[168:171], v[192:195], v[10:13]
	v_mfma_f32_16x16x32_bf16 v[6:9], v[160:163], v[204:207], v[6:9]
	v_mfma_f32_16x16x32_bf16 v[2:5], v[168:171], v[204:207], v[2:5]
	s_setprio 0
	s_barrier
	v_or_b32_e32 v0, 0x18000, v139
	v_add_u32_e32 v144, 0x18400, v139
	ds_read_b128 v[140:143], v0
	ds_read_b128 v[144:147], v144
	v_add_u32_e32 v0, 0x18800, v139
	v_add_u32_e32 v152, 0x18c00, v139
	ds_read_b128 v[148:151], v0
	ds_read_b128 v[152:155], v152
	v_or_b32_e32 v0, 0x1c000, v139
	v_add_u32_e32 v160, 0x1c400, v139
	ds_read_b128 v[156:159], v0
	ds_read_b128 v[160:163], v160
	v_add_u32_e32 v0, 0x1c800, v139
	v_add_u32_e32 v168, 0x1cc00, v139
	ds_read_b128 v[164:167], v0
	ds_read_b128 v[168:171], v168
	s_mov_b32 m0, s82
	v_lshl_add_u64 v[216:217], s[52:53], 0, v[136:137]
	ds_read_b128 v[172:175], v138 offset:32768
	ds_read_b128 v[176:179], v138 offset:33792
	ds_read_b128 v[180:183], v138 offset:34816
	ds_read_b128 v[184:187], v138 offset:35840
	ds_read_b128 v[188:191], v138 offset:36864
	ds_read_b128 v[192:195], v138 offset:37888
	ds_read_b128 v[200:203], v138 offset:38912
	ds_read_b128 v[204:207], v138 offset:39936
	global_load_lds_dwordx4 v[216:217], off
	v_lshl_add_u64 v[216:217], s[52:53], 0, v[132:133]
	s_mov_b32 m0, s83
	s_nop 0
	global_load_lds_dwordx4 v[216:217], off
	s_waitcnt vmcnt(8)
	s_waitcnt lgkmcnt(0)
	s_barrier
	s_setprio 1
	v_mfma_f32_16x16x32_bf16 v[126:129], v[140:143], v[172:175], v[126:129]
	v_mfma_f32_16x16x32_bf16 v[122:125], v[148:151], v[172:175], v[122:125]
	v_mfma_f32_16x16x32_bf16 v[118:121], v[140:143], v[180:183], v[118:121]
	v_mfma_f32_16x16x32_bf16 v[114:117], v[148:151], v[180:183], v[114:117]
	v_mfma_f32_16x16x32_bf16 v[102:105], v[140:143], v[188:191], v[102:105]
	v_mfma_f32_16x16x32_bf16 v[98:101], v[148:151], v[188:191], v[98:101]
	v_mfma_f32_16x16x32_bf16 v[86:89], v[140:143], v[200:203], v[86:89]
	v_mfma_f32_16x16x32_bf16 v[82:85], v[148:151], v[200:203], v[82:85]
	v_mfma_f32_16x16x32_bf16 v[126:129], v[144:147], v[176:179], v[126:129]
	v_mfma_f32_16x16x32_bf16 v[122:125], v[152:155], v[176:179], v[122:125]
	v_mfma_f32_16x16x32_bf16 v[118:121], v[144:147], v[184:187], v[118:121]
	v_mfma_f32_16x16x32_bf16 v[114:117], v[152:155], v[184:187], v[114:117]
	v_mfma_f32_16x16x32_bf16 v[102:105], v[144:147], v[192:195], v[102:105]
	v_mfma_f32_16x16x32_bf16 v[98:101], v[152:155], v[192:195], v[98:101]
	v_mfma_f32_16x16x32_bf16 v[86:89], v[144:147], v[204:207], v[86:89]
	v_mfma_f32_16x16x32_bf16 v[82:85], v[152:155], v[204:207], v[82:85]
	v_mfma_f32_16x16x32_bf16 v[110:113], v[156:159], v[172:175], v[110:113]
	v_mfma_f32_16x16x32_bf16 v[106:109], v[164:167], v[172:175], v[106:109]
	v_mfma_f32_16x16x32_bf16 v[94:97], v[156:159], v[180:183], v[94:97]
	v_mfma_f32_16x16x32_bf16 v[90:93], v[164:167], v[180:183], v[90:93]
	v_mfma_f32_16x16x32_bf16 v[78:81], v[156:159], v[188:191], v[78:81]
	v_mfma_f32_16x16x32_bf16 v[74:77], v[164:167], v[188:191], v[74:77]
	v_mfma_f32_16x16x32_bf16 v[70:73], v[156:159], v[200:203], v[70:73]
	v_mfma_f32_16x16x32_bf16 v[66:69], v[164:167], v[200:203], v[66:69]
	v_mfma_f32_16x16x32_bf16 v[110:113], v[160:163], v[176:179], v[110:113]
	v_mfma_f32_16x16x32_bf16 v[106:109], v[168:171], v[176:179], v[106:109]
	v_mfma_f32_16x16x32_bf16 v[94:97], v[160:163], v[184:187], v[94:97]
	v_mfma_f32_16x16x32_bf16 v[90:93], v[168:171], v[184:187], v[90:93]
	v_mfma_f32_16x16x32_bf16 v[78:81], v[160:163], v[192:195], v[78:81]
	v_mfma_f32_16x16x32_bf16 v[74:77], v[168:171], v[192:195], v[74:77]
	v_mfma_f32_16x16x32_bf16 v[70:73], v[160:163], v[204:207], v[70:73]
	v_mfma_f32_16x16x32_bf16 v[66:69], v[168:171], v[204:207], v[66:69]
	s_setprio 0
	s_barrier
	s_mov_b32 m0, s85
	v_lshl_add_u64 v[208:209], v[208:209], 0, s[18:19]
	ds_read_b128 v[172:175], v138 offset:49152
	ds_read_b128 v[176:179], v138 offset:50176
	ds_read_b128 v[180:183], v138 offset:51200
	ds_read_b128 v[184:187], v138 offset:52224
	ds_read_b128 v[188:191], v138 offset:53248
	ds_read_b128 v[192:195], v138 offset:54272
	ds_read_b128 v[200:203], v138 offset:55296
	ds_read_b128 v[204:207], v138 offset:56320
	global_load_lds_dwordx4 v[208:209], off
	v_lshl_add_u64 v[208:209], v[210:211], 0, s[18:19]
	s_mov_b32 m0, s88
	s_nop 0
	global_load_lds_dwordx4 v[208:209], off
	v_lshl_add_u64 v[208:209], s[50:51], 0, v[134:135]
	s_mov_b32 m0, s91
	s_nop 0
	global_load_lds_dwordx4 v[208:209], off
	v_lshl_add_u64 v[208:209], s[50:51], 0, v[130:131]
	s_mov_b32 m0, s92
	s_nop 0
	global_load_lds_dwordx4 v[208:209], off
	v_lshl_add_u64 v[208:209], v[212:213], 0, s[18:19]
	s_mov_b32 m0, s89
	s_nop 0
	global_load_lds_dwordx4 v[208:209], off
	v_lshl_add_u64 v[208:209], v[214:215], 0, s[18:19]
	s_mov_b32 m0, s90
	s_nop 0
	global_load_lds_dwordx4 v[208:209], off
	s_waitcnt vmcnt(8)
	s_waitcnt lgkmcnt(0)
	s_barrier
	s_setprio 1
	v_mfma_f32_16x16x32_bf16 v[62:65], v[140:143], v[172:175], v[62:65]
	v_mfma_f32_16x16x32_bf16 v[58:61], v[148:151], v[172:175], v[58:61]
	v_mfma_f32_16x16x32_bf16 v[54:57], v[140:143], v[180:183], v[54:57]
	v_mfma_f32_16x16x32_bf16 v[50:53], v[148:151], v[180:183], v[50:53]
	v_mfma_f32_16x16x32_bf16 v[38:41], v[140:143], v[188:191], v[38:41]
	v_mfma_f32_16x16x32_bf16 v[34:37], v[148:151], v[188:191], v[34:37]
	v_mfma_f32_16x16x32_bf16 v[22:25], v[140:143], v[200:203], v[22:25]
	v_mfma_f32_16x16x32_bf16 v[18:21], v[148:151], v[200:203], v[18:21]
	v_mfma_f32_16x16x32_bf16 v[62:65], v[144:147], v[176:179], v[62:65]
	v_mfma_f32_16x16x32_bf16 v[58:61], v[152:155], v[176:179], v[58:61]
	v_mfma_f32_16x16x32_bf16 v[54:57], v[144:147], v[184:187], v[54:57]
	v_mfma_f32_16x16x32_bf16 v[50:53], v[152:155], v[184:187], v[50:53]
	v_mfma_f32_16x16x32_bf16 v[38:41], v[144:147], v[192:195], v[38:41]
	v_mfma_f32_16x16x32_bf16 v[34:37], v[152:155], v[192:195], v[34:37]
	v_mfma_f32_16x16x32_bf16 v[22:25], v[144:147], v[204:207], v[22:25]
	v_mfma_f32_16x16x32_bf16 v[18:21], v[152:155], v[204:207], v[18:21]
	v_mfma_f32_16x16x32_bf16 v[46:49], v[156:159], v[172:175], v[46:49]
	v_mfma_f32_16x16x32_bf16 v[42:45], v[164:167], v[172:175], v[42:45]
	v_mfma_f32_16x16x32_bf16 v[30:33], v[156:159], v[180:183], v[30:33]
	v_mfma_f32_16x16x32_bf16 v[26:29], v[164:167], v[180:183], v[26:29]
	v_mfma_f32_16x16x32_bf16 v[14:17], v[156:159], v[188:191], v[14:17]
	v_mfma_f32_16x16x32_bf16 v[10:13], v[164:167], v[188:191], v[10:13]
	v_mfma_f32_16x16x32_bf16 v[6:9], v[156:159], v[200:203], v[6:9]
	v_mfma_f32_16x16x32_bf16 v[2:5], v[164:167], v[200:203], v[2:5]
	v_mfma_f32_16x16x32_bf16 v[46:49], v[160:163], v[176:179], v[46:49]
	v_mfma_f32_16x16x32_bf16 v[42:45], v[168:171], v[176:179], v[42:45]
	v_mfma_f32_16x16x32_bf16 v[30:33], v[160:163], v[184:187], v[30:33]
	v_mfma_f32_16x16x32_bf16 v[26:29], v[168:171], v[184:187], v[26:29]
	v_mfma_f32_16x16x32_bf16 v[14:17], v[160:163], v[192:195], v[14:17]
	v_mfma_f32_16x16x32_bf16 v[10:13], v[168:171], v[192:195], v[10:13]
	v_mfma_f32_16x16x32_bf16 v[6:9], v[160:163], v[204:207], v[6:9]
	v_mfma_f32_16x16x32_bf16 v[2:5], v[168:171], v[204:207], v[2:5]
	s_setprio 0
	s_barrier
	s_andn2_b64 vcc, exec, s[48:49]
	s_mov_b64 s[50:51], -1
	s_mov_b64 s[48:49], 0
	s_mov_b64 s[52:53], 0x100
	s_cbranch_vccz .LBB0_1213
	s_and_b64 vcc, exec, s[14:15]
	s_cbranch_vccz .LBB0_1216
	s_barrier

.LBB0_2006:
	v_or_b32_e32 v0, 0x10000, v164
	v_add_u32_e32 v165, 0x10400, v164
	ds_read_b128 v[158:161], v0
	ds_read_b128 v[166:169], v165
	v_add_u32_e32 v0, 0x10800, v164
	v_add_u32_e32 v165, 0x10c00, v164
	ds_read_b128 v[170:173], v0
	ds_read_b128 v[174:177], v165
	v_or_b32_e32 v0, 0x14000, v164
	v_add_u32_e32 v165, 0x14400, v164
	ds_read_b128 v[178:181], v0
	ds_read_b128 v[182:185], v165
	v_add_u32_e32 v0, 0x14800, v164
	v_add_u32_e32 v165, 0x14c00, v164
	ds_read_b128 v[186:189], v0
	ds_read_b128 v[190:193], v165
	s_add_u32 s40, s36, 0xfffc0080
	s_addc_u32 s41, s37, -1
	s_cmp_eq_u32 vcc_lo, 12
	s_cselect_b32 s63, s29, s41
	s_cselect_b32 s62, s47, s40
	s_cselect_b32 s61, s49, s95
	s_cselect_b32 s60, s59, s80
	v_lshl_add_u64 v[194:195], s[36:37], 0, v[138:139]
	s_add_i32 m0, s31, 0xc000
	ds_read_b128 v[200:203], v163
	ds_read_b128 v[204:207], v163 offset:1024
	ds_read_b128 v[208:211], v163 offset:2048
	ds_read_b128 v[212:215], v163 offset:3072
	ds_read_b128 v[216:219], v163 offset:4096
	ds_read_b128 v[220:223], v163 offset:5120
	ds_read_b128 v[236:239], v163 offset:6144
	ds_read_b128 v[240:243], v163 offset:7168
	global_load_lds_dwordx4 v[194:195], off
	v_lshl_add_u64 v[194:195], s[36:37], 0, v[140:141]
	s_add_i32 m0, s31, 0xe000
	s_nop 0
	global_load_lds_dwordx4 v[194:195], off
	s_waitcnt vmcnt(8)
	s_waitcnt lgkmcnt(0)
	s_barrier
	s_setprio 1
	v_mfma_f32_16x16x32_bf16 v[126:129], v[158:161], v[200:203], v[126:129]
	v_mfma_f32_16x16x32_bf16 v[122:125], v[170:173], v[200:203], v[122:125]
	v_mfma_f32_16x16x32_bf16 v[114:117], v[158:161], v[208:211], v[114:117]
	v_mfma_f32_16x16x32_bf16 v[106:109], v[170:173], v[208:211], v[106:109]
	v_mfma_f32_16x16x32_bf16 v[98:101], v[158:161], v[216:219], v[98:101]
	v_mfma_f32_16x16x32_bf16 v[90:93], v[170:173], v[216:219], v[90:93]
	v_mfma_f32_16x16x32_bf16 v[82:85], v[158:161], v[236:239], v[82:85]
	v_mfma_f32_16x16x32_bf16 v[74:77], v[170:173], v[236:239], v[74:77]
	v_mfma_f32_16x16x32_bf16 v[126:129], v[166:169], v[204:207], v[126:129]
	v_mfma_f32_16x16x32_bf16 v[122:125], v[174:177], v[204:207], v[122:125]
	v_mfma_f32_16x16x32_bf16 v[114:117], v[166:169], v[212:215], v[114:117]
	v_mfma_f32_16x16x32_bf16 v[106:109], v[174:177], v[212:215], v[106:109]
	v_mfma_f32_16x16x32_bf16 v[98:101], v[166:169], v[220:223], v[98:101]
	v_mfma_f32_16x16x32_bf16 v[90:93], v[174:177], v[220:223], v[90:93]
	v_mfma_f32_16x16x32_bf16 v[82:85], v[166:169], v[240:243], v[82:85]
	v_mfma_f32_16x16x32_bf16 v[74:77], v[174:177], v[240:243], v[74:77]
	v_mfma_f32_16x16x32_bf16 v[118:121], v[178:181], v[200:203], v[118:121]
	v_mfma_f32_16x16x32_bf16 v[110:113], v[186:189], v[200:203], v[110:113]
	v_mfma_f32_16x16x32_bf16 v[102:105], v[178:181], v[208:211], v[102:105]
	v_mfma_f32_16x16x32_bf16 v[94:97], v[186:189], v[208:211], v[94:97]
	v_mfma_f32_16x16x32_bf16 v[86:89], v[178:181], v[216:219], v[86:89]
	v_mfma_f32_16x16x32_bf16 v[78:81], v[186:189], v[216:219], v[78:81]
	v_mfma_f32_16x16x32_bf16 v[70:73], v[178:181], v[236:239], v[70:73]
	v_mfma_f32_16x16x32_bf16 v[66:69], v[186:189], v[236:239], v[66:69]
	v_mfma_f32_16x16x32_bf16 v[118:121], v[182:185], v[204:207], v[118:121]
	v_mfma_f32_16x16x32_bf16 v[110:113], v[190:193], v[204:207], v[110:113]
	v_mfma_f32_16x16x32_bf16 v[102:105], v[182:185], v[212:215], v[102:105]
	v_mfma_f32_16x16x32_bf16 v[94:97], v[190:193], v[212:215], v[94:97]
	v_mfma_f32_16x16x32_bf16 v[86:89], v[182:185], v[220:223], v[86:89]
	v_mfma_f32_16x16x32_bf16 v[78:81], v[190:193], v[220:223], v[78:81]
	v_mfma_f32_16x16x32_bf16 v[70:73], v[182:185], v[240:243], v[70:73]
	v_mfma_f32_16x16x32_bf16 v[66:69], v[190:193], v[240:243], v[66:69]
	s_setprio 0
	s_barrier
	s_mov_b32 m0, s51
	v_lshl_add_u64 v[194:195], s[60:61], 0, v[132:133]
	s_add_u32 s40, s60, 0x40000
	ds_read_b128 v[200:203], v163 offset:16384
	ds_read_b128 v[204:207], v163 offset:17408
	ds_read_b128 v[208:211], v163 offset:18432
	ds_read_b128 v[212:215], v163 offset:19456
	ds_read_b128 v[216:219], v163 offset:20480
	ds_read_b128 v[220:223], v163 offset:21504
	ds_read_b128 v[236:239], v163 offset:22528
	ds_read_b128 v[240:243], v163 offset:23552
	global_load_lds_dwordx4 v[194:195], off
	v_lshl_add_u64 v[226:227], s[60:61], 0, v[136:137]
	s_mov_b32 m0, s65
	s_addc_u32 s41, s61, 0
	global_load_lds_dwordx4 v[226:227], off
	v_lshl_add_u64 v[244:245], s[40:41], 0, v[132:133]
	s_mov_b32 m0, s66
	v_lshl_add_u64 v[246:247], s[62:63], 0, v[134:135]
	global_load_lds_dwordx4 v[244:245], off
	v_lshl_add_u64 v[244:245], s[40:41], 0, v[136:137]
	s_mov_b32 m0, s67
	s_nop 0
	global_load_lds_dwordx4 v[244:245], off
	v_lshl_add_u64 v[244:245], s[62:63], 0, v[130:131]
	s_mov_b32 m0, s31
	s_nop 0
	global_load_lds_dwordx4 v[244:245], off
	s_mov_b32 m0, s82
	s_nop 0
	global_load_lds_dwordx4 v[246:247], off
	s_waitcnt vmcnt(8)
	s_waitcnt lgkmcnt(0)
	s_barrier
	s_setprio 1
	v_mfma_f32_16x16x32_bf16 v[62:65], v[158:161], v[200:203], v[62:65]
	v_mfma_f32_16x16x32_bf16 v[58:61], v[170:173], v[200:203], v[58:61]
	v_mfma_f32_16x16x32_bf16 v[54:57], v[158:161], v[208:211], v[54:57]
	v_mfma_f32_16x16x32_bf16 v[46:49], v[170:173], v[208:211], v[46:49]
	v_mfma_f32_16x16x32_bf16 v[38:41], v[158:161], v[216:219], v[38:41]
	v_mfma_f32_16x16x32_bf16 v[30:33], v[170:173], v[216:219], v[30:33]
	v_mfma_f32_16x16x32_bf16 v[22:25], v[158:161], v[236:239], v[22:25]
	v_mfma_f32_16x16x32_bf16 v[14:17], v[170:173], v[236:239], v[14:17]
	v_mfma_f32_16x16x32_bf16 v[62:65], v[166:169], v[204:207], v[62:65]
	v_mfma_f32_16x16x32_bf16 v[58:61], v[174:177], v[204:207], v[58:61]
	v_mfma_f32_16x16x32_bf16 v[54:57], v[166:169], v[212:215], v[54:57]
	v_mfma_f32_16x16x32_bf16 v[46:49], v[174:177], v[212:215], v[46:49]
	v_mfma_f32_16x16x32_bf16 v[38:41], v[166:169], v[220:223], v[38:41]
	v_mfma_f32_16x16x32_bf16 v[30:33], v[174:177], v[220:223], v[30:33]
	v_mfma_f32_16x16x32_bf16 v[22:25], v[166:169], v[240:243], v[22:25]
	v_mfma_f32_16x16x32_bf16 v[14:17], v[174:177], v[240:243], v[14:17]
	v_mfma_f32_16x16x32_bf16 v[50:53], v[178:181], v[200:203], v[50:53]
	v_mfma_f32_16x16x32_bf16 v[42:45], v[186:189], v[200:203], v[42:45]
	v_mfma_f32_16x16x32_bf16 v[34:37], v[178:181], v[208:211], v[34:37]
	v_mfma_f32_16x16x32_bf16 v[26:29], v[186:189], v[208:211], v[26:29]
	v_mfma_f32_16x16x32_bf16 v[18:21], v[178:181], v[216:219], v[18:21]
	v_mfma_f32_16x16x32_bf16 v[10:13], v[186:189], v[216:219], v[10:13]
	v_mfma_f32_16x16x32_bf16 v[6:9], v[178:181], v[236:239], v[6:9]
	v_mfma_f32_16x16x32_bf16 v[2:5], v[186:189], v[236:239], v[2:5]
	v_mfma_f32_16x16x32_bf16 v[50:53], v[182:185], v[204:207], v[50:53]
	v_mfma_f32_16x16x32_bf16 v[42:45], v[190:193], v[204:207], v[42:45]
	v_mfma_f32_16x16x32_bf16 v[34:37], v[182:185], v[212:215], v[34:37]
	v_mfma_f32_16x16x32_bf16 v[26:29], v[190:193], v[212:215], v[26:29]
	v_mfma_f32_16x16x32_bf16 v[18:21], v[182:185], v[220:223], v[18:21]
	v_mfma_f32_16x16x32_bf16 v[10:13], v[190:193], v[220:223], v[10:13]
	v_mfma_f32_16x16x32_bf16 v[6:9], v[182:185], v[240:243], v[6:9]
	v_mfma_f32_16x16x32_bf16 v[2:5], v[190:193], v[240:243], v[2:5]
	s_setprio 0
	s_barrier
	v_or_b32_e32 v0, 0x18000, v164
	v_add_u32_e32 v165, 0x18400, v164
	ds_read_b128 v[158:161], v0
	ds_read_b128 v[166:169], v165
	v_add_u32_e32 v0, 0x18800, v164
	v_add_u32_e32 v165, 0x18c00, v164
	ds_read_b128 v[170:173], v0
	ds_read_b128 v[174:177], v165
	v_or_b32_e32 v0, 0x1c000, v164
	v_add_u32_e32 v165, 0x1c400, v164
	ds_read_b128 v[178:181], v0
	ds_read_b128 v[182:185], v165
	v_add_u32_e32 v0, 0x1c800, v164
	v_add_u32_e32 v165, 0x1cc00, v164
	ds_read_b128 v[186:189], v0
	ds_read_b128 v[190:193], v165
	s_add_u32 s40, s62, 0x40000
	s_addc_u32 s41, s63, 0
	s_mov_b32 m0, s83
	v_lshl_add_u64 v[248:249], s[40:41], 0, v[130:131]
	ds_read_b128 v[200:203], v163 offset:32768
	ds_read_b128 v[204:207], v163 offset:33792
	ds_read_b128 v[208:211], v163 offset:34816
	ds_read_b128 v[212:215], v163 offset:35840
	ds_read_b128 v[216:219], v163 offset:36864
	ds_read_b128 v[220:223], v163 offset:37888
	ds_read_b128 v[236:239], v163 offset:38912
	ds_read_b128 v[240:243], v163 offset:39936
	global_load_lds_dwordx4 v[248:249], off
	v_lshl_add_u64 v[248:249], s[40:41], 0, v[134:135]
	s_mov_b32 m0, s84
	s_nop 0
	global_load_lds_dwordx4 v[248:249], off
	s_waitcnt vmcnt(8)
	s_waitcnt lgkmcnt(0)
	s_barrier
	s_setprio 1
	v_mfma_f32_16x16x32_bf16 v[126:129], v[158:161], v[200:203], v[126:129]
	v_mfma_f32_16x16x32_bf16 v[122:125], v[170:173], v[200:203], v[122:125]
	v_mfma_f32_16x16x32_bf16 v[114:117], v[158:161], v[208:211], v[114:117]
	v_mfma_f32_16x16x32_bf16 v[106:109], v[170:173], v[208:211], v[106:109]
	v_mfma_f32_16x16x32_bf16 v[98:101], v[158:161], v[216:219], v[98:101]
	v_mfma_f32_16x16x32_bf16 v[90:93], v[170:173], v[216:219], v[90:93]
	v_mfma_f32_16x16x32_bf16 v[82:85], v[158:161], v[236:239], v[82:85]
	v_mfma_f32_16x16x32_bf16 v[74:77], v[170:173], v[236:239], v[74:77]
	v_mfma_f32_16x16x32_bf16 v[126:129], v[166:169], v[204:207], v[126:129]
	v_mfma_f32_16x16x32_bf16 v[122:125], v[174:177], v[204:207], v[122:125]
	v_mfma_f32_16x16x32_bf16 v[114:117], v[166:169], v[212:215], v[114:117]
	v_mfma_f32_16x16x32_bf16 v[106:109], v[174:177], v[212:215], v[106:109]
	v_mfma_f32_16x16x32_bf16 v[98:101], v[166:169], v[220:223], v[98:101]
	v_mfma_f32_16x16x32_bf16 v[90:93], v[174:177], v[220:223], v[90:93]
	v_mfma_f32_16x16x32_bf16 v[82:85], v[166:169], v[240:243], v[82:85]
	v_mfma_f32_16x16x32_bf16 v[74:77], v[174:177], v[240:243], v[74:77]
	v_mfma_f32_16x16x32_bf16 v[118:121], v[178:181], v[200:203], v[118:121]
	v_mfma_f32_16x16x32_bf16 v[110:113], v[186:189], v[200:203], v[110:113]
	v_mfma_f32_16x16x32_bf16 v[102:105], v[178:181], v[208:211], v[102:105]
	v_mfma_f32_16x16x32_bf16 v[94:97], v[186:189], v[208:211], v[94:97]
	v_mfma_f32_16x16x32_bf16 v[86:89], v[178:181], v[216:219], v[86:89]
	v_mfma_f32_16x16x32_bf16 v[78:81], v[186:189], v[216:219], v[78:81]
	v_mfma_f32_16x16x32_bf16 v[70:73], v[178:181], v[236:239], v[70:73]
	v_mfma_f32_16x16x32_bf16 v[66:69], v[186:189], v[236:239], v[66:69]
	v_mfma_f32_16x16x32_bf16 v[118:121], v[182:185], v[204:207], v[118:121]
	v_mfma_f32_16x16x32_bf16 v[110:113], v[190:193], v[204:207], v[110:113]
	v_mfma_f32_16x16x32_bf16 v[102:105], v[182:185], v[212:215], v[102:105]
	v_mfma_f32_16x16x32_bf16 v[94:97], v[190:193], v[212:215], v[94:97]
	v_mfma_f32_16x16x32_bf16 v[86:89], v[182:185], v[220:223], v[86:89]
	v_mfma_f32_16x16x32_bf16 v[78:81], v[190:193], v[220:223], v[78:81]
	v_mfma_f32_16x16x32_bf16 v[70:73], v[182:185], v[240:243], v[70:73]
	v_mfma_f32_16x16x32_bf16 v[66:69], v[190:193], v[240:243], v[66:69]
	s_setprio 0
	s_barrier
	s_mov_b32 m0, s88
	v_lshl_add_u64 v[194:195], v[194:195], 0, s[18:19]
	s_add_u32 s40, s60, 0x40080
	ds_read_b128 v[200:203], v163 offset:49152
	ds_read_b128 v[204:207], v163 offset:50176
	ds_read_b128 v[208:211], v163 offset:51200
	ds_read_b128 v[212:215], v163 offset:52224
	ds_read_b128 v[216:219], v163 offset:53248
	ds_read_b128 v[220:223], v163 offset:54272
	ds_read_b128 v[236:239], v163 offset:55296
	ds_read_b128 v[240:243], v163 offset:56320
	global_load_lds_dwordx4 v[194:195], off
	v_lshl_add_u64 v[194:195], v[226:227], 0, s[18:19]
	s_mov_b32 m0, s89
	s_addc_u32 s41, s61, 0
	global_load_lds_dwordx4 v[194:195], off
	v_lshl_add_u64 v[194:195], s[40:41], 0, v[132:133]
	s_mov_b32 m0, s92
	s_nop 0
	global_load_lds_dwordx4 v[194:195], off
	v_lshl_add_u64 v[194:195], s[40:41], 0, v[136:137]
	s_mov_b32 m0, s93
	s_nop 0
	global_load_lds_dwordx4 v[194:195], off
	v_lshl_add_u64 v[194:195], v[244:245], 0, s[18:19]
	s_mov_b32 m0, s90
	s_nop 0
	global_load_lds_dwordx4 v[194:195], off
	v_lshl_add_u64 v[194:195], v[246:247], 0, s[18:19]
	s_mov_b32 m0, s91
	s_nop 0
	global_load_lds_dwordx4 v[194:195], off
	s_waitcnt vmcnt(8)
	s_waitcnt lgkmcnt(0)
	s_barrier
	s_setprio 1
	v_mfma_f32_16x16x32_bf16 v[62:65], v[158:161], v[200:203], v[62:65]
	v_mfma_f32_16x16x32_bf16 v[58:61], v[170:173], v[200:203], v[58:61]
	v_mfma_f32_16x16x32_bf16 v[54:57], v[158:161], v[208:211], v[54:57]
	v_mfma_f32_16x16x32_bf16 v[46:49], v[170:173], v[208:211], v[46:49]
	v_mfma_f32_16x16x32_bf16 v[38:41], v[158:161], v[216:219], v[38:41]
	v_mfma_f32_16x16x32_bf16 v[30:33], v[170:173], v[216:219], v[30:33]
	v_mfma_f32_16x16x32_bf16 v[22:25], v[158:161], v[236:239], v[22:25]
	v_mfma_f32_16x16x32_bf16 v[14:17], v[170:173], v[236:239], v[14:17]
	v_mfma_f32_16x16x32_bf16 v[62:65], v[166:169], v[204:207], v[62:65]
	v_mfma_f32_16x16x32_bf16 v[58:61], v[174:177], v[204:207], v[58:61]
	v_mfma_f32_16x16x32_bf16 v[54:57], v[166:169], v[212:215], v[54:57]
	v_mfma_f32_16x16x32_bf16 v[46:49], v[174:177], v[212:215], v[46:49]
	v_mfma_f32_16x16x32_bf16 v[38:41], v[166:169], v[220:223], v[38:41]
	v_mfma_f32_16x16x32_bf16 v[30:33], v[174:177], v[220:223], v[30:33]
	v_mfma_f32_16x16x32_bf16 v[22:25], v[166:169], v[240:243], v[22:25]
	v_mfma_f32_16x16x32_bf16 v[14:17], v[174:177], v[240:243], v[14:17]
	v_mfma_f32_16x16x32_bf16 v[50:53], v[178:181], v[200:203], v[50:53]
	v_mfma_f32_16x16x32_bf16 v[42:45], v[186:189], v[200:203], v[42:45]
	v_mfma_f32_16x16x32_bf16 v[34:37], v[178:181], v[208:211], v[34:37]
	v_mfma_f32_16x16x32_bf16 v[26:29], v[186:189], v[208:211], v[26:29]
	v_mfma_f32_16x16x32_bf16 v[18:21], v[178:181], v[216:219], v[18:21]
	v_mfma_f32_16x16x32_bf16 v[10:13], v[186:189], v[216:219], v[10:13]
	v_mfma_f32_16x16x32_bf16 v[6:9], v[178:181], v[236:239], v[6:9]
	v_mfma_f32_16x16x32_bf16 v[2:5], v[186:189], v[236:239], v[2:5]
	v_mfma_f32_16x16x32_bf16 v[50:53], v[182:185], v[204:207], v[50:53]
	v_mfma_f32_16x16x32_bf16 v[42:45], v[190:193], v[204:207], v[42:45]
	v_mfma_f32_16x16x32_bf16 v[34:37], v[182:185], v[212:215], v[34:37]
	v_mfma_f32_16x16x32_bf16 v[26:29], v[190:193], v[212:215], v[26:29]
	v_mfma_f32_16x16x32_bf16 v[18:21], v[182:185], v[220:223], v[18:21]
	v_mfma_f32_16x16x32_bf16 v[10:13], v[190:193], v[220:223], v[10:13]
	v_mfma_f32_16x16x32_bf16 v[6:9], v[182:185], v[240:243], v[6:9]
	v_mfma_f32_16x16x32_bf16 v[2:5], v[190:193], v[240:243], v[2:5]
	s_setprio 0
	s_barrier
	s_add_i32 vcc_lo, vcc_lo, 2
	s_add_u32 s36, s36, 0x100
	s_addc_u32 s37, s37, 0
	s_add_u32 s80, s80, 0x100
	s_addc_u32 s95, s95, 0
	s_cmp_gt_u32 vcc_lo, 13
	s_cbranch_scc0 .LBB0_2006
	s_and_b64 vcc, exec, s[16:17]
	s_cbranch_vccz .LBB0_2009
	s_barrier

.LBB0_2067:
	v_or_b32_e32 v0, 0x10000, v143
	v_add_u32_e32 v148, 0x10400, v143
	ds_read_b128 v[144:147], v0
	ds_read_b128 v[148:151], v148
	v_add_u32_e32 v0, 0x10800, v143
	v_add_u32_e32 v156, 0x10c00, v143
	ds_read_b128 v[152:155], v0
	ds_read_b128 v[156:159], v156
	v_or_b32_e32 v0, 0x14000, v143
	v_add_u32_e32 v164, 0x14400, v143
	ds_read_b128 v[160:163], v0
	ds_read_b128 v[164:167], v164
	v_add_u32_e32 v0, 0x14800, v143
	v_add_u32_e32 v172, 0x14c00, v143
	ds_read_b128 v[168:171], v0
	ds_read_b128 v[172:175], v172
	s_add_u32 s41, s52, 0xfffc0080
	s_addc_u32 s43, s53, -1
	s_cmp_eq_u32 s39, 12
	s_cselect_b32 s57, s47, s43
	s_cselect_b32 s56, s46, s41
	s_cselect_b32 s55, s49, s29
	s_cselect_b32 s54, s48, s17
	v_lshl_add_u64 v[212:213], s[52:53], 0, v[138:139]
	s_add_i32 m0, s59, 0xc000
	ds_read_b128 v[176:179], v142
	ds_read_b128 v[180:183], v142 offset:1024
	ds_read_b128 v[184:187], v142 offset:2048
	ds_read_b128 v[188:191], v142 offset:3072
	ds_read_b128 v[192:195], v142 offset:4096
	ds_read_b128 v[200:203], v142 offset:5120
	ds_read_b128 v[204:207], v142 offset:6144
	ds_read_b128 v[208:211], v142 offset:7168
	global_load_lds_dwordx4 v[212:213], off
	v_lshl_add_u64 v[212:213], s[52:53], 0, v[140:141]
	s_add_i32 m0, s59, 0xe000
	s_nop 0
	global_load_lds_dwordx4 v[212:213], off
	s_waitcnt vmcnt(8)
	s_waitcnt lgkmcnt(0)
	s_barrier
	s_setprio 1
	v_mfma_f32_16x16x32_bf16 v[126:129], v[144:147], v[176:179], v[126:129]
	v_mfma_f32_16x16x32_bf16 v[122:125], v[152:155], v[176:179], v[122:125]
	v_mfma_f32_16x16x32_bf16 v[118:121], v[144:147], v[184:187], v[118:121]
	v_mfma_f32_16x16x32_bf16 v[114:117], v[152:155], v[184:187], v[114:117]
	v_mfma_f32_16x16x32_bf16 v[102:105], v[144:147], v[192:195], v[102:105]
	v_mfma_f32_16x16x32_bf16 v[98:101], v[152:155], v[192:195], v[98:101]
	v_mfma_f32_16x16x32_bf16 v[86:89], v[144:147], v[204:207], v[86:89]
	v_mfma_f32_16x16x32_bf16 v[82:85], v[152:155], v[204:207], v[82:85]
	v_mfma_f32_16x16x32_bf16 v[126:129], v[148:151], v[180:183], v[126:129]
	v_mfma_f32_16x16x32_bf16 v[122:125], v[156:159], v[180:183], v[122:125]
	v_mfma_f32_16x16x32_bf16 v[118:121], v[148:151], v[188:191], v[118:121]
	v_mfma_f32_16x16x32_bf16 v[114:117], v[156:159], v[188:191], v[114:117]
	v_mfma_f32_16x16x32_bf16 v[102:105], v[148:151], v[200:203], v[102:105]
	v_mfma_f32_16x16x32_bf16 v[98:101], v[156:159], v[200:203], v[98:101]
	v_mfma_f32_16x16x32_bf16 v[86:89], v[148:151], v[208:211], v[86:89]
	v_mfma_f32_16x16x32_bf16 v[82:85], v[156:159], v[208:211], v[82:85]
	v_mfma_f32_16x16x32_bf16 v[110:113], v[160:163], v[176:179], v[110:113]
	v_mfma_f32_16x16x32_bf16 v[106:109], v[168:171], v[176:179], v[106:109]
	v_mfma_f32_16x16x32_bf16 v[94:97], v[160:163], v[184:187], v[94:97]
	v_mfma_f32_16x16x32_bf16 v[90:93], v[168:171], v[184:187], v[90:93]
	v_mfma_f32_16x16x32_bf16 v[78:81], v[160:163], v[192:195], v[78:81]
	v_mfma_f32_16x16x32_bf16 v[74:77], v[168:171], v[192:195], v[74:77]
	v_mfma_f32_16x16x32_bf16 v[70:73], v[160:163], v[204:207], v[70:73]
	v_mfma_f32_16x16x32_bf16 v[66:69], v[168:171], v[204:207], v[66:69]
	v_mfma_f32_16x16x32_bf16 v[110:113], v[164:167], v[180:183], v[110:113]
	v_mfma_f32_16x16x32_bf16 v[106:109], v[172:175], v[180:183], v[106:109]
	v_mfma_f32_16x16x32_bf16 v[94:97], v[164:167], v[188:191], v[94:97]
	v_mfma_f32_16x16x32_bf16 v[90:93], v[172:175], v[188:191], v[90:93]
	v_mfma_f32_16x16x32_bf16 v[78:81], v[164:167], v[200:203], v[78:81]
	v_mfma_f32_16x16x32_bf16 v[74:77], v[172:175], v[200:203], v[74:77]
	v_mfma_f32_16x16x32_bf16 v[70:73], v[164:167], v[208:211], v[70:73]
	v_mfma_f32_16x16x32_bf16 v[66:69], v[172:175], v[208:211], v[66:69]
	s_setprio 0
	s_barrier
	s_mov_b32 m0, s60
	v_lshl_add_u64 v[212:213], s[54:55], 0, v[132:133]
	s_add_u32 s94, s54, 0x40000
	ds_read_b128 v[176:179], v142 offset:16384
	ds_read_b128 v[180:183], v142 offset:17408
	ds_read_b128 v[184:187], v142 offset:18432
	ds_read_b128 v[188:191], v142 offset:19456
	ds_read_b128 v[192:195], v142 offset:20480
	ds_read_b128 v[200:203], v142 offset:21504
	ds_read_b128 v[204:207], v142 offset:22528
	ds_read_b128 v[208:211], v142 offset:23552
	global_load_lds_dwordx4 v[212:213], off
	v_lshl_add_u64 v[214:215], s[54:55], 0, v[136:137]
	s_mov_b32 m0, s61
	s_addc_u32 s95, s55, 0
	global_load_lds_dwordx4 v[214:215], off
	v_lshl_add_u64 v[216:217], s[94:95], 0, v[132:133]
	s_mov_b32 m0, s62
	v_lshl_add_u64 v[218:219], s[56:57], 0, v[134:135]
	global_load_lds_dwordx4 v[216:217], off
	v_lshl_add_u64 v[216:217], s[94:95], 0, v[136:137]
	s_mov_b32 m0, s63
	s_nop 0
	global_load_lds_dwordx4 v[216:217], off
	v_lshl_add_u64 v[216:217], s[56:57], 0, v[130:131]
	s_mov_b32 m0, s59
	s_nop 0
	global_load_lds_dwordx4 v[216:217], off
	s_mov_b32 m0, s64
	s_nop 0
	global_load_lds_dwordx4 v[218:219], off
	s_waitcnt vmcnt(8)
	s_waitcnt lgkmcnt(0)
	s_barrier
	s_setprio 1
	v_mfma_f32_16x16x32_bf16 v[62:65], v[144:147], v[176:179], v[62:65]
	v_mfma_f32_16x16x32_bf16 v[58:61], v[152:155], v[176:179], v[58:61]
	v_mfma_f32_16x16x32_bf16 v[54:57], v[144:147], v[184:187], v[54:57]
	v_mfma_f32_16x16x32_bf16 v[50:53], v[152:155], v[184:187], v[50:53]
	v_mfma_f32_16x16x32_bf16 v[38:41], v[144:147], v[192:195], v[38:41]
	v_mfma_f32_16x16x32_bf16 v[34:37], v[152:155], v[192:195], v[34:37]
	v_mfma_f32_16x16x32_bf16 v[22:25], v[144:147], v[204:207], v[22:25]
	v_mfma_f32_16x16x32_bf16 v[18:21], v[152:155], v[204:207], v[18:21]
	v_mfma_f32_16x16x32_bf16 v[62:65], v[148:151], v[180:183], v[62:65]
	v_mfma_f32_16x16x32_bf16 v[58:61], v[156:159], v[180:183], v[58:61]
	v_mfma_f32_16x16x32_bf16 v[54:57], v[148:151], v[188:191], v[54:57]
	v_mfma_f32_16x16x32_bf16 v[50:53], v[156:159], v[188:191], v[50:53]
	v_mfma_f32_16x16x32_bf16 v[38:41], v[148:151], v[200:203], v[38:41]
	v_mfma_f32_16x16x32_bf16 v[34:37], v[156:159], v[200:203], v[34:37]
	v_mfma_f32_16x16x32_bf16 v[22:25], v[148:151], v[208:211], v[22:25]
	v_mfma_f32_16x16x32_bf16 v[18:21], v[156:159], v[208:211], v[18:21]
	v_mfma_f32_16x16x32_bf16 v[46:49], v[160:163], v[176:179], v[46:49]
	v_mfma_f32_16x16x32_bf16 v[42:45], v[168:171], v[176:179], v[42:45]
	v_mfma_f32_16x16x32_bf16 v[30:33], v[160:163], v[184:187], v[30:33]
	v_mfma_f32_16x16x32_bf16 v[26:29], v[168:171], v[184:187], v[26:29]
	v_mfma_f32_16x16x32_bf16 v[14:17], v[160:163], v[192:195], v[14:17]
	v_mfma_f32_16x16x32_bf16 v[10:13], v[168:171], v[192:195], v[10:13]
	v_mfma_f32_16x16x32_bf16 v[6:9], v[160:163], v[204:207], v[6:9]
	v_mfma_f32_16x16x32_bf16 v[2:5], v[168:171], v[204:207], v[2:5]
	v_mfma_f32_16x16x32_bf16 v[46:49], v[164:167], v[180:183], v[46:49]
	v_mfma_f32_16x16x32_bf16 v[42:45], v[172:175], v[180:183], v[42:45]
	v_mfma_f32_16x16x32_bf16 v[30:33], v[164:167], v[188:191], v[30:33]
	v_mfma_f32_16x16x32_bf16 v[26:29], v[172:175], v[188:191], v[26:29]
	v_mfma_f32_16x16x32_bf16 v[14:17], v[164:167], v[200:203], v[14:17]
	v_mfma_f32_16x16x32_bf16 v[10:13], v[172:175], v[200:203], v[10:13]
	v_mfma_f32_16x16x32_bf16 v[6:9], v[164:167], v[208:211], v[6:9]
	v_mfma_f32_16x16x32_bf16 v[2:5], v[172:175], v[208:211], v[2:5]
	s_setprio 0
	s_barrier
	v_or_b32_e32 v0, 0x18000, v143
	v_add_u32_e32 v148, 0x18400, v143
	ds_read_b128 v[144:147], v0
	ds_read_b128 v[148:151], v148
	v_add_u32_e32 v0, 0x18800, v143
	v_add_u32_e32 v156, 0x18c00, v143
	ds_read_b128 v[152:155], v0
	ds_read_b128 v[156:159], v156
	v_or_b32_e32 v0, 0x1c000, v143
	v_add_u32_e32 v164, 0x1c400, v143
	ds_read_b128 v[160:163], v0
	ds_read_b128 v[164:167], v164
	v_add_u32_e32 v0, 0x1c800, v143
	v_add_u32_e32 v172, 0x1cc00, v143
	ds_read_b128 v[168:171], v0
	ds_read_b128 v[172:175], v172
	s_add_u32 s56, s56, 0x40000
	s_addc_u32 s57, s57, 0
	s_mov_b32 m0, s65
	v_lshl_add_u64 v[220:221], s[56:57], 0, v[130:131]
	ds_read_b128 v[176:179], v142 offset:32768
	ds_read_b128 v[180:183], v142 offset:33792
	ds_read_b128 v[184:187], v142 offset:34816
	ds_read_b128 v[188:191], v142 offset:35840
	ds_read_b128 v[192:195], v142 offset:36864
	ds_read_b128 v[200:203], v142 offset:37888
	ds_read_b128 v[204:207], v142 offset:38912
	ds_read_b128 v[208:211], v142 offset:39936
	global_load_lds_dwordx4 v[220:221], off
	v_lshl_add_u64 v[220:221], s[56:57], 0, v[134:135]
	s_mov_b32 m0, s66
	s_nop 0
	global_load_lds_dwordx4 v[220:221], off
	s_waitcnt vmcnt(8)
	s_waitcnt lgkmcnt(0)
	s_barrier
	s_setprio 1
	v_mfma_f32_16x16x32_bf16 v[126:129], v[144:147], v[176:179], v[126:129]
	v_mfma_f32_16x16x32_bf16 v[122:125], v[152:155], v[176:179], v[122:125]
	v_mfma_f32_16x16x32_bf16 v[118:121], v[144:147], v[184:187], v[118:121]
	v_mfma_f32_16x16x32_bf16 v[114:117], v[152:155], v[184:187], v[114:117]
	v_mfma_f32_16x16x32_bf16 v[102:105], v[144:147], v[192:195], v[102:105]
	v_mfma_f32_16x16x32_bf16 v[98:101], v[152:155], v[192:195], v[98:101]
	v_mfma_f32_16x16x32_bf16 v[86:89], v[144:147], v[204:207], v[86:89]
	v_mfma_f32_16x16x32_bf16 v[82:85], v[152:155], v[204:207], v[82:85]
	v_mfma_f32_16x16x32_bf16 v[126:129], v[148:151], v[180:183], v[126:129]
	v_mfma_f32_16x16x32_bf16 v[122:125], v[156:159], v[180:183], v[122:125]
	v_mfma_f32_16x16x32_bf16 v[118:121], v[148:151], v[188:191], v[118:121]
	v_mfma_f32_16x16x32_bf16 v[114:117], v[156:159], v[188:191], v[114:117]
	v_mfma_f32_16x16x32_bf16 v[102:105], v[148:151], v[200:203], v[102:105]
	v_mfma_f32_16x16x32_bf16 v[98:101], v[156:159], v[200:203], v[98:101]
	v_mfma_f32_16x16x32_bf16 v[86:89], v[148:151], v[208:211], v[86:89]
	v_mfma_f32_16x16x32_bf16 v[82:85], v[156:159], v[208:211], v[82:85]
	v_mfma_f32_16x16x32_bf16 v[110:113], v[160:163], v[176:179], v[110:113]
	v_mfma_f32_16x16x32_bf16 v[106:109], v[168:171], v[176:179], v[106:109]
	v_mfma_f32_16x16x32_bf16 v[94:97], v[160:163], v[184:187], v[94:97]
	v_mfma_f32_16x16x32_bf16 v[90:93], v[168:171], v[184:187], v[90:93]
	v_mfma_f32_16x16x32_bf16 v[78:81], v[160:163], v[192:195], v[78:81]
	v_mfma_f32_16x16x32_bf16 v[74:77], v[168:171], v[192:195], v[74:77]
	v_mfma_f32_16x16x32_bf16 v[70:73], v[160:163], v[204:207], v[70:73]
	v_mfma_f32_16x16x32_bf16 v[66:69], v[168:171], v[204:207], v[66:69]
	v_mfma_f32_16x16x32_bf16 v[110:113], v[164:167], v[180:183], v[110:113]
	v_mfma_f32_16x16x32_bf16 v[106:109], v[172:175], v[180:183], v[106:109]
	v_mfma_f32_16x16x32_bf16 v[94:97], v[164:167], v[188:191], v[94:97]
	v_mfma_f32_16x16x32_bf16 v[90:93], v[172:175], v[188:191], v[90:93]
	v_mfma_f32_16x16x32_bf16 v[78:81], v[164:167], v[200:203], v[78:81]
	v_mfma_f32_16x16x32_bf16 v[74:77], v[172:175], v[200:203], v[74:77]
	v_mfma_f32_16x16x32_bf16 v[70:73], v[164:167], v[208:211], v[70:73]
	v_mfma_f32_16x16x32_bf16 v[66:69], v[172:175], v[208:211], v[66:69]
	s_setprio 0
	s_barrier
	s_mov_b32 m0, s80
	v_lshl_add_u64 v[212:213], v[212:213], 0, s[18:19]
	s_add_u32 s54, s54, 0x40080
	ds_read_b128 v[176:179], v142 offset:49152
	ds_read_b128 v[180:183], v142 offset:50176
	ds_read_b128 v[184:187], v142 offset:51200
	ds_read_b128 v[188:191], v142 offset:52224
	ds_read_b128 v[192:195], v142 offset:53248
	ds_read_b128 v[200:203], v142 offset:54272
	ds_read_b128 v[204:207], v142 offset:55296
	ds_read_b128 v[208:211], v142 offset:56320
	global_load_lds_dwordx4 v[212:213], off
	v_lshl_add_u64 v[212:213], v[214:215], 0, s[18:19]
	s_mov_b32 m0, s82
	s_addc_u32 s55, s55, 0
	global_load_lds_dwordx4 v[212:213], off
	v_lshl_add_u64 v[212:213], s[54:55], 0, v[132:133]
	s_mov_b32 m0, s85
	s_nop 0
	global_load_lds_dwordx4 v[212:213], off
	v_lshl_add_u64 v[212:213], s[54:55], 0, v[136:137]
	s_mov_b32 m0, s88
	s_nop 0
	global_load_lds_dwordx4 v[212:213], off
	v_lshl_add_u64 v[212:213], v[216:217], 0, s[18:19]
	s_mov_b32 m0, s83
	s_nop 0
	global_load_lds_dwordx4 v[212:213], off
	v_lshl_add_u64 v[212:213], v[218:219], 0, s[18:19]
	s_mov_b32 m0, s84
	s_nop 0
	global_load_lds_dwordx4 v[212:213], off
	s_waitcnt vmcnt(8)
	s_waitcnt lgkmcnt(0)
	s_barrier
	s_setprio 1
	v_mfma_f32_16x16x32_bf16 v[62:65], v[144:147], v[176:179], v[62:65]
	v_mfma_f32_16x16x32_bf16 v[58:61], v[152:155], v[176:179], v[58:61]
	v_mfma_f32_16x16x32_bf16 v[54:57], v[144:147], v[184:187], v[54:57]
	v_mfma_f32_16x16x32_bf16 v[50:53], v[152:155], v[184:187], v[50:53]
	v_mfma_f32_16x16x32_bf16 v[38:41], v[144:147], v[192:195], v[38:41]
	v_mfma_f32_16x16x32_bf16 v[34:37], v[152:155], v[192:195], v[34:37]
	v_mfma_f32_16x16x32_bf16 v[22:25], v[144:147], v[204:207], v[22:25]
	v_mfma_f32_16x16x32_bf16 v[18:21], v[152:155], v[204:207], v[18:21]
	v_mfma_f32_16x16x32_bf16 v[62:65], v[148:151], v[180:183], v[62:65]
	v_mfma_f32_16x16x32_bf16 v[58:61], v[156:159], v[180:183], v[58:61]
	v_mfma_f32_16x16x32_bf16 v[54:57], v[148:151], v[188:191], v[54:57]
	v_mfma_f32_16x16x32_bf16 v[50:53], v[156:159], v[188:191], v[50:53]
	v_mfma_f32_16x16x32_bf16 v[38:41], v[148:151], v[200:203], v[38:41]
	v_mfma_f32_16x16x32_bf16 v[34:37], v[156:159], v[200:203], v[34:37]
	v_mfma_f32_16x16x32_bf16 v[22:25], v[148:151], v[208:211], v[22:25]
	v_mfma_f32_16x16x32_bf16 v[18:21], v[156:159], v[208:211], v[18:21]
	v_mfma_f32_16x16x32_bf16 v[46:49], v[160:163], v[176:179], v[46:49]
	v_mfma_f32_16x16x32_bf16 v[42:45], v[168:171], v[176:179], v[42:45]
	v_mfma_f32_16x16x32_bf16 v[30:33], v[160:163], v[184:187], v[30:33]
	v_mfma_f32_16x16x32_bf16 v[26:29], v[168:171], v[184:187], v[26:29]
	v_mfma_f32_16x16x32_bf16 v[14:17], v[160:163], v[192:195], v[14:17]
	v_mfma_f32_16x16x32_bf16 v[10:13], v[168:171], v[192:195], v[10:13]
	v_mfma_f32_16x16x32_bf16 v[6:9], v[160:163], v[204:207], v[6:9]
	v_mfma_f32_16x16x32_bf16 v[2:5], v[168:171], v[204:207], v[2:5]
	v_mfma_f32_16x16x32_bf16 v[46:49], v[164:167], v[180:183], v[46:49]
	v_mfma_f32_16x16x32_bf16 v[42:45], v[172:175], v[180:183], v[42:45]
	v_mfma_f32_16x16x32_bf16 v[30:33], v[164:167], v[188:191], v[30:33]
	v_mfma_f32_16x16x32_bf16 v[26:29], v[172:175], v[188:191], v[26:29]
	v_mfma_f32_16x16x32_bf16 v[14:17], v[164:167], v[200:203], v[14:17]
	v_mfma_f32_16x16x32_bf16 v[10:13], v[172:175], v[200:203], v[10:13]
	v_mfma_f32_16x16x32_bf16 v[6:9], v[164:167], v[208:211], v[6:9]
	v_mfma_f32_16x16x32_bf16 v[2:5], v[172:175], v[208:211], v[2:5]
	s_setprio 0
	s_barrier
	s_add_i32 s39, s39, 2
	s_add_u32 s52, s52, 0x100
	s_addc_u32 s53, s53, 0
	s_add_u32 s17, s17, 0x100
	s_addc_u32 s29, s29, 0
	s_cmp_gt_u32 s39, 13
	s_cbranch_scc0 .LBB0_2067
	s_and_b64 vcc, exec, s[14:15]
	s_cbranch_vccz .LBB0_2070
	s_barrier
